# static priority raise for waves 4-7 at kernel entry, per-cluster s_setprio flips deleted (7.4)
# baseline (speedup 1.0000x reference)
_Z10fwd_kernel4Args:
	v_readfirstlane_b32 s99, v0
	s_nop 3
	s_and_b32 s99, s99, 0x3ff
	s_lshr_b32 s99, s99, 6
	s_cmp_ge_u32 s99, 4
	s_cbranch_scc0 .Lprio_done
	s_setprio 1
.Lprio_done:
	s_load_dwordx2 s[92:93], s[0:1], 0xa0
	s_load_dword s90, s[0:1], 0xb0
	s_load_dwordx8 s[4:11], s[0:1], 0x80
	v_readfirstlane_b32 s3, v0
	s_mov_b32 s96, s2
	s_waitcnt lgkmcnt(0)
	v_writelane_b32 v254, s4, 0
	s_nop 1
	v_writelane_b32 v254, s5, 1
	v_writelane_b32 v254, s6, 2
	v_writelane_b32 v254, s7, 3
	v_writelane_b32 v254, s8, 4
	v_writelane_b32 v254, s9, 5
	v_writelane_b32 v254, s10, 6
	v_writelane_b32 v254, s11, 7
	s_add_u32 s4, s0, 0xb0
	v_writelane_b32 v254, s3, 8
	s_addc_u32 s5, s1, 0
	v_writelane_b32 v254, s4, 9
	s_and_b32 s3, s90, 7
	s_cmp_lg_u32 s3, 0
	v_writelane_b32 v254, s5, 10
	s_cbranch_scc1 .LBB0_2
	s_ashr_i32 s4, s2, 31
	s_lshr_b32 s4, s4, 29
	s_add_i32 s4, s2, s4
	s_ashr_i32 s5, s4, 3
	s_and_b32 s4, s4, -8
	s_ashr_i32 s3, s90, 3
	s_sub_i32 s4, s2, s4
	s_mul_i32 s3, s3, s4
	s_add_i32 s96, s3, s5

.Lpk0_entry:
	s_waitcnt lgkmcnt(0)
	ds_read_b128 v[106:109], v198
	ds_read_b128 v[110:113], v198 offset:1024
	ds_read_b128 v[114:117], v198 offset:2048
	ds_read_b128 v[118:121], v198 offset:3072
	ds_read_b128 v[182:185], v199
	ds_read_b128 v[186:189], v199 offset:1024
	ds_read_b128 v[190:193], v199 offset:2048
	ds_read_b128 v[202:205], v199 offset:3072
	s_add_u32 s14, s12, 0x100
	s_addc_u32 s15, s13, 0
	s_cmp_eq_u32 s67, 12
	s_cselect_b32 s43, s11, s15
	s_cselect_b32 s42, s31, s14
	s_cselect_b32 s41, s35, s66
	s_cselect_b32 s40, s64, s65
	v_lshl_add_u64 v[194:195], s[12:13], 0, v[172:173]
	s_add_i32 m0, s53, 0xc000
	ds_read_b128 v[206:209], v200
	ds_read_b128 v[210:213], v200 offset:1024
	ds_read_b128 v[214:217], v200 offset:2048
	ds_read_b128 v[218:221], v200 offset:3072
	ds_read_b128 v[222:225], v200 offset:4096
	ds_read_b128 v[226:229], v200 offset:5120
	ds_read_b128 v[230:233], v200 offset:6144
	ds_read_b128 v[234:237], v200 offset:7168
	global_load_lds_dwordx4 v[194:195], off
	v_lshl_add_u64 v[194:195], s[12:13], 0, v[174:175]
	s_add_i32 m0, s53, 0xe000
	s_nop 0
	global_load_lds_dwordx4 v[194:195], off
	s_waitcnt vmcnt(8)
	s_waitcnt lgkmcnt(0)
	s_barrier
	s_waitcnt lgkmcnt(0)
	v_mfma_i32_16x16x64_i8 v[142:145], v[106:109], v[206:209], 0
	v_mfma_i32_16x16x64_i8 v[138:141], v[114:117], v[206:209], 0
	v_mfma_i32_16x16x64_i8 v[122:125], v[106:109], v[214:217], 0
	v_mfma_i32_16x16x64_i8 v[126:129], v[114:117], v[214:217], 0
	v_mfma_i32_16x16x64_i8 v[94:97], v[106:109], v[222:225], 0
	v_mfma_i32_16x16x64_i8 v[90:93], v[114:117], v[222:225], 0
	v_mfma_i32_16x16x64_i8 v[74:77], v[106:109], v[230:233], 0
	v_mfma_i32_16x16x64_i8 v[82:85], v[114:117], v[230:233], 0
	v_mfma_i32_16x16x64_i8 v[142:145], v[110:113], v[210:213], v[142:145]
	v_mfma_i32_16x16x64_i8 v[138:141], v[118:121], v[210:213], v[138:141]
	v_mfma_i32_16x16x64_i8 v[122:125], v[110:113], v[218:221], v[122:125]
	v_mfma_i32_16x16x64_i8 v[126:129], v[118:121], v[218:221], v[126:129]
	v_mfma_i32_16x16x64_i8 v[94:97], v[110:113], v[226:229], v[94:97]
	v_mfma_i32_16x16x64_i8 v[90:93], v[118:121], v[226:229], v[90:93]
	v_mfma_i32_16x16x64_i8 v[74:77], v[110:113], v[234:237], v[74:77]
	v_mfma_i32_16x16x64_i8 v[82:85], v[118:121], v[234:237], v[82:85]
	v_mfma_i32_16x16x64_i8 v[134:137], v[182:185], v[206:209], 0
	v_mfma_i32_16x16x64_i8 v[130:133], v[190:193], v[206:209], 0
	v_mfma_i32_16x16x64_i8 v[98:101], v[182:185], v[214:217], 0
	v_mfma_i32_16x16x64_i8 v[102:105], v[190:193], v[214:217], 0
	v_mfma_i32_16x16x64_i8 v[86:89], v[182:185], v[222:225], 0
	v_mfma_i32_16x16x64_i8 v[78:81], v[190:193], v[222:225], 0
	v_mfma_i32_16x16x64_i8 v[58:61], v[182:185], v[230:233], 0
	v_mfma_i32_16x16x64_i8 v[70:73], v[190:193], v[230:233], 0
	v_mfma_i32_16x16x64_i8 v[134:137], v[186:189], v[210:213], v[134:137]
	v_mfma_i32_16x16x64_i8 v[130:133], v[202:205], v[210:213], v[130:133]
	v_mfma_i32_16x16x64_i8 v[98:101], v[186:189], v[218:221], v[98:101]
	v_mfma_i32_16x16x64_i8 v[102:105], v[202:205], v[218:221], v[102:105]
	v_mfma_i32_16x16x64_i8 v[86:89], v[186:189], v[226:229], v[86:89]
	v_mfma_i32_16x16x64_i8 v[78:81], v[202:205], v[226:229], v[78:81]
	v_mfma_i32_16x16x64_i8 v[58:61], v[186:189], v[234:237], v[58:61]
	v_mfma_i32_16x16x64_i8 v[70:73], v[202:205], v[234:237], v[70:73]
	s_barrier
	s_add_i32 s12, s60, s29
	v_lshl_add_u64 v[194:195], s[40:41], 0, v[148:149]
	s_mov_b32 m0, s12
	ds_read_b128 v[206:209], v200 offset:16384
	ds_read_b128 v[210:213], v200 offset:17408
	ds_read_b128 v[214:217], v200 offset:18432
	ds_read_b128 v[218:221], v200 offset:19456
	ds_read_b128 v[222:225], v200 offset:20480
	ds_read_b128 v[226:229], v200 offset:21504
	ds_read_b128 v[230:233], v200 offset:22528
	ds_read_b128 v[234:237], v200 offset:23552
	global_load_lds_dwordx4 v[194:195], off
	s_add_i32 m0, s12, 0x2000
	s_add_u32 s12, s40, 0x40000
	v_lshl_add_u64 v[238:239], s[40:41], 0, v[150:151]
	s_addc_u32 s13, s41, 0
	s_add_i32 s68, s61, s29
	global_load_lds_dwordx4 v[238:239], off
	v_lshl_add_u64 v[240:241], s[12:13], 0, v[148:149]
	s_mov_b32 m0, s68
	v_lshl_add_u64 v[242:243], s[42:43], 0, v[154:155]
	global_load_lds_dwordx4 v[240:241], off
	v_lshl_add_u64 v[240:241], s[12:13], 0, v[150:151]
	s_add_i32 m0, s68, 0x2000
	s_nop 0
	global_load_lds_dwordx4 v[240:241], off
	v_lshl_add_u64 v[240:241], s[42:43], 0, v[152:153]
	s_mov_b32 m0, s53
	s_nop 0
	global_load_lds_dwordx4 v[240:241], off
	s_mov_b32 m0, s54
	s_nop 0
	global_load_lds_dwordx4 v[242:243], off
	s_waitcnt vmcnt(8)
	s_waitcnt lgkmcnt(0)
	s_barrier
	s_waitcnt lgkmcnt(0)
	v_mfma_i32_16x16x64_i8 v[54:57], v[106:109], v[206:209], 0
	v_mfma_i32_16x16x64_i8 v[50:53], v[114:117], v[206:209], 0
	v_mfma_i32_16x16x64_i8 v[34:37], v[106:109], v[214:217], 0
	v_mfma_i32_16x16x64_i8 v[38:41], v[114:117], v[214:217], 0
	v_mfma_i32_16x16x64_i8 v[22:25], v[106:109], v[222:225], 0
	v_mfma_i32_16x16x64_i8 v[18:21], v[114:117], v[222:225], 0
	v_mfma_i32_16x16x64_i8 v[2:5], v[106:109], v[230:233], 0
	v_mfma_i32_16x16x64_i8 v[6:9], v[114:117], v[230:233], 0
	v_mfma_i32_16x16x64_i8 v[54:57], v[110:113], v[210:213], v[54:57]
	v_mfma_i32_16x16x64_i8 v[50:53], v[118:121], v[210:213], v[50:53]
	v_mfma_i32_16x16x64_i8 v[34:37], v[110:113], v[218:221], v[34:37]
	v_mfma_i32_16x16x64_i8 v[38:41], v[118:121], v[218:221], v[38:41]
	v_mfma_i32_16x16x64_i8 v[22:25], v[110:113], v[226:229], v[22:25]
	v_mfma_i32_16x16x64_i8 v[18:21], v[118:121], v[226:229], v[18:21]
	v_mfma_i32_16x16x64_i8 v[2:5], v[110:113], v[234:237], v[2:5]
	v_mfma_i32_16x16x64_i8 v[6:9], v[118:121], v[234:237], v[6:9]
	v_mfma_i32_16x16x64_i8 v[66:69], v[182:185], v[206:209], 0
	v_mfma_i32_16x16x64_i8 v[62:65], v[190:193], v[206:209], 0
	v_mfma_i32_16x16x64_i8 v[42:45], v[182:185], v[214:217], 0
	v_mfma_i32_16x16x64_i8 v[46:49], v[190:193], v[214:217], 0
	v_mfma_i32_16x16x64_i8 v[30:33], v[182:185], v[222:225], 0
	v_mfma_i32_16x16x64_i8 v[26:29], v[190:193], v[222:225], 0
	v_mfma_i32_16x16x64_i8 v[10:13], v[182:185], v[230:233], 0
	v_mfma_i32_16x16x64_i8 v[14:17], v[190:193], v[230:233], 0
	v_mfma_i32_16x16x64_i8 v[66:69], v[186:189], v[210:213], v[66:69]
	v_mfma_i32_16x16x64_i8 v[62:65], v[202:205], v[210:213], v[62:65]
	v_mfma_i32_16x16x64_i8 v[42:45], v[186:189], v[218:221], v[42:45]
	v_mfma_i32_16x16x64_i8 v[46:49], v[202:205], v[218:221], v[46:49]
	v_mfma_i32_16x16x64_i8 v[30:33], v[186:189], v[226:229], v[30:33]
	v_mfma_i32_16x16x64_i8 v[26:29], v[202:205], v[226:229], v[26:29]
	v_mfma_i32_16x16x64_i8 v[10:13], v[186:189], v[234:237], v[10:13]
	v_mfma_i32_16x16x64_i8 v[14:17], v[202:205], v[234:237], v[14:17]
	s_barrier
	s_add_i32 s12, 0, 0x18000
	s_add_i32 s68, 0, 0x1c000
	v_add_u32_e32 v118, s12, v196
	v_add_u32_e32 v146, s68, v196
	ds_read_b128 v[106:109], v118
	ds_read_b128 v[110:113], v118 offset:1024
	ds_read_b128 v[114:117], v118 offset:2048
	ds_read_b128 v[118:121], v118 offset:3072
	ds_read_b128 v[182:185], v146
	ds_read_b128 v[186:189], v146 offset:1024
	ds_read_b128 v[190:193], v146 offset:2048
	ds_read_b128 v[202:205], v146 offset:3072
	s_mov_b32 m0, s55
	v_lshl_add_u64 v[244:245], s[42:43], 0, v[156:157]
	ds_read_b128 v[206:209], v200 offset:32768
	ds_read_b128 v[210:213], v200 offset:33792
	ds_read_b128 v[214:217], v200 offset:34816
	ds_read_b128 v[218:221], v200 offset:35840
	ds_read_b128 v[222:225], v200 offset:36864
	ds_read_b128 v[226:229], v200 offset:37888
	ds_read_b128 v[230:233], v200 offset:38912
	ds_read_b128 v[234:237], v200 offset:39936
	global_load_lds_dwordx4 v[244:245], off
	v_lshl_add_u64 v[244:245], s[42:43], 0, v[158:159]
	s_mov_b32 m0, s56
	s_nop 0
	global_load_lds_dwordx4 v[244:245], off
	s_waitcnt vmcnt(8)
	s_waitcnt lgkmcnt(0)
	s_barrier
	s_waitcnt lgkmcnt(0)
	v_mfma_i32_16x16x64_i8 v[142:145], v[106:109], v[206:209], v[142:145]
	v_mfma_i32_16x16x64_i8 v[138:141], v[114:117], v[206:209], v[138:141]
	v_mfma_i32_16x16x64_i8 v[122:125], v[106:109], v[214:217], v[122:125]
	v_mfma_i32_16x16x64_i8 v[126:129], v[114:117], v[214:217], v[126:129]
	v_mfma_i32_16x16x64_i8 v[94:97], v[106:109], v[222:225], v[94:97]
	v_mfma_i32_16x16x64_i8 v[90:93], v[114:117], v[222:225], v[90:93]
	v_mfma_i32_16x16x64_i8 v[74:77], v[106:109], v[230:233], v[74:77]
	v_mfma_i32_16x16x64_i8 v[82:85], v[114:117], v[230:233], v[82:85]
	v_mfma_i32_16x16x64_i8 v[142:145], v[110:113], v[210:213], v[142:145]
	v_mfma_i32_16x16x64_i8 v[138:141], v[118:121], v[210:213], v[138:141]
	v_mfma_i32_16x16x64_i8 v[122:125], v[110:113], v[218:221], v[122:125]
	v_mfma_i32_16x16x64_i8 v[126:129], v[118:121], v[218:221], v[126:129]
	v_mfma_i32_16x16x64_i8 v[94:97], v[110:113], v[226:229], v[94:97]
	v_mfma_i32_16x16x64_i8 v[90:93], v[118:121], v[226:229], v[90:93]
	v_mfma_i32_16x16x64_i8 v[74:77], v[110:113], v[234:237], v[74:77]
	v_mfma_i32_16x16x64_i8 v[82:85], v[118:121], v[234:237], v[82:85]
	v_mfma_i32_16x16x64_i8 v[134:137], v[182:185], v[206:209], v[134:137]
	v_mfma_i32_16x16x64_i8 v[130:133], v[190:193], v[206:209], v[130:133]
	v_mfma_i32_16x16x64_i8 v[98:101], v[182:185], v[214:217], v[98:101]
	v_mfma_i32_16x16x64_i8 v[102:105], v[190:193], v[214:217], v[102:105]
	v_mfma_i32_16x16x64_i8 v[86:89], v[182:185], v[222:225], v[86:89]
	v_mfma_i32_16x16x64_i8 v[78:81], v[190:193], v[222:225], v[78:81]
	v_mfma_i32_16x16x64_i8 v[58:61], v[182:185], v[230:233], v[58:61]
	v_mfma_i32_16x16x64_i8 v[70:73], v[190:193], v[230:233], v[70:73]
	v_mfma_i32_16x16x64_i8 v[134:137], v[186:189], v[210:213], v[134:137]
	v_mfma_i32_16x16x64_i8 v[130:133], v[202:205], v[210:213], v[130:133]
	v_mfma_i32_16x16x64_i8 v[98:101], v[186:189], v[218:221], v[98:101]
	v_mfma_i32_16x16x64_i8 v[102:105], v[202:205], v[218:221], v[102:105]
	v_mfma_i32_16x16x64_i8 v[86:89], v[186:189], v[226:229], v[86:89]
	v_mfma_i32_16x16x64_i8 v[78:81], v[202:205], v[226:229], v[78:81]
	v_mfma_i32_16x16x64_i8 v[58:61], v[186:189], v[234:237], v[58:61]
	v_mfma_i32_16x16x64_i8 v[70:73], v[202:205], v[234:237], v[70:73]
	s_barrier
	s_add_i32 s12, s12, s29
	v_lshl_add_u64 v[194:195], v[194:195], 0, s[24:25]
	s_mov_b32 m0, s12
	ds_read_b128 v[206:209], v200 offset:49152
	ds_read_b128 v[210:213], v200 offset:50176
	ds_read_b128 v[214:217], v200 offset:51200
	ds_read_b128 v[218:221], v200 offset:52224
	ds_read_b128 v[222:225], v200 offset:53248
	ds_read_b128 v[226:229], v200 offset:54272
	ds_read_b128 v[230:233], v200 offset:55296
	ds_read_b128 v[234:237], v200 offset:56320
	global_load_lds_dwordx4 v[194:195], off
	s_add_i32 m0, s12, 0x2000
	s_add_u32 s12, s40, 0x40080
	v_lshl_add_u64 v[194:195], v[238:239], 0, s[24:25]
	s_addc_u32 s13, s41, 0
	s_add_i32 s40, s68, s29
	global_load_lds_dwordx4 v[194:195], off
	v_lshl_add_u64 v[194:195], s[12:13], 0, v[148:149]
	s_mov_b32 m0, s40
	s_nop 0
	global_load_lds_dwordx4 v[194:195], off
	v_lshl_add_u64 v[194:195], s[12:13], 0, v[150:151]
	s_add_i32 m0, s40, 0x2000
	s_nop 0
	global_load_lds_dwordx4 v[194:195], off
	v_lshl_add_u64 v[194:195], v[240:241], 0, s[24:25]
	s_mov_b32 m0, s58
	s_nop 0
	global_load_lds_dwordx4 v[194:195], off
	v_lshl_add_u64 v[194:195], v[242:243], 0, s[24:25]
	s_mov_b32 m0, s59
	s_nop 0
	global_load_lds_dwordx4 v[194:195], off
	s_waitcnt vmcnt(8)
	s_waitcnt lgkmcnt(0)
	s_barrier
	s_waitcnt lgkmcnt(0)
	v_mfma_i32_16x16x64_i8 v[54:57], v[106:109], v[206:209], v[54:57]
	v_mfma_i32_16x16x64_i8 v[50:53], v[114:117], v[206:209], v[50:53]
	v_mfma_i32_16x16x64_i8 v[34:37], v[106:109], v[214:217], v[34:37]
	v_mfma_i32_16x16x64_i8 v[38:41], v[114:117], v[214:217], v[38:41]
	v_mfma_i32_16x16x64_i8 v[22:25], v[106:109], v[222:225], v[22:25]
	v_mfma_i32_16x16x64_i8 v[18:21], v[114:117], v[222:225], v[18:21]
	v_mfma_i32_16x16x64_i8 v[2:5], v[106:109], v[230:233], v[2:5]
	v_mfma_i32_16x16x64_i8 v[6:9], v[114:117], v[230:233], v[6:9]
	v_mfma_i32_16x16x64_i8 v[54:57], v[110:113], v[210:213], v[54:57]
	v_mfma_i32_16x16x64_i8 v[50:53], v[118:121], v[210:213], v[50:53]
	v_mfma_i32_16x16x64_i8 v[34:37], v[110:113], v[218:221], v[34:37]
	v_mfma_i32_16x16x64_i8 v[38:41], v[118:121], v[218:221], v[38:41]
	v_mfma_i32_16x16x64_i8 v[22:25], v[110:113], v[226:229], v[22:25]
	v_mfma_i32_16x16x64_i8 v[18:21], v[118:121], v[226:229], v[18:21]
	v_mfma_i32_16x16x64_i8 v[2:5], v[110:113], v[234:237], v[2:5]
	v_mfma_i32_16x16x64_i8 v[6:9], v[118:121], v[234:237], v[6:9]
	v_mfma_i32_16x16x64_i8 v[66:69], v[182:185], v[206:209], v[66:69]
	v_mfma_i32_16x16x64_i8 v[62:65], v[190:193], v[206:209], v[62:65]
	v_mfma_i32_16x16x64_i8 v[42:45], v[182:185], v[214:217], v[42:45]
	v_mfma_i32_16x16x64_i8 v[46:49], v[190:193], v[214:217], v[46:49]
	v_mfma_i32_16x16x64_i8 v[30:33], v[182:185], v[222:225], v[30:33]
	v_mfma_i32_16x16x64_i8 v[26:29], v[190:193], v[222:225], v[26:29]
	v_mfma_i32_16x16x64_i8 v[10:13], v[182:185], v[230:233], v[10:13]
	v_mfma_i32_16x16x64_i8 v[14:17], v[190:193], v[230:233], v[14:17]
	v_mfma_i32_16x16x64_i8 v[66:69], v[186:189], v[210:213], v[66:69]
	v_mfma_i32_16x16x64_i8 v[62:65], v[202:205], v[210:213], v[62:65]
	v_mfma_i32_16x16x64_i8 v[42:45], v[186:189], v[218:221], v[42:45]
	v_mfma_i32_16x16x64_i8 v[46:49], v[202:205], v[218:221], v[46:49]
	v_mfma_i32_16x16x64_i8 v[30:33], v[186:189], v[226:229], v[30:33]
	v_mfma_i32_16x16x64_i8 v[26:29], v[202:205], v[226:229], v[26:29]
	v_mfma_i32_16x16x64_i8 v[10:13], v[186:189], v[234:237], v[10:13]
	v_mfma_i32_16x16x64_i8 v[14:17], v[202:205], v[234:237], v[14:17]
	s_barrier
	s_add_i32 s67, s67, 2
	s_add_u32 s65, s65, 0x100
	s_addc_u32 s66, s66, 0
	s_cmp_gt_u32 s67, 13
	s_mov_b64 s[12:13], s[14:15]
	s_cbranch_scc0 .LBB0_164
	s_branch .Lpk0_exit
.LBB0_164:
	s_waitcnt lgkmcnt(0)
	ds_read_b128 v[106:109], v198
	ds_read_b128 v[110:113], v198 offset:1024
	ds_read_b128 v[114:117], v198 offset:2048
	ds_read_b128 v[118:121], v198 offset:3072
	ds_read_b128 v[182:185], v199
	ds_read_b128 v[186:189], v199 offset:1024
	ds_read_b128 v[190:193], v199 offset:2048
	ds_read_b128 v[202:205], v199 offset:3072
	s_add_u32 s14, s12, 0x100
	s_addc_u32 s15, s13, 0
	s_cmp_eq_u32 s67, 12
	s_cselect_b32 s43, s11, s15
	s_cselect_b32 s42, s31, s14
	s_cselect_b32 s41, s35, s66
	s_cselect_b32 s40, s64, s65
	v_lshl_add_u64 v[194:195], s[12:13], 0, v[172:173]
	s_add_i32 m0, s53, 0xc000
	ds_read_b128 v[206:209], v200
	ds_read_b128 v[210:213], v200 offset:1024
	ds_read_b128 v[214:217], v200 offset:2048
	ds_read_b128 v[218:221], v200 offset:3072
	ds_read_b128 v[222:225], v200 offset:4096
	ds_read_b128 v[226:229], v200 offset:5120
	ds_read_b128 v[230:233], v200 offset:6144
	ds_read_b128 v[234:237], v200 offset:7168
	global_load_lds_dwordx4 v[194:195], off
	v_lshl_add_u64 v[194:195], s[12:13], 0, v[174:175]
	s_add_i32 m0, s53, 0xe000
	s_nop 0
	global_load_lds_dwordx4 v[194:195], off
	s_waitcnt vmcnt(8)
	s_waitcnt lgkmcnt(0)
	s_barrier
	s_waitcnt lgkmcnt(0)
	v_mfma_i32_16x16x64_i8 v[142:145], v[106:109], v[206:209], v[142:145]
	v_mfma_i32_16x16x64_i8 v[138:141], v[114:117], v[206:209], v[138:141]
	v_mfma_i32_16x16x64_i8 v[122:125], v[106:109], v[214:217], v[122:125]
	v_mfma_i32_16x16x64_i8 v[126:129], v[114:117], v[214:217], v[126:129]
	v_mfma_i32_16x16x64_i8 v[94:97], v[106:109], v[222:225], v[94:97]
	v_mfma_i32_16x16x64_i8 v[90:93], v[114:117], v[222:225], v[90:93]
	v_mfma_i32_16x16x64_i8 v[74:77], v[106:109], v[230:233], v[74:77]
	v_mfma_i32_16x16x64_i8 v[82:85], v[114:117], v[230:233], v[82:85]
	v_mfma_i32_16x16x64_i8 v[142:145], v[110:113], v[210:213], v[142:145]
	v_mfma_i32_16x16x64_i8 v[138:141], v[118:121], v[210:213], v[138:141]
	v_mfma_i32_16x16x64_i8 v[122:125], v[110:113], v[218:221], v[122:125]
	v_mfma_i32_16x16x64_i8 v[126:129], v[118:121], v[218:221], v[126:129]
	v_mfma_i32_16x16x64_i8 v[94:97], v[110:113], v[226:229], v[94:97]
	v_mfma_i32_16x16x64_i8 v[90:93], v[118:121], v[226:229], v[90:93]
	v_mfma_i32_16x16x64_i8 v[74:77], v[110:113], v[234:237], v[74:77]
	v_mfma_i32_16x16x64_i8 v[82:85], v[118:121], v[234:237], v[82:85]
	v_mfma_i32_16x16x64_i8 v[134:137], v[182:185], v[206:209], v[134:137]
	v_mfma_i32_16x16x64_i8 v[130:133], v[190:193], v[206:209], v[130:133]
	v_mfma_i32_16x16x64_i8 v[98:101], v[182:185], v[214:217], v[98:101]
	v_mfma_i32_16x16x64_i8 v[102:105], v[190:193], v[214:217], v[102:105]
	v_mfma_i32_16x16x64_i8 v[86:89], v[182:185], v[222:225], v[86:89]
	v_mfma_i32_16x16x64_i8 v[78:81], v[190:193], v[222:225], v[78:81]
	v_mfma_i32_16x16x64_i8 v[58:61], v[182:185], v[230:233], v[58:61]
	v_mfma_i32_16x16x64_i8 v[70:73], v[190:193], v[230:233], v[70:73]
	v_mfma_i32_16x16x64_i8 v[134:137], v[186:189], v[210:213], v[134:137]
	v_mfma_i32_16x16x64_i8 v[130:133], v[202:205], v[210:213], v[130:133]
	v_mfma_i32_16x16x64_i8 v[98:101], v[186:189], v[218:221], v[98:101]
	v_mfma_i32_16x16x64_i8 v[102:105], v[202:205], v[218:221], v[102:105]
	v_mfma_i32_16x16x64_i8 v[86:89], v[186:189], v[226:229], v[86:89]
	v_mfma_i32_16x16x64_i8 v[78:81], v[202:205], v[226:229], v[78:81]
	v_mfma_i32_16x16x64_i8 v[58:61], v[186:189], v[234:237], v[58:61]
	v_mfma_i32_16x16x64_i8 v[70:73], v[202:205], v[234:237], v[70:73]
	s_barrier
	s_add_i32 s12, s60, s29
	v_lshl_add_u64 v[194:195], s[40:41], 0, v[148:149]
	s_mov_b32 m0, s12
	ds_read_b128 v[206:209], v200 offset:16384
	ds_read_b128 v[210:213], v200 offset:17408
	ds_read_b128 v[214:217], v200 offset:18432
	ds_read_b128 v[218:221], v200 offset:19456
	ds_read_b128 v[222:225], v200 offset:20480
	ds_read_b128 v[226:229], v200 offset:21504
	ds_read_b128 v[230:233], v200 offset:22528
	ds_read_b128 v[234:237], v200 offset:23552
	global_load_lds_dwordx4 v[194:195], off
	s_add_i32 m0, s12, 0x2000
	s_add_u32 s12, s40, 0x40000
	v_lshl_add_u64 v[238:239], s[40:41], 0, v[150:151]
	s_addc_u32 s13, s41, 0
	s_add_i32 s68, s61, s29
	global_load_lds_dwordx4 v[238:239], off
	v_lshl_add_u64 v[240:241], s[12:13], 0, v[148:149]
	s_mov_b32 m0, s68
	v_lshl_add_u64 v[242:243], s[42:43], 0, v[154:155]
	global_load_lds_dwordx4 v[240:241], off
	v_lshl_add_u64 v[240:241], s[12:13], 0, v[150:151]
	s_add_i32 m0, s68, 0x2000
	s_nop 0
	global_load_lds_dwordx4 v[240:241], off
	v_lshl_add_u64 v[240:241], s[42:43], 0, v[152:153]
	s_mov_b32 m0, s53
	s_nop 0
	global_load_lds_dwordx4 v[240:241], off
	s_mov_b32 m0, s54
	s_nop 0
	global_load_lds_dwordx4 v[242:243], off
	s_waitcnt vmcnt(8)
	s_waitcnt lgkmcnt(0)
	s_barrier
	s_waitcnt lgkmcnt(0)
	v_mfma_i32_16x16x64_i8 v[54:57], v[106:109], v[206:209], v[54:57]
	v_mfma_i32_16x16x64_i8 v[50:53], v[114:117], v[206:209], v[50:53]
	v_mfma_i32_16x16x64_i8 v[34:37], v[106:109], v[214:217], v[34:37]
	v_mfma_i32_16x16x64_i8 v[38:41], v[114:117], v[214:217], v[38:41]
	v_mfma_i32_16x16x64_i8 v[22:25], v[106:109], v[222:225], v[22:25]
	v_mfma_i32_16x16x64_i8 v[18:21], v[114:117], v[222:225], v[18:21]
	v_mfma_i32_16x16x64_i8 v[2:5], v[106:109], v[230:233], v[2:5]
	v_mfma_i32_16x16x64_i8 v[6:9], v[114:117], v[230:233], v[6:9]
	v_mfma_i32_16x16x64_i8 v[54:57], v[110:113], v[210:213], v[54:57]
	v_mfma_i32_16x16x64_i8 v[50:53], v[118:121], v[210:213], v[50:53]
	v_mfma_i32_16x16x64_i8 v[34:37], v[110:113], v[218:221], v[34:37]
	v_mfma_i32_16x16x64_i8 v[38:41], v[118:121], v[218:221], v[38:41]
	v_mfma_i32_16x16x64_i8 v[22:25], v[110:113], v[226:229], v[22:25]
	v_mfma_i32_16x16x64_i8 v[18:21], v[118:121], v[226:229], v[18:21]
	v_mfma_i32_16x16x64_i8 v[2:5], v[110:113], v[234:237], v[2:5]
	v_mfma_i32_16x16x64_i8 v[6:9], v[118:121], v[234:237], v[6:9]
	v_mfma_i32_16x16x64_i8 v[66:69], v[182:185], v[206:209], v[66:69]
	v_mfma_i32_16x16x64_i8 v[62:65], v[190:193], v[206:209], v[62:65]
	v_mfma_i32_16x16x64_i8 v[42:45], v[182:185], v[214:217], v[42:45]
	v_mfma_i32_16x16x64_i8 v[46:49], v[190:193], v[214:217], v[46:49]
	v_mfma_i32_16x16x64_i8 v[30:33], v[182:185], v[222:225], v[30:33]
	v_mfma_i32_16x16x64_i8 v[26:29], v[190:193], v[222:225], v[26:29]
	v_mfma_i32_16x16x64_i8 v[10:13], v[182:185], v[230:233], v[10:13]
	v_mfma_i32_16x16x64_i8 v[14:17], v[190:193], v[230:233], v[14:17]
	v_mfma_i32_16x16x64_i8 v[66:69], v[186:189], v[210:213], v[66:69]
	v_mfma_i32_16x16x64_i8 v[62:65], v[202:205], v[210:213], v[62:65]
	v_mfma_i32_16x16x64_i8 v[42:45], v[186:189], v[218:221], v[42:45]
	v_mfma_i32_16x16x64_i8 v[46:49], v[202:205], v[218:221], v[46:49]
	v_mfma_i32_16x16x64_i8 v[30:33], v[186:189], v[226:229], v[30:33]
	v_mfma_i32_16x16x64_i8 v[26:29], v[202:205], v[226:229], v[26:29]
	v_mfma_i32_16x16x64_i8 v[10:13], v[186:189], v[234:237], v[10:13]
	v_mfma_i32_16x16x64_i8 v[14:17], v[202:205], v[234:237], v[14:17]
	s_barrier
	s_add_i32 s12, 0, 0x18000
	s_add_i32 s68, 0, 0x1c000
	v_add_u32_e32 v118, s12, v196
	v_add_u32_e32 v146, s68, v196
	ds_read_b128 v[106:109], v118
	ds_read_b128 v[110:113], v118 offset:1024
	ds_read_b128 v[114:117], v118 offset:2048
	ds_read_b128 v[118:121], v118 offset:3072
	ds_read_b128 v[182:185], v146
	ds_read_b128 v[186:189], v146 offset:1024
	ds_read_b128 v[190:193], v146 offset:2048
	ds_read_b128 v[202:205], v146 offset:3072
	s_mov_b32 m0, s55
	v_lshl_add_u64 v[244:245], s[42:43], 0, v[156:157]
	ds_read_b128 v[206:209], v200 offset:32768
	ds_read_b128 v[210:213], v200 offset:33792
	ds_read_b128 v[214:217], v200 offset:34816
	ds_read_b128 v[218:221], v200 offset:35840
	ds_read_b128 v[222:225], v200 offset:36864
	ds_read_b128 v[226:229], v200 offset:37888
	ds_read_b128 v[230:233], v200 offset:38912
	ds_read_b128 v[234:237], v200 offset:39936
	global_load_lds_dwordx4 v[244:245], off
	v_lshl_add_u64 v[244:245], s[42:43], 0, v[158:159]
	s_mov_b32 m0, s56
	s_nop 0
	global_load_lds_dwordx4 v[244:245], off
	s_waitcnt vmcnt(8)
	s_waitcnt lgkmcnt(0)
	s_barrier
	s_waitcnt lgkmcnt(0)
	v_mfma_i32_16x16x64_i8 v[142:145], v[106:109], v[206:209], v[142:145]
	v_mfma_i32_16x16x64_i8 v[138:141], v[114:117], v[206:209], v[138:141]
	v_mfma_i32_16x16x64_i8 v[122:125], v[106:109], v[214:217], v[122:125]
	v_mfma_i32_16x16x64_i8 v[126:129], v[114:117], v[214:217], v[126:129]
	v_mfma_i32_16x16x64_i8 v[94:97], v[106:109], v[222:225], v[94:97]
	v_mfma_i32_16x16x64_i8 v[90:93], v[114:117], v[222:225], v[90:93]
	v_mfma_i32_16x16x64_i8 v[74:77], v[106:109], v[230:233], v[74:77]
	v_mfma_i32_16x16x64_i8 v[82:85], v[114:117], v[230:233], v[82:85]
	v_mfma_i32_16x16x64_i8 v[142:145], v[110:113], v[210:213], v[142:145]
	v_mfma_i32_16x16x64_i8 v[138:141], v[118:121], v[210:213], v[138:141]
	v_mfma_i32_16x16x64_i8 v[122:125], v[110:113], v[218:221], v[122:125]
	v_mfma_i32_16x16x64_i8 v[126:129], v[118:121], v[218:221], v[126:129]
	v_mfma_i32_16x16x64_i8 v[94:97], v[110:113], v[226:229], v[94:97]
	v_mfma_i32_16x16x64_i8 v[90:93], v[118:121], v[226:229], v[90:93]
	v_mfma_i32_16x16x64_i8 v[74:77], v[110:113], v[234:237], v[74:77]
	v_mfma_i32_16x16x64_i8 v[82:85], v[118:121], v[234:237], v[82:85]
	v_mfma_i32_16x16x64_i8 v[134:137], v[182:185], v[206:209], v[134:137]
	v_mfma_i32_16x16x64_i8 v[130:133], v[190:193], v[206:209], v[130:133]
	v_mfma_i32_16x16x64_i8 v[98:101], v[182:185], v[214:217], v[98:101]
	v_mfma_i32_16x16x64_i8 v[102:105], v[190:193], v[214:217], v[102:105]
	v_mfma_i32_16x16x64_i8 v[86:89], v[182:185], v[222:225], v[86:89]
	v_mfma_i32_16x16x64_i8 v[78:81], v[190:193], v[222:225], v[78:81]
	v_mfma_i32_16x16x64_i8 v[58:61], v[182:185], v[230:233], v[58:61]
	v_mfma_i32_16x16x64_i8 v[70:73], v[190:193], v[230:233], v[70:73]
	v_mfma_i32_16x16x64_i8 v[134:137], v[186:189], v[210:213], v[134:137]
	v_mfma_i32_16x16x64_i8 v[130:133], v[202:205], v[210:213], v[130:133]
	v_mfma_i32_16x16x64_i8 v[98:101], v[186:189], v[218:221], v[98:101]
	v_mfma_i32_16x16x64_i8 v[102:105], v[202:205], v[218:221], v[102:105]
	v_mfma_i32_16x16x64_i8 v[86:89], v[186:189], v[226:229], v[86:89]
	v_mfma_i32_16x16x64_i8 v[78:81], v[202:205], v[226:229], v[78:81]
	v_mfma_i32_16x16x64_i8 v[58:61], v[186:189], v[234:237], v[58:61]
	v_mfma_i32_16x16x64_i8 v[70:73], v[202:205], v[234:237], v[70:73]
	s_barrier
	s_add_i32 s12, s12, s29
	v_lshl_add_u64 v[194:195], v[194:195], 0, s[24:25]
	s_mov_b32 m0, s12
	ds_read_b128 v[206:209], v200 offset:49152
	ds_read_b128 v[210:213], v200 offset:50176
	ds_read_b128 v[214:217], v200 offset:51200
	ds_read_b128 v[218:221], v200 offset:52224
	ds_read_b128 v[222:225], v200 offset:53248
	ds_read_b128 v[226:229], v200 offset:54272
	ds_read_b128 v[230:233], v200 offset:55296
	ds_read_b128 v[234:237], v200 offset:56320
	global_load_lds_dwordx4 v[194:195], off
	s_add_i32 m0, s12, 0x2000
	s_add_u32 s12, s40, 0x40080
	v_lshl_add_u64 v[194:195], v[238:239], 0, s[24:25]
	s_addc_u32 s13, s41, 0
	s_add_i32 s40, s68, s29
	global_load_lds_dwordx4 v[194:195], off
	v_lshl_add_u64 v[194:195], s[12:13], 0, v[148:149]
	s_mov_b32 m0, s40
	s_nop 0
	global_load_lds_dwordx4 v[194:195], off
	v_lshl_add_u64 v[194:195], s[12:13], 0, v[150:151]
	s_add_i32 m0, s40, 0x2000
	s_nop 0
	global_load_lds_dwordx4 v[194:195], off
	v_lshl_add_u64 v[194:195], v[240:241], 0, s[24:25]
	s_mov_b32 m0, s58
	s_nop 0
	global_load_lds_dwordx4 v[194:195], off
	v_lshl_add_u64 v[194:195], v[242:243], 0, s[24:25]
	s_mov_b32 m0, s59
	s_nop 0
	global_load_lds_dwordx4 v[194:195], off
	s_waitcnt vmcnt(8)
	s_waitcnt lgkmcnt(0)
	s_barrier
	s_waitcnt lgkmcnt(0)
	v_mfma_i32_16x16x64_i8 v[54:57], v[106:109], v[206:209], v[54:57]
	v_mfma_i32_16x16x64_i8 v[50:53], v[114:117], v[206:209], v[50:53]
	v_mfma_i32_16x16x64_i8 v[34:37], v[106:109], v[214:217], v[34:37]
	v_mfma_i32_16x16x64_i8 v[38:41], v[114:117], v[214:217], v[38:41]
	v_mfma_i32_16x16x64_i8 v[22:25], v[106:109], v[222:225], v[22:25]
	v_mfma_i32_16x16x64_i8 v[18:21], v[114:117], v[222:225], v[18:21]
	v_mfma_i32_16x16x64_i8 v[2:5], v[106:109], v[230:233], v[2:5]
	v_mfma_i32_16x16x64_i8 v[6:9], v[114:117], v[230:233], v[6:9]
	v_mfma_i32_16x16x64_i8 v[54:57], v[110:113], v[210:213], v[54:57]
	v_mfma_i32_16x16x64_i8 v[50:53], v[118:121], v[210:213], v[50:53]
	v_mfma_i32_16x16x64_i8 v[34:37], v[110:113], v[218:221], v[34:37]
	v_mfma_i32_16x16x64_i8 v[38:41], v[118:121], v[218:221], v[38:41]
	v_mfma_i32_16x16x64_i8 v[22:25], v[110:113], v[226:229], v[22:25]
	v_mfma_i32_16x16x64_i8 v[18:21], v[118:121], v[226:229], v[18:21]
	v_mfma_i32_16x16x64_i8 v[2:5], v[110:113], v[234:237], v[2:5]
	v_mfma_i32_16x16x64_i8 v[6:9], v[118:121], v[234:237], v[6:9]
	v_mfma_i32_16x16x64_i8 v[66:69], v[182:185], v[206:209], v[66:69]
	v_mfma_i32_16x16x64_i8 v[62:65], v[190:193], v[206:209], v[62:65]
	v_mfma_i32_16x16x64_i8 v[42:45], v[182:185], v[214:217], v[42:45]
	v_mfma_i32_16x16x64_i8 v[46:49], v[190:193], v[214:217], v[46:49]
	v_mfma_i32_16x16x64_i8 v[30:33], v[182:185], v[222:225], v[30:33]
	v_mfma_i32_16x16x64_i8 v[26:29], v[190:193], v[222:225], v[26:29]
	v_mfma_i32_16x16x64_i8 v[10:13], v[182:185], v[230:233], v[10:13]
	v_mfma_i32_16x16x64_i8 v[14:17], v[190:193], v[230:233], v[14:17]
	v_mfma_i32_16x16x64_i8 v[66:69], v[186:189], v[210:213], v[66:69]
	v_mfma_i32_16x16x64_i8 v[62:65], v[202:205], v[210:213], v[62:65]
	v_mfma_i32_16x16x64_i8 v[42:45], v[186:189], v[218:221], v[42:45]
	v_mfma_i32_16x16x64_i8 v[46:49], v[202:205], v[218:221], v[46:49]
	v_mfma_i32_16x16x64_i8 v[30:33], v[186:189], v[226:229], v[30:33]
	v_mfma_i32_16x16x64_i8 v[26:29], v[202:205], v[226:229], v[26:29]
	v_mfma_i32_16x16x64_i8 v[10:13], v[186:189], v[234:237], v[10:13]
	v_mfma_i32_16x16x64_i8 v[14:17], v[202:205], v[234:237], v[14:17]
	s_barrier
	s_add_i32 s67, s67, 2
	s_add_u32 s65, s65, 0x100
	s_addc_u32 s66, s66, 0
	s_cmp_gt_u32 s67, 13
	s_mov_b64 s[12:13], s[14:15]
	s_cbranch_scc0 .LBB0_164

.Lpk1_entry:
	s_waitcnt lgkmcnt(0)
	ds_read_b128 v[106:109], v198
	ds_read_b128 v[110:113], v198 offset:1024
	ds_read_b128 v[114:117], v198 offset:2048
	ds_read_b128 v[118:121], v198 offset:3072
	ds_read_b128 v[182:185], v199
	ds_read_b128 v[186:189], v199 offset:1024
	ds_read_b128 v[190:193], v199 offset:2048
	ds_read_b128 v[202:205], v199 offset:3072
	s_add_u32 s14, s12, 0x100
	s_addc_u32 s15, s13, 0
	s_cmp_eq_u32 s63, 12
	s_cselect_b32 s39, s11, s15
	s_cselect_b32 s38, s19, s14
	s_cselect_b32 s37, s29, s62
	s_cselect_b32 s36, s60, s61
	v_lshl_add_u64 v[194:195], s[12:13], 0, v[172:173]
	s_add_i32 m0, s42, 0xc000
	ds_read_b128 v[206:209], v200
	ds_read_b128 v[210:213], v200 offset:1024
	ds_read_b128 v[214:217], v200 offset:2048
	ds_read_b128 v[218:221], v200 offset:3072
	ds_read_b128 v[222:225], v200 offset:4096
	ds_read_b128 v[226:229], v200 offset:5120
	ds_read_b128 v[230:233], v200 offset:6144
	ds_read_b128 v[234:237], v200 offset:7168
	global_load_lds_dwordx4 v[194:195], off
	v_lshl_add_u64 v[194:195], s[12:13], 0, v[174:175]
	s_add_i32 m0, s42, 0xe000
	s_nop 0
	global_load_lds_dwordx4 v[194:195], off
	s_waitcnt vmcnt(8)
	s_waitcnt lgkmcnt(0)
	s_barrier
	s_waitcnt lgkmcnt(0)
	v_mfma_i32_16x16x64_i8 v[142:145], v[106:109], v[206:209], 0
	v_mfma_i32_16x16x64_i8 v[138:141], v[114:117], v[206:209], 0
	v_mfma_i32_16x16x64_i8 v[122:125], v[106:109], v[214:217], 0
	v_mfma_i32_16x16x64_i8 v[126:129], v[114:117], v[214:217], 0
	v_mfma_i32_16x16x64_i8 v[94:97], v[106:109], v[222:225], 0
	v_mfma_i32_16x16x64_i8 v[90:93], v[114:117], v[222:225], 0
	v_mfma_i32_16x16x64_i8 v[74:77], v[106:109], v[230:233], 0
	v_mfma_i32_16x16x64_i8 v[82:85], v[114:117], v[230:233], 0
	v_mfma_i32_16x16x64_i8 v[142:145], v[110:113], v[210:213], v[142:145]
	v_mfma_i32_16x16x64_i8 v[138:141], v[118:121], v[210:213], v[138:141]
	v_mfma_i32_16x16x64_i8 v[122:125], v[110:113], v[218:221], v[122:125]
	v_mfma_i32_16x16x64_i8 v[126:129], v[118:121], v[218:221], v[126:129]
	v_mfma_i32_16x16x64_i8 v[94:97], v[110:113], v[226:229], v[94:97]
	v_mfma_i32_16x16x64_i8 v[90:93], v[118:121], v[226:229], v[90:93]
	v_mfma_i32_16x16x64_i8 v[74:77], v[110:113], v[234:237], v[74:77]
	v_mfma_i32_16x16x64_i8 v[82:85], v[118:121], v[234:237], v[82:85]
	v_mfma_i32_16x16x64_i8 v[134:137], v[182:185], v[206:209], 0
	v_mfma_i32_16x16x64_i8 v[130:133], v[190:193], v[206:209], 0
	v_mfma_i32_16x16x64_i8 v[98:101], v[182:185], v[214:217], 0
	v_mfma_i32_16x16x64_i8 v[102:105], v[190:193], v[214:217], 0
	v_mfma_i32_16x16x64_i8 v[86:89], v[182:185], v[222:225], 0
	v_mfma_i32_16x16x64_i8 v[78:81], v[190:193], v[222:225], 0
	v_mfma_i32_16x16x64_i8 v[58:61], v[182:185], v[230:233], 0
	v_mfma_i32_16x16x64_i8 v[70:73], v[190:193], v[230:233], 0
	v_mfma_i32_16x16x64_i8 v[134:137], v[186:189], v[210:213], v[134:137]
	v_mfma_i32_16x16x64_i8 v[130:133], v[202:205], v[210:213], v[130:133]
	v_mfma_i32_16x16x64_i8 v[98:101], v[186:189], v[218:221], v[98:101]
	v_mfma_i32_16x16x64_i8 v[102:105], v[202:205], v[218:221], v[102:105]
	v_mfma_i32_16x16x64_i8 v[86:89], v[186:189], v[226:229], v[86:89]
	v_mfma_i32_16x16x64_i8 v[78:81], v[202:205], v[226:229], v[78:81]
	v_mfma_i32_16x16x64_i8 v[58:61], v[186:189], v[234:237], v[58:61]
	v_mfma_i32_16x16x64_i8 v[70:73], v[202:205], v[234:237], v[70:73]
	s_barrier
	s_add_i32 s12, s17, s40
	v_lshl_add_u64 v[194:195], s[36:37], 0, v[148:149]
	s_mov_b32 m0, s12
	ds_read_b128 v[206:209], v200 offset:16384
	ds_read_b128 v[210:213], v200 offset:17408
	ds_read_b128 v[214:217], v200 offset:18432
	ds_read_b128 v[218:221], v200 offset:19456
	ds_read_b128 v[222:225], v200 offset:20480
	ds_read_b128 v[226:229], v200 offset:21504
	ds_read_b128 v[230:233], v200 offset:22528
	ds_read_b128 v[234:237], v200 offset:23552
	global_load_lds_dwordx4 v[194:195], off
	s_add_i32 m0, s12, 0x2000
	s_add_u32 s12, s36, 0x40000
	v_lshl_add_u64 v[238:239], s[36:37], 0, v[150:151]
	s_addc_u32 s13, s37, 0
	s_add_i32 s64, s57, s40
	global_load_lds_dwordx4 v[238:239], off
	v_lshl_add_u64 v[240:241], s[12:13], 0, v[148:149]
	s_mov_b32 m0, s64
	v_lshl_add_u64 v[242:243], s[38:39], 0, v[154:155]
	global_load_lds_dwordx4 v[240:241], off
	v_lshl_add_u64 v[240:241], s[12:13], 0, v[150:151]
	s_add_i32 m0, s64, 0x2000
	s_nop 0
	global_load_lds_dwordx4 v[240:241], off
	v_lshl_add_u64 v[240:241], s[38:39], 0, v[152:153]
	s_mov_b32 m0, s42
	s_nop 0
	global_load_lds_dwordx4 v[240:241], off
	s_mov_b32 m0, s43
	s_nop 0
	global_load_lds_dwordx4 v[242:243], off
	s_waitcnt vmcnt(8)
	s_waitcnt lgkmcnt(0)
	s_barrier
	s_waitcnt lgkmcnt(0)
	v_mfma_i32_16x16x64_i8 v[54:57], v[106:109], v[206:209], 0
	v_mfma_i32_16x16x64_i8 v[50:53], v[114:117], v[206:209], 0
	v_mfma_i32_16x16x64_i8 v[34:37], v[106:109], v[214:217], 0
	v_mfma_i32_16x16x64_i8 v[38:41], v[114:117], v[214:217], 0
	v_mfma_i32_16x16x64_i8 v[22:25], v[106:109], v[222:225], 0
	v_mfma_i32_16x16x64_i8 v[18:21], v[114:117], v[222:225], 0
	v_mfma_i32_16x16x64_i8 v[2:5], v[106:109], v[230:233], 0
	v_mfma_i32_16x16x64_i8 v[6:9], v[114:117], v[230:233], 0
	v_mfma_i32_16x16x64_i8 v[54:57], v[110:113], v[210:213], v[54:57]
	v_mfma_i32_16x16x64_i8 v[50:53], v[118:121], v[210:213], v[50:53]
	v_mfma_i32_16x16x64_i8 v[34:37], v[110:113], v[218:221], v[34:37]
	v_mfma_i32_16x16x64_i8 v[38:41], v[118:121], v[218:221], v[38:41]
	v_mfma_i32_16x16x64_i8 v[22:25], v[110:113], v[226:229], v[22:25]
	v_mfma_i32_16x16x64_i8 v[18:21], v[118:121], v[226:229], v[18:21]
	v_mfma_i32_16x16x64_i8 v[2:5], v[110:113], v[234:237], v[2:5]
	v_mfma_i32_16x16x64_i8 v[6:9], v[118:121], v[234:237], v[6:9]
	v_mfma_i32_16x16x64_i8 v[66:69], v[182:185], v[206:209], 0
	v_mfma_i32_16x16x64_i8 v[62:65], v[190:193], v[206:209], 0
	v_mfma_i32_16x16x64_i8 v[42:45], v[182:185], v[214:217], 0
	v_mfma_i32_16x16x64_i8 v[46:49], v[190:193], v[214:217], 0
	v_mfma_i32_16x16x64_i8 v[30:33], v[182:185], v[222:225], 0
	v_mfma_i32_16x16x64_i8 v[26:29], v[190:193], v[222:225], 0
	v_mfma_i32_16x16x64_i8 v[10:13], v[182:185], v[230:233], 0
	v_mfma_i32_16x16x64_i8 v[14:17], v[190:193], v[230:233], 0
	v_mfma_i32_16x16x64_i8 v[66:69], v[186:189], v[210:213], v[66:69]
	v_mfma_i32_16x16x64_i8 v[62:65], v[202:205], v[210:213], v[62:65]
	v_mfma_i32_16x16x64_i8 v[42:45], v[186:189], v[218:221], v[42:45]
	v_mfma_i32_16x16x64_i8 v[46:49], v[202:205], v[218:221], v[46:49]
	v_mfma_i32_16x16x64_i8 v[30:33], v[186:189], v[226:229], v[30:33]
	v_mfma_i32_16x16x64_i8 v[26:29], v[202:205], v[226:229], v[26:29]
	v_mfma_i32_16x16x64_i8 v[10:13], v[186:189], v[234:237], v[10:13]
	v_mfma_i32_16x16x64_i8 v[14:17], v[202:205], v[234:237], v[14:17]
	s_barrier
	s_add_i32 s12, 0, 0x18000
	s_add_i32 s64, 0, 0x1c000
	v_add_u32_e32 v118, s12, v196
	v_add_u32_e32 v146, s64, v196
	ds_read_b128 v[106:109], v118
	ds_read_b128 v[110:113], v118 offset:1024
	ds_read_b128 v[114:117], v118 offset:2048
	ds_read_b128 v[118:121], v118 offset:3072
	ds_read_b128 v[182:185], v146
	ds_read_b128 v[186:189], v146 offset:1024
	ds_read_b128 v[190:193], v146 offset:2048
	ds_read_b128 v[202:205], v146 offset:3072
	s_mov_b32 m0, s52
	v_lshl_add_u64 v[244:245], s[38:39], 0, v[156:157]
	ds_read_b128 v[206:209], v200 offset:32768
	ds_read_b128 v[210:213], v200 offset:33792
	ds_read_b128 v[214:217], v200 offset:34816
	ds_read_b128 v[218:221], v200 offset:35840
	ds_read_b128 v[222:225], v200 offset:36864
	ds_read_b128 v[226:229], v200 offset:37888
	ds_read_b128 v[230:233], v200 offset:38912
	ds_read_b128 v[234:237], v200 offset:39936
	global_load_lds_dwordx4 v[244:245], off
	v_lshl_add_u64 v[244:245], s[38:39], 0, v[158:159]
	s_mov_b32 m0, s53
	s_nop 0
	global_load_lds_dwordx4 v[244:245], off
	s_waitcnt vmcnt(8)
	s_waitcnt lgkmcnt(0)
	s_barrier
	s_waitcnt lgkmcnt(0)
	v_mfma_i32_16x16x64_i8 v[142:145], v[106:109], v[206:209], v[142:145]
	v_mfma_i32_16x16x64_i8 v[138:141], v[114:117], v[206:209], v[138:141]
	v_mfma_i32_16x16x64_i8 v[122:125], v[106:109], v[214:217], v[122:125]
	v_mfma_i32_16x16x64_i8 v[126:129], v[114:117], v[214:217], v[126:129]
	v_mfma_i32_16x16x64_i8 v[94:97], v[106:109], v[222:225], v[94:97]
	v_mfma_i32_16x16x64_i8 v[90:93], v[114:117], v[222:225], v[90:93]
	v_mfma_i32_16x16x64_i8 v[74:77], v[106:109], v[230:233], v[74:77]
	v_mfma_i32_16x16x64_i8 v[82:85], v[114:117], v[230:233], v[82:85]
	v_mfma_i32_16x16x64_i8 v[142:145], v[110:113], v[210:213], v[142:145]
	v_mfma_i32_16x16x64_i8 v[138:141], v[118:121], v[210:213], v[138:141]
	v_mfma_i32_16x16x64_i8 v[122:125], v[110:113], v[218:221], v[122:125]
	v_mfma_i32_16x16x64_i8 v[126:129], v[118:121], v[218:221], v[126:129]
	v_mfma_i32_16x16x64_i8 v[94:97], v[110:113], v[226:229], v[94:97]
	v_mfma_i32_16x16x64_i8 v[90:93], v[118:121], v[226:229], v[90:93]
	v_mfma_i32_16x16x64_i8 v[74:77], v[110:113], v[234:237], v[74:77]
	v_mfma_i32_16x16x64_i8 v[82:85], v[118:121], v[234:237], v[82:85]
	v_mfma_i32_16x16x64_i8 v[134:137], v[182:185], v[206:209], v[134:137]
	v_mfma_i32_16x16x64_i8 v[130:133], v[190:193], v[206:209], v[130:133]
	v_mfma_i32_16x16x64_i8 v[98:101], v[182:185], v[214:217], v[98:101]
	v_mfma_i32_16x16x64_i8 v[102:105], v[190:193], v[214:217], v[102:105]
	v_mfma_i32_16x16x64_i8 v[86:89], v[182:185], v[222:225], v[86:89]
	v_mfma_i32_16x16x64_i8 v[78:81], v[190:193], v[222:225], v[78:81]
	v_mfma_i32_16x16x64_i8 v[58:61], v[182:185], v[230:233], v[58:61]
	v_mfma_i32_16x16x64_i8 v[70:73], v[190:193], v[230:233], v[70:73]
	v_mfma_i32_16x16x64_i8 v[134:137], v[186:189], v[210:213], v[134:137]
	v_mfma_i32_16x16x64_i8 v[130:133], v[202:205], v[210:213], v[130:133]
	v_mfma_i32_16x16x64_i8 v[98:101], v[186:189], v[218:221], v[98:101]
	v_mfma_i32_16x16x64_i8 v[102:105], v[202:205], v[218:221], v[102:105]
	v_mfma_i32_16x16x64_i8 v[86:89], v[186:189], v[226:229], v[86:89]
	v_mfma_i32_16x16x64_i8 v[78:81], v[202:205], v[226:229], v[78:81]
	v_mfma_i32_16x16x64_i8 v[58:61], v[186:189], v[234:237], v[58:61]
	v_mfma_i32_16x16x64_i8 v[70:73], v[202:205], v[234:237], v[70:73]
	s_barrier
	s_add_i32 s12, s12, s40
	v_lshl_add_u64 v[194:195], v[194:195], 0, s[24:25]
	s_mov_b32 m0, s12
	ds_read_b128 v[206:209], v200 offset:49152
	ds_read_b128 v[210:213], v200 offset:50176
	ds_read_b128 v[214:217], v200 offset:51200
	ds_read_b128 v[218:221], v200 offset:52224
	ds_read_b128 v[222:225], v200 offset:53248
	ds_read_b128 v[226:229], v200 offset:54272
	ds_read_b128 v[230:233], v200 offset:55296
	ds_read_b128 v[234:237], v200 offset:56320
	global_load_lds_dwordx4 v[194:195], off
	s_add_i32 m0, s12, 0x2000
	s_add_u32 s12, s36, 0x40080
	v_lshl_add_u64 v[194:195], v[238:239], 0, s[24:25]
	s_addc_u32 s13, s37, 0
	s_add_i32 s36, s64, s40
	global_load_lds_dwordx4 v[194:195], off
	v_lshl_add_u64 v[194:195], s[12:13], 0, v[148:149]
	s_mov_b32 m0, s36
	s_nop 0
	global_load_lds_dwordx4 v[194:195], off
	v_lshl_add_u64 v[194:195], s[12:13], 0, v[150:151]
	s_add_i32 m0, s36, 0x2000
	s_nop 0
	global_load_lds_dwordx4 v[194:195], off
	v_lshl_add_u64 v[194:195], v[240:241], 0, s[24:25]
	s_mov_b32 m0, s55
	s_nop 0
	global_load_lds_dwordx4 v[194:195], off
	v_lshl_add_u64 v[194:195], v[242:243], 0, s[24:25]
	s_mov_b32 m0, s56
	s_nop 0
	global_load_lds_dwordx4 v[194:195], off
	s_waitcnt vmcnt(8)
	s_waitcnt lgkmcnt(0)
	s_barrier
	s_waitcnt lgkmcnt(0)
	v_mfma_i32_16x16x64_i8 v[54:57], v[106:109], v[206:209], v[54:57]
	v_mfma_i32_16x16x64_i8 v[50:53], v[114:117], v[206:209], v[50:53]
	v_mfma_i32_16x16x64_i8 v[34:37], v[106:109], v[214:217], v[34:37]
	v_mfma_i32_16x16x64_i8 v[38:41], v[114:117], v[214:217], v[38:41]
	v_mfma_i32_16x16x64_i8 v[22:25], v[106:109], v[222:225], v[22:25]
	v_mfma_i32_16x16x64_i8 v[18:21], v[114:117], v[222:225], v[18:21]
	v_mfma_i32_16x16x64_i8 v[2:5], v[106:109], v[230:233], v[2:5]
	v_mfma_i32_16x16x64_i8 v[6:9], v[114:117], v[230:233], v[6:9]
	v_mfma_i32_16x16x64_i8 v[54:57], v[110:113], v[210:213], v[54:57]
	v_mfma_i32_16x16x64_i8 v[50:53], v[118:121], v[210:213], v[50:53]
	v_mfma_i32_16x16x64_i8 v[34:37], v[110:113], v[218:221], v[34:37]
	v_mfma_i32_16x16x64_i8 v[38:41], v[118:121], v[218:221], v[38:41]
	v_mfma_i32_16x16x64_i8 v[22:25], v[110:113], v[226:229], v[22:25]
	v_mfma_i32_16x16x64_i8 v[18:21], v[118:121], v[226:229], v[18:21]
	v_mfma_i32_16x16x64_i8 v[2:5], v[110:113], v[234:237], v[2:5]
	v_mfma_i32_16x16x64_i8 v[6:9], v[118:121], v[234:237], v[6:9]
	v_mfma_i32_16x16x64_i8 v[66:69], v[182:185], v[206:209], v[66:69]
	v_mfma_i32_16x16x64_i8 v[62:65], v[190:193], v[206:209], v[62:65]
	v_mfma_i32_16x16x64_i8 v[42:45], v[182:185], v[214:217], v[42:45]
	v_mfma_i32_16x16x64_i8 v[46:49], v[190:193], v[214:217], v[46:49]
	v_mfma_i32_16x16x64_i8 v[30:33], v[182:185], v[222:225], v[30:33]
	v_mfma_i32_16x16x64_i8 v[26:29], v[190:193], v[222:225], v[26:29]
	v_mfma_i32_16x16x64_i8 v[10:13], v[182:185], v[230:233], v[10:13]
	v_mfma_i32_16x16x64_i8 v[14:17], v[190:193], v[230:233], v[14:17]
	v_mfma_i32_16x16x64_i8 v[66:69], v[186:189], v[210:213], v[66:69]
	v_mfma_i32_16x16x64_i8 v[62:65], v[202:205], v[210:213], v[62:65]
	v_mfma_i32_16x16x64_i8 v[42:45], v[186:189], v[218:221], v[42:45]
	v_mfma_i32_16x16x64_i8 v[46:49], v[202:205], v[218:221], v[46:49]
	v_mfma_i32_16x16x64_i8 v[30:33], v[186:189], v[226:229], v[30:33]
	v_mfma_i32_16x16x64_i8 v[26:29], v[202:205], v[226:229], v[26:29]
	v_mfma_i32_16x16x64_i8 v[10:13], v[186:189], v[234:237], v[10:13]
	v_mfma_i32_16x16x64_i8 v[14:17], v[202:205], v[234:237], v[14:17]
	s_barrier
	s_add_i32 s63, s63, 2
	s_add_u32 s61, s61, 0x100
	s_addc_u32 s62, s62, 0
	s_cmp_gt_u32 s63, 13
	s_mov_b64 s[12:13], s[14:15]
	s_cbranch_scc0 .LBB0_246
	s_branch .Lpk1_exit
.LBB0_246:
	s_waitcnt lgkmcnt(0)
	ds_read_b128 v[106:109], v198
	ds_read_b128 v[110:113], v198 offset:1024
	ds_read_b128 v[114:117], v198 offset:2048
	ds_read_b128 v[118:121], v198 offset:3072
	ds_read_b128 v[182:185], v199
	ds_read_b128 v[186:189], v199 offset:1024
	ds_read_b128 v[190:193], v199 offset:2048
	ds_read_b128 v[202:205], v199 offset:3072
	s_add_u32 s14, s12, 0x100
	s_addc_u32 s15, s13, 0
	s_cmp_eq_u32 s63, 12
	s_cselect_b32 s39, s11, s15
	s_cselect_b32 s38, s19, s14
	s_cselect_b32 s37, s29, s62
	s_cselect_b32 s36, s60, s61
	v_lshl_add_u64 v[194:195], s[12:13], 0, v[172:173]
	s_add_i32 m0, s42, 0xc000
	ds_read_b128 v[206:209], v200
	ds_read_b128 v[210:213], v200 offset:1024
	ds_read_b128 v[214:217], v200 offset:2048
	ds_read_b128 v[218:221], v200 offset:3072
	ds_read_b128 v[222:225], v200 offset:4096
	ds_read_b128 v[226:229], v200 offset:5120
	ds_read_b128 v[230:233], v200 offset:6144
	ds_read_b128 v[234:237], v200 offset:7168
	global_load_lds_dwordx4 v[194:195], off
	v_lshl_add_u64 v[194:195], s[12:13], 0, v[174:175]
	s_add_i32 m0, s42, 0xe000
	s_nop 0
	global_load_lds_dwordx4 v[194:195], off
	s_waitcnt vmcnt(8)
	s_waitcnt lgkmcnt(0)
	s_barrier
	s_waitcnt lgkmcnt(0)
	v_mfma_i32_16x16x64_i8 v[142:145], v[106:109], v[206:209], v[142:145]
	v_mfma_i32_16x16x64_i8 v[138:141], v[114:117], v[206:209], v[138:141]
	v_mfma_i32_16x16x64_i8 v[122:125], v[106:109], v[214:217], v[122:125]
	v_mfma_i32_16x16x64_i8 v[126:129], v[114:117], v[214:217], v[126:129]
	v_mfma_i32_16x16x64_i8 v[94:97], v[106:109], v[222:225], v[94:97]
	v_mfma_i32_16x16x64_i8 v[90:93], v[114:117], v[222:225], v[90:93]
	v_mfma_i32_16x16x64_i8 v[74:77], v[106:109], v[230:233], v[74:77]
	v_mfma_i32_16x16x64_i8 v[82:85], v[114:117], v[230:233], v[82:85]
	v_mfma_i32_16x16x64_i8 v[142:145], v[110:113], v[210:213], v[142:145]
	v_mfma_i32_16x16x64_i8 v[138:141], v[118:121], v[210:213], v[138:141]
	v_mfma_i32_16x16x64_i8 v[122:125], v[110:113], v[218:221], v[122:125]
	v_mfma_i32_16x16x64_i8 v[126:129], v[118:121], v[218:221], v[126:129]
	v_mfma_i32_16x16x64_i8 v[94:97], v[110:113], v[226:229], v[94:97]
	v_mfma_i32_16x16x64_i8 v[90:93], v[118:121], v[226:229], v[90:93]
	v_mfma_i32_16x16x64_i8 v[74:77], v[110:113], v[234:237], v[74:77]
	v_mfma_i32_16x16x64_i8 v[82:85], v[118:121], v[234:237], v[82:85]
	v_mfma_i32_16x16x64_i8 v[134:137], v[182:185], v[206:209], v[134:137]
	v_mfma_i32_16x16x64_i8 v[130:133], v[190:193], v[206:209], v[130:133]
	v_mfma_i32_16x16x64_i8 v[98:101], v[182:185], v[214:217], v[98:101]
	v_mfma_i32_16x16x64_i8 v[102:105], v[190:193], v[214:217], v[102:105]
	v_mfma_i32_16x16x64_i8 v[86:89], v[182:185], v[222:225], v[86:89]
	v_mfma_i32_16x16x64_i8 v[78:81], v[190:193], v[222:225], v[78:81]
	v_mfma_i32_16x16x64_i8 v[58:61], v[182:185], v[230:233], v[58:61]
	v_mfma_i32_16x16x64_i8 v[70:73], v[190:193], v[230:233], v[70:73]
	v_mfma_i32_16x16x64_i8 v[134:137], v[186:189], v[210:213], v[134:137]
	v_mfma_i32_16x16x64_i8 v[130:133], v[202:205], v[210:213], v[130:133]
	v_mfma_i32_16x16x64_i8 v[98:101], v[186:189], v[218:221], v[98:101]
	v_mfma_i32_16x16x64_i8 v[102:105], v[202:205], v[218:221], v[102:105]
	v_mfma_i32_16x16x64_i8 v[86:89], v[186:189], v[226:229], v[86:89]
	v_mfma_i32_16x16x64_i8 v[78:81], v[202:205], v[226:229], v[78:81]
	v_mfma_i32_16x16x64_i8 v[58:61], v[186:189], v[234:237], v[58:61]
	v_mfma_i32_16x16x64_i8 v[70:73], v[202:205], v[234:237], v[70:73]
	s_barrier
	s_add_i32 s12, s17, s40
	v_lshl_add_u64 v[194:195], s[36:37], 0, v[148:149]
	s_mov_b32 m0, s12
	ds_read_b128 v[206:209], v200 offset:16384
	ds_read_b128 v[210:213], v200 offset:17408
	ds_read_b128 v[214:217], v200 offset:18432
	ds_read_b128 v[218:221], v200 offset:19456
	ds_read_b128 v[222:225], v200 offset:20480
	ds_read_b128 v[226:229], v200 offset:21504
	ds_read_b128 v[230:233], v200 offset:22528
	ds_read_b128 v[234:237], v200 offset:23552
	global_load_lds_dwordx4 v[194:195], off
	s_add_i32 m0, s12, 0x2000
	s_add_u32 s12, s36, 0x40000
	v_lshl_add_u64 v[238:239], s[36:37], 0, v[150:151]
	s_addc_u32 s13, s37, 0
	s_add_i32 s64, s57, s40
	global_load_lds_dwordx4 v[238:239], off
	v_lshl_add_u64 v[240:241], s[12:13], 0, v[148:149]
	s_mov_b32 m0, s64
	v_lshl_add_u64 v[242:243], s[38:39], 0, v[154:155]
	global_load_lds_dwordx4 v[240:241], off
	v_lshl_add_u64 v[240:241], s[12:13], 0, v[150:151]
	s_add_i32 m0, s64, 0x2000
	s_nop 0
	global_load_lds_dwordx4 v[240:241], off
	v_lshl_add_u64 v[240:241], s[38:39], 0, v[152:153]
	s_mov_b32 m0, s42
	s_nop 0
	global_load_lds_dwordx4 v[240:241], off
	s_mov_b32 m0, s43
	s_nop 0
	global_load_lds_dwordx4 v[242:243], off
	s_waitcnt vmcnt(8)
	s_waitcnt lgkmcnt(0)
	s_barrier
	s_waitcnt lgkmcnt(0)
	v_mfma_i32_16x16x64_i8 v[54:57], v[106:109], v[206:209], v[54:57]
	v_mfma_i32_16x16x64_i8 v[50:53], v[114:117], v[206:209], v[50:53]
	v_mfma_i32_16x16x64_i8 v[34:37], v[106:109], v[214:217], v[34:37]
	v_mfma_i32_16x16x64_i8 v[38:41], v[114:117], v[214:217], v[38:41]
	v_mfma_i32_16x16x64_i8 v[22:25], v[106:109], v[222:225], v[22:25]
	v_mfma_i32_16x16x64_i8 v[18:21], v[114:117], v[222:225], v[18:21]
	v_mfma_i32_16x16x64_i8 v[2:5], v[106:109], v[230:233], v[2:5]
	v_mfma_i32_16x16x64_i8 v[6:9], v[114:117], v[230:233], v[6:9]
	v_mfma_i32_16x16x64_i8 v[54:57], v[110:113], v[210:213], v[54:57]
	v_mfma_i32_16x16x64_i8 v[50:53], v[118:121], v[210:213], v[50:53]
	v_mfma_i32_16x16x64_i8 v[34:37], v[110:113], v[218:221], v[34:37]
	v_mfma_i32_16x16x64_i8 v[38:41], v[118:121], v[218:221], v[38:41]
	v_mfma_i32_16x16x64_i8 v[22:25], v[110:113], v[226:229], v[22:25]
	v_mfma_i32_16x16x64_i8 v[18:21], v[118:121], v[226:229], v[18:21]
	v_mfma_i32_16x16x64_i8 v[2:5], v[110:113], v[234:237], v[2:5]
	v_mfma_i32_16x16x64_i8 v[6:9], v[118:121], v[234:237], v[6:9]
	v_mfma_i32_16x16x64_i8 v[66:69], v[182:185], v[206:209], v[66:69]
	v_mfma_i32_16x16x64_i8 v[62:65], v[190:193], v[206:209], v[62:65]
	v_mfma_i32_16x16x64_i8 v[42:45], v[182:185], v[214:217], v[42:45]
	v_mfma_i32_16x16x64_i8 v[46:49], v[190:193], v[214:217], v[46:49]
	v_mfma_i32_16x16x64_i8 v[30:33], v[182:185], v[222:225], v[30:33]
	v_mfma_i32_16x16x64_i8 v[26:29], v[190:193], v[222:225], v[26:29]
	v_mfma_i32_16x16x64_i8 v[10:13], v[182:185], v[230:233], v[10:13]
	v_mfma_i32_16x16x64_i8 v[14:17], v[190:193], v[230:233], v[14:17]
	v_mfma_i32_16x16x64_i8 v[66:69], v[186:189], v[210:213], v[66:69]
	v_mfma_i32_16x16x64_i8 v[62:65], v[202:205], v[210:213], v[62:65]
	v_mfma_i32_16x16x64_i8 v[42:45], v[186:189], v[218:221], v[42:45]
	v_mfma_i32_16x16x64_i8 v[46:49], v[202:205], v[218:221], v[46:49]
	v_mfma_i32_16x16x64_i8 v[30:33], v[186:189], v[226:229], v[30:33]
	v_mfma_i32_16x16x64_i8 v[26:29], v[202:205], v[226:229], v[26:29]
	v_mfma_i32_16x16x64_i8 v[10:13], v[186:189], v[234:237], v[10:13]
	v_mfma_i32_16x16x64_i8 v[14:17], v[202:205], v[234:237], v[14:17]
	s_barrier
	s_add_i32 s12, 0, 0x18000
	s_add_i32 s64, 0, 0x1c000
	v_add_u32_e32 v118, s12, v196
	v_add_u32_e32 v146, s64, v196
	ds_read_b128 v[106:109], v118
	ds_read_b128 v[110:113], v118 offset:1024
	ds_read_b128 v[114:117], v118 offset:2048
	ds_read_b128 v[118:121], v118 offset:3072
	ds_read_b128 v[182:185], v146
	ds_read_b128 v[186:189], v146 offset:1024
	ds_read_b128 v[190:193], v146 offset:2048
	ds_read_b128 v[202:205], v146 offset:3072
	s_mov_b32 m0, s52
	v_lshl_add_u64 v[244:245], s[38:39], 0, v[156:157]
	ds_read_b128 v[206:209], v200 offset:32768
	ds_read_b128 v[210:213], v200 offset:33792
	ds_read_b128 v[214:217], v200 offset:34816
	ds_read_b128 v[218:221], v200 offset:35840
	ds_read_b128 v[222:225], v200 offset:36864
	ds_read_b128 v[226:229], v200 offset:37888
	ds_read_b128 v[230:233], v200 offset:38912
	ds_read_b128 v[234:237], v200 offset:39936
	global_load_lds_dwordx4 v[244:245], off
	v_lshl_add_u64 v[244:245], s[38:39], 0, v[158:159]
	s_mov_b32 m0, s53
	s_nop 0
	global_load_lds_dwordx4 v[244:245], off
	s_waitcnt vmcnt(8)
	s_waitcnt lgkmcnt(0)
	s_barrier
	s_waitcnt lgkmcnt(0)
	v_mfma_i32_16x16x64_i8 v[142:145], v[106:109], v[206:209], v[142:145]
	v_mfma_i32_16x16x64_i8 v[138:141], v[114:117], v[206:209], v[138:141]
	v_mfma_i32_16x16x64_i8 v[122:125], v[106:109], v[214:217], v[122:125]
	v_mfma_i32_16x16x64_i8 v[126:129], v[114:117], v[214:217], v[126:129]
	v_mfma_i32_16x16x64_i8 v[94:97], v[106:109], v[222:225], v[94:97]
	v_mfma_i32_16x16x64_i8 v[90:93], v[114:117], v[222:225], v[90:93]
	v_mfma_i32_16x16x64_i8 v[74:77], v[106:109], v[230:233], v[74:77]
	v_mfma_i32_16x16x64_i8 v[82:85], v[114:117], v[230:233], v[82:85]
	v_mfma_i32_16x16x64_i8 v[142:145], v[110:113], v[210:213], v[142:145]
	v_mfma_i32_16x16x64_i8 v[138:141], v[118:121], v[210:213], v[138:141]
	v_mfma_i32_16x16x64_i8 v[122:125], v[110:113], v[218:221], v[122:125]
	v_mfma_i32_16x16x64_i8 v[126:129], v[118:121], v[218:221], v[126:129]
	v_mfma_i32_16x16x64_i8 v[94:97], v[110:113], v[226:229], v[94:97]
	v_mfma_i32_16x16x64_i8 v[90:93], v[118:121], v[226:229], v[90:93]
	v_mfma_i32_16x16x64_i8 v[74:77], v[110:113], v[234:237], v[74:77]
	v_mfma_i32_16x16x64_i8 v[82:85], v[118:121], v[234:237], v[82:85]
	v_mfma_i32_16x16x64_i8 v[134:137], v[182:185], v[206:209], v[134:137]
	v_mfma_i32_16x16x64_i8 v[130:133], v[190:193], v[206:209], v[130:133]
	v_mfma_i32_16x16x64_i8 v[98:101], v[182:185], v[214:217], v[98:101]
	v_mfma_i32_16x16x64_i8 v[102:105], v[190:193], v[214:217], v[102:105]
	v_mfma_i32_16x16x64_i8 v[86:89], v[182:185], v[222:225], v[86:89]
	v_mfma_i32_16x16x64_i8 v[78:81], v[190:193], v[222:225], v[78:81]
	v_mfma_i32_16x16x64_i8 v[58:61], v[182:185], v[230:233], v[58:61]
	v_mfma_i32_16x16x64_i8 v[70:73], v[190:193], v[230:233], v[70:73]
	v_mfma_i32_16x16x64_i8 v[134:137], v[186:189], v[210:213], v[134:137]
	v_mfma_i32_16x16x64_i8 v[130:133], v[202:205], v[210:213], v[130:133]
	v_mfma_i32_16x16x64_i8 v[98:101], v[186:189], v[218:221], v[98:101]
	v_mfma_i32_16x16x64_i8 v[102:105], v[202:205], v[218:221], v[102:105]
	v_mfma_i32_16x16x64_i8 v[86:89], v[186:189], v[226:229], v[86:89]
	v_mfma_i32_16x16x64_i8 v[78:81], v[202:205], v[226:229], v[78:81]
	v_mfma_i32_16x16x64_i8 v[58:61], v[186:189], v[234:237], v[58:61]
	v_mfma_i32_16x16x64_i8 v[70:73], v[202:205], v[234:237], v[70:73]
	s_barrier
	s_add_i32 s12, s12, s40
	v_lshl_add_u64 v[194:195], v[194:195], 0, s[24:25]
	s_mov_b32 m0, s12
	ds_read_b128 v[206:209], v200 offset:49152
	ds_read_b128 v[210:213], v200 offset:50176
	ds_read_b128 v[214:217], v200 offset:51200
	ds_read_b128 v[218:221], v200 offset:52224
	ds_read_b128 v[222:225], v200 offset:53248
	ds_read_b128 v[226:229], v200 offset:54272
	ds_read_b128 v[230:233], v200 offset:55296
	ds_read_b128 v[234:237], v200 offset:56320
	global_load_lds_dwordx4 v[194:195], off
	s_add_i32 m0, s12, 0x2000
	s_add_u32 s12, s36, 0x40080
	v_lshl_add_u64 v[194:195], v[238:239], 0, s[24:25]
	s_addc_u32 s13, s37, 0
	s_add_i32 s36, s64, s40
	global_load_lds_dwordx4 v[194:195], off
	v_lshl_add_u64 v[194:195], s[12:13], 0, v[148:149]
	s_mov_b32 m0, s36
	s_nop 0
	global_load_lds_dwordx4 v[194:195], off
	v_lshl_add_u64 v[194:195], s[12:13], 0, v[150:151]
	s_add_i32 m0, s36, 0x2000
	s_nop 0
	global_load_lds_dwordx4 v[194:195], off
	v_lshl_add_u64 v[194:195], v[240:241], 0, s[24:25]
	s_mov_b32 m0, s55
	s_nop 0
	global_load_lds_dwordx4 v[194:195], off
	v_lshl_add_u64 v[194:195], v[242:243], 0, s[24:25]
	s_mov_b32 m0, s56
	s_nop 0
	global_load_lds_dwordx4 v[194:195], off
	s_waitcnt vmcnt(8)
	s_waitcnt lgkmcnt(0)
	s_barrier
	s_waitcnt lgkmcnt(0)
	v_mfma_i32_16x16x64_i8 v[54:57], v[106:109], v[206:209], v[54:57]
	v_mfma_i32_16x16x64_i8 v[50:53], v[114:117], v[206:209], v[50:53]
	v_mfma_i32_16x16x64_i8 v[34:37], v[106:109], v[214:217], v[34:37]
	v_mfma_i32_16x16x64_i8 v[38:41], v[114:117], v[214:217], v[38:41]
	v_mfma_i32_16x16x64_i8 v[22:25], v[106:109], v[222:225], v[22:25]
	v_mfma_i32_16x16x64_i8 v[18:21], v[114:117], v[222:225], v[18:21]
	v_mfma_i32_16x16x64_i8 v[2:5], v[106:109], v[230:233], v[2:5]
	v_mfma_i32_16x16x64_i8 v[6:9], v[114:117], v[230:233], v[6:9]
	v_mfma_i32_16x16x64_i8 v[54:57], v[110:113], v[210:213], v[54:57]
	v_mfma_i32_16x16x64_i8 v[50:53], v[118:121], v[210:213], v[50:53]
	v_mfma_i32_16x16x64_i8 v[34:37], v[110:113], v[218:221], v[34:37]
	v_mfma_i32_16x16x64_i8 v[38:41], v[118:121], v[218:221], v[38:41]
	v_mfma_i32_16x16x64_i8 v[22:25], v[110:113], v[226:229], v[22:25]
	v_mfma_i32_16x16x64_i8 v[18:21], v[118:121], v[226:229], v[18:21]
	v_mfma_i32_16x16x64_i8 v[2:5], v[110:113], v[234:237], v[2:5]
	v_mfma_i32_16x16x64_i8 v[6:9], v[118:121], v[234:237], v[6:9]
	v_mfma_i32_16x16x64_i8 v[66:69], v[182:185], v[206:209], v[66:69]
	v_mfma_i32_16x16x64_i8 v[62:65], v[190:193], v[206:209], v[62:65]
	v_mfma_i32_16x16x64_i8 v[42:45], v[182:185], v[214:217], v[42:45]
	v_mfma_i32_16x16x64_i8 v[46:49], v[190:193], v[214:217], v[46:49]
	v_mfma_i32_16x16x64_i8 v[30:33], v[182:185], v[222:225], v[30:33]
	v_mfma_i32_16x16x64_i8 v[26:29], v[190:193], v[222:225], v[26:29]
	v_mfma_i32_16x16x64_i8 v[10:13], v[182:185], v[230:233], v[10:13]
	v_mfma_i32_16x16x64_i8 v[14:17], v[190:193], v[230:233], v[14:17]
	v_mfma_i32_16x16x64_i8 v[66:69], v[186:189], v[210:213], v[66:69]
	v_mfma_i32_16x16x64_i8 v[62:65], v[202:205], v[210:213], v[62:65]
	v_mfma_i32_16x16x64_i8 v[42:45], v[186:189], v[218:221], v[42:45]
	v_mfma_i32_16x16x64_i8 v[46:49], v[202:205], v[218:221], v[46:49]
	v_mfma_i32_16x16x64_i8 v[30:33], v[186:189], v[226:229], v[30:33]
	v_mfma_i32_16x16x64_i8 v[26:29], v[202:205], v[226:229], v[26:29]
	v_mfma_i32_16x16x64_i8 v[10:13], v[186:189], v[234:237], v[10:13]
	v_mfma_i32_16x16x64_i8 v[14:17], v[202:205], v[234:237], v[14:17]
	s_barrier
	s_add_i32 s63, s63, 2
	s_add_u32 s61, s61, 0x100
	s_addc_u32 s62, s62, 0
	s_cmp_gt_u32 s63, 13
	s_mov_b64 s[12:13], s[14:15]
	s_cbranch_scc0 .LBB0_246

.Lpk2_entry:
	ds_read_b128 v[18:21], v195
	ds_read_b128 v[22:25], v195 offset:1024
	ds_read_b128 v[26:29], v195 offset:2048
	ds_read_b128 v[30:33], v195 offset:3072
	ds_read_b128 v[2:5], v196
	ds_read_b128 v[6:9], v196 offset:1024
	ds_read_b128 v[10:13], v196 offset:2048
	ds_read_b128 v[14:17], v196 offset:3072
	s_add_u32 s28, s30, 0x100
	s_addc_u32 s29, s31, 0
	s_cmp_eq_u32 s57, 4
	s_cselect_b32 s37, s19, s29
	s_cselect_b32 s36, s53, s28
	s_cselect_b32 s35, s21, s56
	s_cselect_b32 s34, s54, s55
	v_lshl_add_u64 v[222:223], s[30:31], 0, v[176:177]
	s_add_i32 m0, s27, 0xc000
	ds_read_b128 v[182:185], v197
	ds_read_b128 v[186:189], v197 offset:1024
	ds_read_b128 v[198:201], v197 offset:2048
	ds_read_b128 v[202:205], v197 offset:3072
	ds_read_b128 v[206:209], v197 offset:4096
	ds_read_b128 v[210:213], v197 offset:5120
	ds_read_b128 v[214:217], v197 offset:6144
	ds_read_b128 v[218:221], v197 offset:7168
	global_load_lds_dwordx4 v[222:223], off
	v_lshl_add_u64 v[222:223], s[30:31], 0, v[178:179]
	s_add_i32 m0, s27, 0xe000
	s_nop 0
	global_load_lds_dwordx4 v[222:223], off
	s_waitcnt vmcnt(8)
	s_waitcnt lgkmcnt(0)
	s_barrier
	s_waitcnt lgkmcnt(0)
	v_mfma_f32_16x16x128_f8f6f4 v[158:161], v[18:25], v[182:189], 0
	v_mfma_f32_16x16x128_f8f6f4 v[154:157], v[26:33], v[182:189], 0
	v_mfma_f32_16x16x128_f8f6f4 v[138:141], v[18:25], v[198:205], 0
	v_mfma_f32_16x16x128_f8f6f4 v[142:145], v[26:33], v[198:205], 0
	v_mfma_f32_16x16x128_f8f6f4 v[126:129], v[18:25], v[206:213], 0
	v_mfma_f32_16x16x128_f8f6f4 v[122:125], v[26:33], v[206:213], 0
	v_mfma_f32_16x16x128_f8f6f4 v[106:109], v[18:25], v[214:221], 0
	v_mfma_f32_16x16x128_f8f6f4 v[110:113], v[26:33], v[214:221], 0
	v_mfma_f32_16x16x128_f8f6f4 v[150:153], v[2:9], v[182:189], 0
	v_mfma_f32_16x16x128_f8f6f4 v[146:149], v[10:17], v[182:189], 0
	v_mfma_f32_16x16x128_f8f6f4 v[130:133], v[2:9], v[198:205], 0
	v_mfma_f32_16x16x128_f8f6f4 v[134:137], v[10:17], v[198:205], 0
	v_mfma_f32_16x16x128_f8f6f4 v[118:121], v[2:9], v[206:213], 0
	v_mfma_f32_16x16x128_f8f6f4 v[114:117], v[10:17], v[206:213], 0
	v_mfma_f32_16x16x128_f8f6f4 v[98:101], v[2:9], v[214:221], 0
	v_mfma_f32_16x16x128_f8f6f4 v[102:105], v[10:17], v[214:221], 0
	s_barrier
	s_add_i32 s30, s49, s42
	v_lshl_add_u64 v[182:183], s[34:35], 0, v[162:163]
	s_mov_b32 m0, s30
	ds_read_b128 v[198:201], v197 offset:16384
	ds_read_b128 v[202:205], v197 offset:17408
	ds_read_b128 v[206:209], v197 offset:18432
	ds_read_b128 v[210:213], v197 offset:19456
	ds_read_b128 v[214:217], v197 offset:20480
	ds_read_b128 v[218:221], v197 offset:21504
	ds_read_b128 v[222:225], v197 offset:22528
	ds_read_b128 v[226:229], v197 offset:23552
	global_load_lds_dwordx4 v[182:183], off
	s_add_i32 m0, s30, 0x2000
	s_add_u32 s30, s34, 0x20000
	v_lshl_add_u64 v[184:185], s[34:35], 0, v[164:165]
	s_addc_u32 s31, s35, 0
	s_add_i32 s58, s50, s42
	global_load_lds_dwordx4 v[184:185], off
	v_lshl_add_u64 v[186:187], s[30:31], 0, v[162:163]
	s_mov_b32 m0, s58
	v_lshl_add_u64 v[188:189], s[36:37], 0, v[168:169]
	global_load_lds_dwordx4 v[186:187], off
	v_lshl_add_u64 v[186:187], s[30:31], 0, v[164:165]
	s_add_i32 m0, s58, 0x2000
	s_nop 0
	global_load_lds_dwordx4 v[186:187], off
	v_lshl_add_u64 v[186:187], s[36:37], 0, v[166:167]
	s_mov_b32 m0, s27
	s_nop 0
	global_load_lds_dwordx4 v[186:187], off
	s_mov_b32 m0, s43
	s_nop 0
	global_load_lds_dwordx4 v[188:189], off
	s_waitcnt vmcnt(8)
	s_waitcnt lgkmcnt(0)
	s_barrier
	s_waitcnt lgkmcnt(0)
	v_mfma_f32_16x16x128_f8f6f4 v[86:89], v[18:25], v[198:205], 0
	v_mfma_f32_16x16x128_f8f6f4 v[82:85], v[26:33], v[198:205], 0
	v_mfma_f32_16x16x128_f8f6f4 v[66:69], v[18:25], v[206:213], 0
	v_mfma_f32_16x16x128_f8f6f4 v[70:73], v[26:33], v[206:213], 0
	v_mfma_f32_16x16x128_f8f6f4 v[54:57], v[18:25], v[214:221], 0
	v_mfma_f32_16x16x128_f8f6f4 v[50:53], v[26:33], v[214:221], 0
	v_mfma_f32_16x16x128_f8f6f4 v[34:37], v[18:25], v[222:229], 0
	v_mfma_f32_16x16x128_f8f6f4 v[38:41], v[26:33], v[222:229], 0
	v_mfma_f32_16x16x128_f8f6f4 v[94:97], v[2:9], v[198:205], 0
	v_mfma_f32_16x16x128_f8f6f4 v[90:93], v[10:17], v[198:205], 0
	v_mfma_f32_16x16x128_f8f6f4 v[74:77], v[2:9], v[206:213], 0
	v_mfma_f32_16x16x128_f8f6f4 v[78:81], v[10:17], v[206:213], 0
	v_mfma_f32_16x16x128_f8f6f4 v[62:65], v[2:9], v[214:221], 0
	v_mfma_f32_16x16x128_f8f6f4 v[58:61], v[10:17], v[214:221], 0
	v_mfma_f32_16x16x128_f8f6f4 v[42:45], v[2:9], v[222:229], 0
	v_mfma_f32_16x16x128_f8f6f4 v[46:49], v[10:17], v[222:229], 0
	s_barrier
	s_add_i32 s30, 0, 0x18000
	s_add_i32 s58, 0, 0x1c000
	v_add_u32_e32 v14, s30, v191
	v_add_u32_e32 v30, s58, v191
	ds_read_b128 v[2:5], v14
	ds_read_b128 v[6:9], v14 offset:1024
	ds_read_b128 v[10:13], v14 offset:2048
	ds_read_b128 v[14:17], v14 offset:3072
	ds_read_b128 v[18:21], v30
	ds_read_b128 v[22:25], v30 offset:1024
	ds_read_b128 v[26:29], v30 offset:2048
	ds_read_b128 v[30:33], v30 offset:3072
	s_mov_b32 m0, s44
	v_lshl_add_u64 v[230:231], s[36:37], 0, v[170:171]
	ds_read_b128 v[198:201], v197 offset:32768
	ds_read_b128 v[202:205], v197 offset:33792
	ds_read_b128 v[206:209], v197 offset:34816
	ds_read_b128 v[210:213], v197 offset:35840
	ds_read_b128 v[214:217], v197 offset:36864
	ds_read_b128 v[218:221], v197 offset:37888
	ds_read_b128 v[222:225], v197 offset:38912
	ds_read_b128 v[226:229], v197 offset:39936
	global_load_lds_dwordx4 v[230:231], off
	v_lshl_add_u64 v[230:231], s[36:37], 0, v[172:173]
	s_mov_b32 m0, s45
	s_nop 0
	global_load_lds_dwordx4 v[230:231], off
	s_waitcnt vmcnt(8)
	s_waitcnt lgkmcnt(0)
	s_barrier
	s_waitcnt lgkmcnt(0)
	v_mfma_f32_16x16x128_f8f6f4 v[158:161], v[2:9], v[198:205], v[158:161]
	v_mfma_f32_16x16x128_f8f6f4 v[154:157], v[10:17], v[198:205], v[154:157]
	v_mfma_f32_16x16x128_f8f6f4 v[138:141], v[2:9], v[206:213], v[138:141]
	v_mfma_f32_16x16x128_f8f6f4 v[142:145], v[10:17], v[206:213], v[142:145]
	v_mfma_f32_16x16x128_f8f6f4 v[126:129], v[2:9], v[214:221], v[126:129]
	v_mfma_f32_16x16x128_f8f6f4 v[122:125], v[10:17], v[214:221], v[122:125]
	v_mfma_f32_16x16x128_f8f6f4 v[106:109], v[2:9], v[222:229], v[106:109]
	v_mfma_f32_16x16x128_f8f6f4 v[110:113], v[10:17], v[222:229], v[110:113]
	v_mfma_f32_16x16x128_f8f6f4 v[150:153], v[18:25], v[198:205], v[150:153]
	v_mfma_f32_16x16x128_f8f6f4 v[146:149], v[26:33], v[198:205], v[146:149]
	v_mfma_f32_16x16x128_f8f6f4 v[130:133], v[18:25], v[206:213], v[130:133]
	v_mfma_f32_16x16x128_f8f6f4 v[134:137], v[26:33], v[206:213], v[134:137]
	v_mfma_f32_16x16x128_f8f6f4 v[118:121], v[18:25], v[214:221], v[118:121]
	v_mfma_f32_16x16x128_f8f6f4 v[114:117], v[26:33], v[214:221], v[114:117]
	v_mfma_f32_16x16x128_f8f6f4 v[98:101], v[18:25], v[222:229], v[98:101]
	v_mfma_f32_16x16x128_f8f6f4 v[102:105], v[26:33], v[222:229], v[102:105]
	s_barrier
	s_add_i32 s30, s30, s42
	v_lshl_add_u64 v[182:183], v[182:183], 0, s[10:11]
	s_mov_b32 m0, s30
	ds_read_b128 v[198:201], v197 offset:49152
	ds_read_b128 v[202:205], v197 offset:50176
	ds_read_b128 v[206:209], v197 offset:51200
	ds_read_b128 v[210:213], v197 offset:52224
	ds_read_b128 v[214:217], v197 offset:53248
	ds_read_b128 v[218:221], v197 offset:54272
	ds_read_b128 v[222:225], v197 offset:55296
	ds_read_b128 v[226:229], v197 offset:56320
	global_load_lds_dwordx4 v[182:183], off
	s_add_i32 m0, s30, 0x2000
	s_add_u32 s30, s34, 0x20080
	v_lshl_add_u64 v[182:183], v[184:185], 0, s[10:11]
	s_addc_u32 s31, s35, 0
	s_add_i32 s34, s58, s42
	global_load_lds_dwordx4 v[182:183], off
	v_lshl_add_u64 v[182:183], s[30:31], 0, v[162:163]
	s_mov_b32 m0, s34
	s_nop 0
	global_load_lds_dwordx4 v[182:183], off
	v_lshl_add_u64 v[182:183], s[30:31], 0, v[164:165]
	s_add_i32 m0, s34, 0x2000
	s_nop 0
	global_load_lds_dwordx4 v[182:183], off
	v_lshl_add_u64 v[182:183], v[186:187], 0, s[10:11]
	s_mov_b32 m0, s47
	s_nop 0
	global_load_lds_dwordx4 v[182:183], off
	v_lshl_add_u64 v[182:183], v[188:189], 0, s[10:11]
	s_mov_b32 m0, s48
	s_nop 0
	global_load_lds_dwordx4 v[182:183], off
	s_waitcnt vmcnt(8)
	s_waitcnt lgkmcnt(0)
	s_barrier
	s_waitcnt lgkmcnt(0)
	v_mfma_f32_16x16x128_f8f6f4 v[86:89], v[2:9], v[198:205], v[86:89]
	v_mfma_f32_16x16x128_f8f6f4 v[82:85], v[10:17], v[198:205], v[82:85]
	v_mfma_f32_16x16x128_f8f6f4 v[66:69], v[2:9], v[206:213], v[66:69]
	v_mfma_f32_16x16x128_f8f6f4 v[70:73], v[10:17], v[206:213], v[70:73]
	v_mfma_f32_16x16x128_f8f6f4 v[54:57], v[2:9], v[214:221], v[54:57]
	v_mfma_f32_16x16x128_f8f6f4 v[50:53], v[10:17], v[214:221], v[50:53]
	v_mfma_f32_16x16x128_f8f6f4 v[34:37], v[2:9], v[222:229], v[34:37]
	v_mfma_f32_16x16x128_f8f6f4 v[38:41], v[10:17], v[222:229], v[38:41]
	v_mfma_f32_16x16x128_f8f6f4 v[94:97], v[18:25], v[198:205], v[94:97]
	v_mfma_f32_16x16x128_f8f6f4 v[90:93], v[26:33], v[198:205], v[90:93]
	v_mfma_f32_16x16x128_f8f6f4 v[74:77], v[18:25], v[206:213], v[74:77]
	v_mfma_f32_16x16x128_f8f6f4 v[78:81], v[26:33], v[206:213], v[78:81]
	v_mfma_f32_16x16x128_f8f6f4 v[62:65], v[18:25], v[214:221], v[62:65]
	v_mfma_f32_16x16x128_f8f6f4 v[58:61], v[26:33], v[214:221], v[58:61]
	v_mfma_f32_16x16x128_f8f6f4 v[42:45], v[18:25], v[222:229], v[42:45]
	v_mfma_f32_16x16x128_f8f6f4 v[46:49], v[26:33], v[222:229], v[46:49]
	s_barrier
	s_add_i32 s57, s57, 2
	s_add_u32 s55, s55, 0x100
	s_addc_u32 s56, s56, 0
	s_cmp_gt_u32 s57, 5
	s_mov_b64 s[30:31], s[28:29]
	s_cbranch_scc0 .LBB0_530
	s_branch .Lpk2_exit
.LBB0_530:
	ds_read_b128 v[18:21], v195
	ds_read_b128 v[22:25], v195 offset:1024
	ds_read_b128 v[26:29], v195 offset:2048
	ds_read_b128 v[30:33], v195 offset:3072
	ds_read_b128 v[2:5], v196
	ds_read_b128 v[6:9], v196 offset:1024
	ds_read_b128 v[10:13], v196 offset:2048
	ds_read_b128 v[14:17], v196 offset:3072
	s_add_u32 s28, s30, 0x100
	s_addc_u32 s29, s31, 0
	s_cmp_eq_u32 s57, 4
	s_cselect_b32 s37, s19, s29
	s_cselect_b32 s36, s53, s28
	s_cselect_b32 s35, s21, s56
	s_cselect_b32 s34, s54, s55
	v_lshl_add_u64 v[222:223], s[30:31], 0, v[176:177]
	s_add_i32 m0, s27, 0xc000
	ds_read_b128 v[182:185], v197
	ds_read_b128 v[186:189], v197 offset:1024
	ds_read_b128 v[198:201], v197 offset:2048
	ds_read_b128 v[202:205], v197 offset:3072
	ds_read_b128 v[206:209], v197 offset:4096
	ds_read_b128 v[210:213], v197 offset:5120
	ds_read_b128 v[214:217], v197 offset:6144
	ds_read_b128 v[218:221], v197 offset:7168
	global_load_lds_dwordx4 v[222:223], off
	v_lshl_add_u64 v[222:223], s[30:31], 0, v[178:179]
	s_add_i32 m0, s27, 0xe000
	s_nop 0
	global_load_lds_dwordx4 v[222:223], off
	s_waitcnt vmcnt(8)
	s_waitcnt lgkmcnt(0)
	s_barrier
	s_waitcnt lgkmcnt(0)
	v_mfma_f32_16x16x128_f8f6f4 v[158:161], v[18:25], v[182:189], v[158:161]
	v_mfma_f32_16x16x128_f8f6f4 v[154:157], v[26:33], v[182:189], v[154:157]
	v_mfma_f32_16x16x128_f8f6f4 v[138:141], v[18:25], v[198:205], v[138:141]
	v_mfma_f32_16x16x128_f8f6f4 v[142:145], v[26:33], v[198:205], v[142:145]
	v_mfma_f32_16x16x128_f8f6f4 v[126:129], v[18:25], v[206:213], v[126:129]
	v_mfma_f32_16x16x128_f8f6f4 v[122:125], v[26:33], v[206:213], v[122:125]
	v_mfma_f32_16x16x128_f8f6f4 v[106:109], v[18:25], v[214:221], v[106:109]
	v_mfma_f32_16x16x128_f8f6f4 v[110:113], v[26:33], v[214:221], v[110:113]
	v_mfma_f32_16x16x128_f8f6f4 v[150:153], v[2:9], v[182:189], v[150:153]
	v_mfma_f32_16x16x128_f8f6f4 v[146:149], v[10:17], v[182:189], v[146:149]
	v_mfma_f32_16x16x128_f8f6f4 v[130:133], v[2:9], v[198:205], v[130:133]
	v_mfma_f32_16x16x128_f8f6f4 v[134:137], v[10:17], v[198:205], v[134:137]
	v_mfma_f32_16x16x128_f8f6f4 v[118:121], v[2:9], v[206:213], v[118:121]
	v_mfma_f32_16x16x128_f8f6f4 v[114:117], v[10:17], v[206:213], v[114:117]
	v_mfma_f32_16x16x128_f8f6f4 v[98:101], v[2:9], v[214:221], v[98:101]
	v_mfma_f32_16x16x128_f8f6f4 v[102:105], v[10:17], v[214:221], v[102:105]
	s_barrier
	s_add_i32 s30, s49, s42
	v_lshl_add_u64 v[182:183], s[34:35], 0, v[162:163]
	s_mov_b32 m0, s30
	ds_read_b128 v[198:201], v197 offset:16384
	ds_read_b128 v[202:205], v197 offset:17408
	ds_read_b128 v[206:209], v197 offset:18432
	ds_read_b128 v[210:213], v197 offset:19456
	ds_read_b128 v[214:217], v197 offset:20480
	ds_read_b128 v[218:221], v197 offset:21504
	ds_read_b128 v[222:225], v197 offset:22528
	ds_read_b128 v[226:229], v197 offset:23552
	global_load_lds_dwordx4 v[182:183], off
	s_add_i32 m0, s30, 0x2000
	s_add_u32 s30, s34, 0x20000
	v_lshl_add_u64 v[184:185], s[34:35], 0, v[164:165]
	s_addc_u32 s31, s35, 0
	s_add_i32 s58, s50, s42
	global_load_lds_dwordx4 v[184:185], off
	v_lshl_add_u64 v[186:187], s[30:31], 0, v[162:163]
	s_mov_b32 m0, s58
	v_lshl_add_u64 v[188:189], s[36:37], 0, v[168:169]
	global_load_lds_dwordx4 v[186:187], off
	v_lshl_add_u64 v[186:187], s[30:31], 0, v[164:165]
	s_add_i32 m0, s58, 0x2000
	s_nop 0
	global_load_lds_dwordx4 v[186:187], off
	v_lshl_add_u64 v[186:187], s[36:37], 0, v[166:167]
	s_mov_b32 m0, s27
	s_nop 0
	global_load_lds_dwordx4 v[186:187], off
	s_mov_b32 m0, s43
	s_nop 0
	global_load_lds_dwordx4 v[188:189], off
	s_waitcnt vmcnt(8)
	s_waitcnt lgkmcnt(0)
	s_barrier
	s_waitcnt lgkmcnt(0)
	v_mfma_f32_16x16x128_f8f6f4 v[86:89], v[18:25], v[198:205], v[86:89]
	v_mfma_f32_16x16x128_f8f6f4 v[82:85], v[26:33], v[198:205], v[82:85]
	v_mfma_f32_16x16x128_f8f6f4 v[66:69], v[18:25], v[206:213], v[66:69]
	v_mfma_f32_16x16x128_f8f6f4 v[70:73], v[26:33], v[206:213], v[70:73]
	v_mfma_f32_16x16x128_f8f6f4 v[54:57], v[18:25], v[214:221], v[54:57]
	v_mfma_f32_16x16x128_f8f6f4 v[50:53], v[26:33], v[214:221], v[50:53]
	v_mfma_f32_16x16x128_f8f6f4 v[34:37], v[18:25], v[222:229], v[34:37]
	v_mfma_f32_16x16x128_f8f6f4 v[38:41], v[26:33], v[222:229], v[38:41]
	v_mfma_f32_16x16x128_f8f6f4 v[94:97], v[2:9], v[198:205], v[94:97]
	v_mfma_f32_16x16x128_f8f6f4 v[90:93], v[10:17], v[198:205], v[90:93]
	v_mfma_f32_16x16x128_f8f6f4 v[74:77], v[2:9], v[206:213], v[74:77]
	v_mfma_f32_16x16x128_f8f6f4 v[78:81], v[10:17], v[206:213], v[78:81]
	v_mfma_f32_16x16x128_f8f6f4 v[62:65], v[2:9], v[214:221], v[62:65]
	v_mfma_f32_16x16x128_f8f6f4 v[58:61], v[10:17], v[214:221], v[58:61]
	v_mfma_f32_16x16x128_f8f6f4 v[42:45], v[2:9], v[222:229], v[42:45]
	v_mfma_f32_16x16x128_f8f6f4 v[46:49], v[10:17], v[222:229], v[46:49]
	s_barrier
	s_add_i32 s30, 0, 0x18000
	s_add_i32 s58, 0, 0x1c000
	v_add_u32_e32 v14, s30, v191
	v_add_u32_e32 v30, s58, v191
	ds_read_b128 v[2:5], v14
	ds_read_b128 v[6:9], v14 offset:1024
	ds_read_b128 v[10:13], v14 offset:2048
	ds_read_b128 v[14:17], v14 offset:3072
	ds_read_b128 v[18:21], v30
	ds_read_b128 v[22:25], v30 offset:1024
	ds_read_b128 v[26:29], v30 offset:2048
	ds_read_b128 v[30:33], v30 offset:3072
	s_mov_b32 m0, s44
	v_lshl_add_u64 v[230:231], s[36:37], 0, v[170:171]
	ds_read_b128 v[198:201], v197 offset:32768
	ds_read_b128 v[202:205], v197 offset:33792
	ds_read_b128 v[206:209], v197 offset:34816
	ds_read_b128 v[210:213], v197 offset:35840
	ds_read_b128 v[214:217], v197 offset:36864
	ds_read_b128 v[218:221], v197 offset:37888
	ds_read_b128 v[222:225], v197 offset:38912
	ds_read_b128 v[226:229], v197 offset:39936
	global_load_lds_dwordx4 v[230:231], off
	v_lshl_add_u64 v[230:231], s[36:37], 0, v[172:173]
	s_mov_b32 m0, s45
	s_nop 0
	global_load_lds_dwordx4 v[230:231], off
	s_waitcnt vmcnt(8)
	s_waitcnt lgkmcnt(0)
	s_barrier
	s_waitcnt lgkmcnt(0)
	v_mfma_f32_16x16x128_f8f6f4 v[158:161], v[2:9], v[198:205], v[158:161]
	v_mfma_f32_16x16x128_f8f6f4 v[154:157], v[10:17], v[198:205], v[154:157]
	v_mfma_f32_16x16x128_f8f6f4 v[138:141], v[2:9], v[206:213], v[138:141]
	v_mfma_f32_16x16x128_f8f6f4 v[142:145], v[10:17], v[206:213], v[142:145]
	v_mfma_f32_16x16x128_f8f6f4 v[126:129], v[2:9], v[214:221], v[126:129]
	v_mfma_f32_16x16x128_f8f6f4 v[122:125], v[10:17], v[214:221], v[122:125]
	v_mfma_f32_16x16x128_f8f6f4 v[106:109], v[2:9], v[222:229], v[106:109]
	v_mfma_f32_16x16x128_f8f6f4 v[110:113], v[10:17], v[222:229], v[110:113]
	v_mfma_f32_16x16x128_f8f6f4 v[150:153], v[18:25], v[198:205], v[150:153]
	v_mfma_f32_16x16x128_f8f6f4 v[146:149], v[26:33], v[198:205], v[146:149]
	v_mfma_f32_16x16x128_f8f6f4 v[130:133], v[18:25], v[206:213], v[130:133]
	v_mfma_f32_16x16x128_f8f6f4 v[134:137], v[26:33], v[206:213], v[134:137]
	v_mfma_f32_16x16x128_f8f6f4 v[118:121], v[18:25], v[214:221], v[118:121]
	v_mfma_f32_16x16x128_f8f6f4 v[114:117], v[26:33], v[214:221], v[114:117]
	v_mfma_f32_16x16x128_f8f6f4 v[98:101], v[18:25], v[222:229], v[98:101]
	v_mfma_f32_16x16x128_f8f6f4 v[102:105], v[26:33], v[222:229], v[102:105]
	s_barrier
	s_add_i32 s30, s30, s42
	v_lshl_add_u64 v[182:183], v[182:183], 0, s[10:11]
	s_mov_b32 m0, s30
	ds_read_b128 v[198:201], v197 offset:49152
	ds_read_b128 v[202:205], v197 offset:50176
	ds_read_b128 v[206:209], v197 offset:51200
	ds_read_b128 v[210:213], v197 offset:52224
	ds_read_b128 v[214:217], v197 offset:53248
	ds_read_b128 v[218:221], v197 offset:54272
	ds_read_b128 v[222:225], v197 offset:55296
	ds_read_b128 v[226:229], v197 offset:56320
	global_load_lds_dwordx4 v[182:183], off
	s_add_i32 m0, s30, 0x2000
	s_add_u32 s30, s34, 0x20080
	v_lshl_add_u64 v[182:183], v[184:185], 0, s[10:11]
	s_addc_u32 s31, s35, 0
	s_add_i32 s34, s58, s42
	global_load_lds_dwordx4 v[182:183], off
	v_lshl_add_u64 v[182:183], s[30:31], 0, v[162:163]
	s_mov_b32 m0, s34
	s_nop 0
	global_load_lds_dwordx4 v[182:183], off
	v_lshl_add_u64 v[182:183], s[30:31], 0, v[164:165]
	s_add_i32 m0, s34, 0x2000
	s_nop 0
	global_load_lds_dwordx4 v[182:183], off
	v_lshl_add_u64 v[182:183], v[186:187], 0, s[10:11]
	s_mov_b32 m0, s47
	s_nop 0
	global_load_lds_dwordx4 v[182:183], off
	v_lshl_add_u64 v[182:183], v[188:189], 0, s[10:11]
	s_mov_b32 m0, s48
	s_nop 0
	global_load_lds_dwordx4 v[182:183], off
	s_waitcnt vmcnt(8)
	s_waitcnt lgkmcnt(0)
	s_barrier
	s_waitcnt lgkmcnt(0)
	v_mfma_f32_16x16x128_f8f6f4 v[86:89], v[2:9], v[198:205], v[86:89]
	v_mfma_f32_16x16x128_f8f6f4 v[82:85], v[10:17], v[198:205], v[82:85]
	v_mfma_f32_16x16x128_f8f6f4 v[66:69], v[2:9], v[206:213], v[66:69]
	v_mfma_f32_16x16x128_f8f6f4 v[70:73], v[10:17], v[206:213], v[70:73]
	v_mfma_f32_16x16x128_f8f6f4 v[54:57], v[2:9], v[214:221], v[54:57]
	v_mfma_f32_16x16x128_f8f6f4 v[50:53], v[10:17], v[214:221], v[50:53]
	v_mfma_f32_16x16x128_f8f6f4 v[34:37], v[2:9], v[222:229], v[34:37]
	v_mfma_f32_16x16x128_f8f6f4 v[38:41], v[10:17], v[222:229], v[38:41]
	v_mfma_f32_16x16x128_f8f6f4 v[94:97], v[18:25], v[198:205], v[94:97]
	v_mfma_f32_16x16x128_f8f6f4 v[90:93], v[26:33], v[198:205], v[90:93]
	v_mfma_f32_16x16x128_f8f6f4 v[74:77], v[18:25], v[206:213], v[74:77]
	v_mfma_f32_16x16x128_f8f6f4 v[78:81], v[26:33], v[206:213], v[78:81]
	v_mfma_f32_16x16x128_f8f6f4 v[62:65], v[18:25], v[214:221], v[62:65]
	v_mfma_f32_16x16x128_f8f6f4 v[58:61], v[26:33], v[214:221], v[58:61]
	v_mfma_f32_16x16x128_f8f6f4 v[42:45], v[18:25], v[222:229], v[42:45]
	v_mfma_f32_16x16x128_f8f6f4 v[46:49], v[26:33], v[222:229], v[46:49]
	s_barrier
	s_add_i32 s57, s57, 2
	s_add_u32 s55, s55, 0x100
	s_addc_u32 s56, s56, 0
	s_cmp_gt_u32 s57, 5
	s_mov_b64 s[30:31], s[28:29]
	s_cbranch_scc0 .LBB0_530

.Lpk3_entry:
	ds_read_b128 v[18:21], v197
	ds_read_b128 v[22:25], v197 offset:1024
	ds_read_b128 v[26:29], v197 offset:2048
	ds_read_b128 v[30:33], v197 offset:3072
	ds_read_b128 v[2:5], v198
	ds_read_b128 v[6:9], v198 offset:1024
	ds_read_b128 v[10:13], v198 offset:2048
	ds_read_b128 v[14:17], v198 offset:3072
	s_add_u32 s30, s28, 0x100
	s_addc_u32 s31, s29, 0
	s_cmp_eq_u32 s57, 4
	s_cselect_b32 s37, s19, s31
	s_cselect_b32 s36, s53, s30
	s_cselect_b32 s35, s21, s56
	s_cselect_b32 s34, s54, s55
	v_lshl_add_u64 v[224:225], s[28:29], 0, v[176:177]
	s_add_i32 m0, s27, 0xc000
	ds_read_b128 v[184:187], v199
	ds_read_b128 v[188:191], v199 offset:1024
	ds_read_b128 v[200:203], v199 offset:2048
	ds_read_b128 v[204:207], v199 offset:3072
	ds_read_b128 v[208:211], v199 offset:4096
	ds_read_b128 v[212:215], v199 offset:5120
	ds_read_b128 v[216:219], v199 offset:6144
	ds_read_b128 v[220:223], v199 offset:7168
	global_load_lds_dwordx4 v[224:225], off
	v_lshl_add_u64 v[224:225], s[28:29], 0, v[178:179]
	s_add_i32 m0, s27, 0xe000
	s_nop 0
	global_load_lds_dwordx4 v[224:225], off
	s_waitcnt vmcnt(8)
	s_waitcnt lgkmcnt(0)
	s_barrier
	s_waitcnt lgkmcnt(0)
	v_mfma_f32_16x16x128_f8f6f4 v[158:161], v[18:25], v[184:191], 0
	v_mfma_f32_16x16x128_f8f6f4 v[154:157], v[26:33], v[184:191], 0
	v_mfma_f32_16x16x128_f8f6f4 v[138:141], v[18:25], v[200:207], 0
	v_mfma_f32_16x16x128_f8f6f4 v[142:145], v[26:33], v[200:207], 0
	v_mfma_f32_16x16x128_f8f6f4 v[126:129], v[18:25], v[208:215], 0
	v_mfma_f32_16x16x128_f8f6f4 v[122:125], v[26:33], v[208:215], 0
	v_mfma_f32_16x16x128_f8f6f4 v[106:109], v[18:25], v[216:223], 0
	v_mfma_f32_16x16x128_f8f6f4 v[110:113], v[26:33], v[216:223], 0
	v_mfma_f32_16x16x128_f8f6f4 v[150:153], v[2:9], v[184:191], 0
	v_mfma_f32_16x16x128_f8f6f4 v[146:149], v[10:17], v[184:191], 0
	v_mfma_f32_16x16x128_f8f6f4 v[130:133], v[2:9], v[200:207], 0
	v_mfma_f32_16x16x128_f8f6f4 v[134:137], v[10:17], v[200:207], 0
	v_mfma_f32_16x16x128_f8f6f4 v[118:121], v[2:9], v[208:215], 0
	v_mfma_f32_16x16x128_f8f6f4 v[114:117], v[10:17], v[208:215], 0
	v_mfma_f32_16x16x128_f8f6f4 v[98:101], v[2:9], v[216:223], 0
	v_mfma_f32_16x16x128_f8f6f4 v[102:105], v[10:17], v[216:223], 0
	s_barrier
	s_add_i32 s28, s49, s42
	v_lshl_add_u64 v[184:185], s[34:35], 0, v[162:163]
	s_mov_b32 m0, s28
	ds_read_b128 v[200:203], v199 offset:16384
	ds_read_b128 v[204:207], v199 offset:17408
	ds_read_b128 v[208:211], v199 offset:18432
	ds_read_b128 v[212:215], v199 offset:19456
	ds_read_b128 v[216:219], v199 offset:20480
	ds_read_b128 v[220:223], v199 offset:21504
	ds_read_b128 v[224:227], v199 offset:22528
	ds_read_b128 v[228:231], v199 offset:23552
	global_load_lds_dwordx4 v[184:185], off
	s_add_i32 m0, s28, 0x2000
	s_add_u32 s28, s34, 0x20000
	v_lshl_add_u64 v[186:187], s[34:35], 0, v[164:165]
	s_addc_u32 s29, s35, 0
	s_add_i32 s58, s50, s42
	global_load_lds_dwordx4 v[186:187], off
	v_lshl_add_u64 v[188:189], s[28:29], 0, v[162:163]
	s_mov_b32 m0, s58
	v_lshl_add_u64 v[190:191], s[36:37], 0, v[168:169]
	global_load_lds_dwordx4 v[188:189], off
	v_lshl_add_u64 v[188:189], s[28:29], 0, v[164:165]
	s_add_i32 m0, s58, 0x2000
	s_nop 0
	global_load_lds_dwordx4 v[188:189], off
	v_lshl_add_u64 v[188:189], s[36:37], 0, v[166:167]
	s_mov_b32 m0, s27
	s_nop 0
	global_load_lds_dwordx4 v[188:189], off
	s_mov_b32 m0, s43
	s_nop 0
	global_load_lds_dwordx4 v[190:191], off
	s_waitcnt vmcnt(8)
	s_waitcnt lgkmcnt(0)
	s_barrier
	s_waitcnt lgkmcnt(0)
	v_mfma_f32_16x16x128_f8f6f4 v[94:97], v[18:25], v[200:207], 0
	v_mfma_f32_16x16x128_f8f6f4 v[90:93], v[26:33], v[200:207], 0
	v_mfma_f32_16x16x128_f8f6f4 v[70:73], v[18:25], v[208:215], 0
	v_mfma_f32_16x16x128_f8f6f4 v[78:81], v[26:33], v[208:215], 0
	v_mfma_f32_16x16x128_f8f6f4 v[54:57], v[18:25], v[216:223], 0
	v_mfma_f32_16x16x128_f8f6f4 v[50:53], v[26:33], v[216:223], 0
	v_mfma_f32_16x16x128_f8f6f4 v[38:41], v[18:25], v[224:231], 0
	v_mfma_f32_16x16x128_f8f6f4 v[42:45], v[26:33], v[224:231], 0
	v_mfma_f32_16x16x128_f8f6f4 v[86:89], v[2:9], v[200:207], 0
	v_mfma_f32_16x16x128_f8f6f4 v[82:85], v[10:17], v[200:207], 0
	v_mfma_f32_16x16x128_f8f6f4 v[66:69], v[2:9], v[208:215], 0
	v_mfma_f32_16x16x128_f8f6f4 v[74:77], v[10:17], v[208:215], 0
	v_mfma_f32_16x16x128_f8f6f4 v[62:65], v[2:9], v[216:223], 0
	v_mfma_f32_16x16x128_f8f6f4 v[58:61], v[10:17], v[216:223], 0
	v_mfma_f32_16x16x128_f8f6f4 v[34:37], v[2:9], v[224:231], 0
	v_mfma_f32_16x16x128_f8f6f4 v[46:49], v[10:17], v[224:231], 0
	s_barrier
	s_add_i32 s28, 0, 0x18000
	s_add_i32 s58, 0, 0x1c000
	v_add_u32_e32 v14, s28, v193
	v_add_u32_e32 v30, s58, v193
	ds_read_b128 v[2:5], v14
	ds_read_b128 v[6:9], v14 offset:1024
	ds_read_b128 v[10:13], v14 offset:2048
	ds_read_b128 v[14:17], v14 offset:3072
	ds_read_b128 v[18:21], v30
	ds_read_b128 v[22:25], v30 offset:1024
	ds_read_b128 v[26:29], v30 offset:2048
	ds_read_b128 v[30:33], v30 offset:3072
	s_mov_b32 m0, s44
	v_lshl_add_u64 v[232:233], s[36:37], 0, v[170:171]
	ds_read_b128 v[200:203], v199 offset:32768
	ds_read_b128 v[204:207], v199 offset:33792
	ds_read_b128 v[208:211], v199 offset:34816
	ds_read_b128 v[212:215], v199 offset:35840
	ds_read_b128 v[216:219], v199 offset:36864
	ds_read_b128 v[220:223], v199 offset:37888
	ds_read_b128 v[224:227], v199 offset:38912
	ds_read_b128 v[228:231], v199 offset:39936
	global_load_lds_dwordx4 v[232:233], off
	v_lshl_add_u64 v[232:233], s[36:37], 0, v[172:173]
	s_mov_b32 m0, s45
	s_nop 0
	global_load_lds_dwordx4 v[232:233], off
	s_waitcnt vmcnt(8)
	s_waitcnt lgkmcnt(0)
	s_barrier
	s_waitcnt lgkmcnt(0)
	v_mfma_f32_16x16x128_f8f6f4 v[158:161], v[2:9], v[200:207], v[158:161]
	v_mfma_f32_16x16x128_f8f6f4 v[154:157], v[10:17], v[200:207], v[154:157]
	v_mfma_f32_16x16x128_f8f6f4 v[138:141], v[2:9], v[208:215], v[138:141]
	v_mfma_f32_16x16x128_f8f6f4 v[142:145], v[10:17], v[208:215], v[142:145]
	v_mfma_f32_16x16x128_f8f6f4 v[126:129], v[2:9], v[216:223], v[126:129]
	v_mfma_f32_16x16x128_f8f6f4 v[122:125], v[10:17], v[216:223], v[122:125]
	v_mfma_f32_16x16x128_f8f6f4 v[106:109], v[2:9], v[224:231], v[106:109]
	v_mfma_f32_16x16x128_f8f6f4 v[110:113], v[10:17], v[224:231], v[110:113]
	v_mfma_f32_16x16x128_f8f6f4 v[150:153], v[18:25], v[200:207], v[150:153]
	v_mfma_f32_16x16x128_f8f6f4 v[146:149], v[26:33], v[200:207], v[146:149]
	v_mfma_f32_16x16x128_f8f6f4 v[130:133], v[18:25], v[208:215], v[130:133]
	v_mfma_f32_16x16x128_f8f6f4 v[134:137], v[26:33], v[208:215], v[134:137]
	v_mfma_f32_16x16x128_f8f6f4 v[118:121], v[18:25], v[216:223], v[118:121]
	v_mfma_f32_16x16x128_f8f6f4 v[114:117], v[26:33], v[216:223], v[114:117]
	v_mfma_f32_16x16x128_f8f6f4 v[98:101], v[18:25], v[224:231], v[98:101]
	v_mfma_f32_16x16x128_f8f6f4 v[102:105], v[26:33], v[224:231], v[102:105]
	s_barrier
	s_add_i32 s28, s28, s42
	v_lshl_add_u64 v[184:185], v[184:185], 0, s[10:11]
	s_mov_b32 m0, s28
	ds_read_b128 v[200:203], v199 offset:49152
	ds_read_b128 v[204:207], v199 offset:50176
	ds_read_b128 v[208:211], v199 offset:51200
	ds_read_b128 v[212:215], v199 offset:52224
	ds_read_b128 v[216:219], v199 offset:53248
	ds_read_b128 v[220:223], v199 offset:54272
	ds_read_b128 v[224:227], v199 offset:55296
	ds_read_b128 v[228:231], v199 offset:56320
	global_load_lds_dwordx4 v[184:185], off
	s_add_i32 m0, s28, 0x2000
	s_add_u32 s28, s34, 0x20080
	v_lshl_add_u64 v[184:185], v[186:187], 0, s[10:11]
	s_addc_u32 s29, s35, 0
	s_add_i32 s34, s58, s42
	global_load_lds_dwordx4 v[184:185], off
	v_lshl_add_u64 v[184:185], s[28:29], 0, v[162:163]
	s_mov_b32 m0, s34
	s_nop 0
	global_load_lds_dwordx4 v[184:185], off
	v_lshl_add_u64 v[184:185], s[28:29], 0, v[164:165]
	s_add_i32 m0, s34, 0x2000
	s_nop 0
	global_load_lds_dwordx4 v[184:185], off
	v_lshl_add_u64 v[184:185], v[188:189], 0, s[10:11]
	s_mov_b32 m0, s47
	s_nop 0
	global_load_lds_dwordx4 v[184:185], off
	v_lshl_add_u64 v[184:185], v[190:191], 0, s[10:11]
	s_mov_b32 m0, s48
	s_nop 0
	global_load_lds_dwordx4 v[184:185], off
	s_waitcnt vmcnt(8)
	s_waitcnt lgkmcnt(0)
	s_barrier
	s_waitcnt lgkmcnt(0)
	v_mfma_f32_16x16x128_f8f6f4 v[94:97], v[2:9], v[200:207], v[94:97]
	v_mfma_f32_16x16x128_f8f6f4 v[90:93], v[10:17], v[200:207], v[90:93]
	v_mfma_f32_16x16x128_f8f6f4 v[70:73], v[2:9], v[208:215], v[70:73]
	v_mfma_f32_16x16x128_f8f6f4 v[78:81], v[10:17], v[208:215], v[78:81]
	v_mfma_f32_16x16x128_f8f6f4 v[54:57], v[2:9], v[216:223], v[54:57]
	v_mfma_f32_16x16x128_f8f6f4 v[50:53], v[10:17], v[216:223], v[50:53]
	v_mfma_f32_16x16x128_f8f6f4 v[38:41], v[2:9], v[224:231], v[38:41]
	v_mfma_f32_16x16x128_f8f6f4 v[42:45], v[10:17], v[224:231], v[42:45]
	v_mfma_f32_16x16x128_f8f6f4 v[86:89], v[18:25], v[200:207], v[86:89]
	v_mfma_f32_16x16x128_f8f6f4 v[82:85], v[26:33], v[200:207], v[82:85]
	v_mfma_f32_16x16x128_f8f6f4 v[66:69], v[18:25], v[208:215], v[66:69]
	v_mfma_f32_16x16x128_f8f6f4 v[74:77], v[26:33], v[208:215], v[74:77]
	v_mfma_f32_16x16x128_f8f6f4 v[62:65], v[18:25], v[216:223], v[62:65]
	v_mfma_f32_16x16x128_f8f6f4 v[58:61], v[26:33], v[216:223], v[58:61]
	v_mfma_f32_16x16x128_f8f6f4 v[34:37], v[18:25], v[224:231], v[34:37]
	v_mfma_f32_16x16x128_f8f6f4 v[46:49], v[26:33], v[224:231], v[46:49]
	s_barrier
	s_add_i32 s57, s57, 2
	s_add_u32 s55, s55, 0x100
	s_addc_u32 s56, s56, 0
	s_cmp_gt_u32 s57, 5
	s_mov_b64 s[28:29], s[30:31]
	s_cbranch_scc0 .LBB0_554
	s_branch .Lpk3_exit
.LBB0_554:
	ds_read_b128 v[18:21], v197
	ds_read_b128 v[22:25], v197 offset:1024
	ds_read_b128 v[26:29], v197 offset:2048
	ds_read_b128 v[30:33], v197 offset:3072
	ds_read_b128 v[2:5], v198
	ds_read_b128 v[6:9], v198 offset:1024
	ds_read_b128 v[10:13], v198 offset:2048
	ds_read_b128 v[14:17], v198 offset:3072
	s_add_u32 s30, s28, 0x100
	s_addc_u32 s31, s29, 0
	s_cmp_eq_u32 s57, 4
	s_cselect_b32 s37, s19, s31
	s_cselect_b32 s36, s53, s30
	s_cselect_b32 s35, s21, s56
	s_cselect_b32 s34, s54, s55
	v_lshl_add_u64 v[224:225], s[28:29], 0, v[176:177]
	s_add_i32 m0, s27, 0xc000
	ds_read_b128 v[184:187], v199
	ds_read_b128 v[188:191], v199 offset:1024
	ds_read_b128 v[200:203], v199 offset:2048
	ds_read_b128 v[204:207], v199 offset:3072
	ds_read_b128 v[208:211], v199 offset:4096
	ds_read_b128 v[212:215], v199 offset:5120
	ds_read_b128 v[216:219], v199 offset:6144
	ds_read_b128 v[220:223], v199 offset:7168
	global_load_lds_dwordx4 v[224:225], off
	v_lshl_add_u64 v[224:225], s[28:29], 0, v[178:179]
	s_add_i32 m0, s27, 0xe000
	s_nop 0
	global_load_lds_dwordx4 v[224:225], off
	s_waitcnt vmcnt(8)
	s_waitcnt lgkmcnt(0)
	s_barrier
	s_waitcnt lgkmcnt(0)
	v_mfma_f32_16x16x128_f8f6f4 v[158:161], v[18:25], v[184:191], v[158:161]
	v_mfma_f32_16x16x128_f8f6f4 v[154:157], v[26:33], v[184:191], v[154:157]
	v_mfma_f32_16x16x128_f8f6f4 v[138:141], v[18:25], v[200:207], v[138:141]
	v_mfma_f32_16x16x128_f8f6f4 v[142:145], v[26:33], v[200:207], v[142:145]
	v_mfma_f32_16x16x128_f8f6f4 v[126:129], v[18:25], v[208:215], v[126:129]
	v_mfma_f32_16x16x128_f8f6f4 v[122:125], v[26:33], v[208:215], v[122:125]
	v_mfma_f32_16x16x128_f8f6f4 v[106:109], v[18:25], v[216:223], v[106:109]
	v_mfma_f32_16x16x128_f8f6f4 v[110:113], v[26:33], v[216:223], v[110:113]
	v_mfma_f32_16x16x128_f8f6f4 v[150:153], v[2:9], v[184:191], v[150:153]
	v_mfma_f32_16x16x128_f8f6f4 v[146:149], v[10:17], v[184:191], v[146:149]
	v_mfma_f32_16x16x128_f8f6f4 v[130:133], v[2:9], v[200:207], v[130:133]
	v_mfma_f32_16x16x128_f8f6f4 v[134:137], v[10:17], v[200:207], v[134:137]
	v_mfma_f32_16x16x128_f8f6f4 v[118:121], v[2:9], v[208:215], v[118:121]
	v_mfma_f32_16x16x128_f8f6f4 v[114:117], v[10:17], v[208:215], v[114:117]
	v_mfma_f32_16x16x128_f8f6f4 v[98:101], v[2:9], v[216:223], v[98:101]
	v_mfma_f32_16x16x128_f8f6f4 v[102:105], v[10:17], v[216:223], v[102:105]
	s_barrier
	s_add_i32 s28, s49, s42
	v_lshl_add_u64 v[184:185], s[34:35], 0, v[162:163]
	s_mov_b32 m0, s28
	ds_read_b128 v[200:203], v199 offset:16384
	ds_read_b128 v[204:207], v199 offset:17408
	ds_read_b128 v[208:211], v199 offset:18432
	ds_read_b128 v[212:215], v199 offset:19456
	ds_read_b128 v[216:219], v199 offset:20480
	ds_read_b128 v[220:223], v199 offset:21504
	ds_read_b128 v[224:227], v199 offset:22528
	ds_read_b128 v[228:231], v199 offset:23552
	global_load_lds_dwordx4 v[184:185], off
	s_add_i32 m0, s28, 0x2000
	s_add_u32 s28, s34, 0x20000
	v_lshl_add_u64 v[186:187], s[34:35], 0, v[164:165]
	s_addc_u32 s29, s35, 0
	s_add_i32 s58, s50, s42
	global_load_lds_dwordx4 v[186:187], off
	v_lshl_add_u64 v[188:189], s[28:29], 0, v[162:163]
	s_mov_b32 m0, s58
	v_lshl_add_u64 v[190:191], s[36:37], 0, v[168:169]
	global_load_lds_dwordx4 v[188:189], off
	v_lshl_add_u64 v[188:189], s[28:29], 0, v[164:165]
	s_add_i32 m0, s58, 0x2000
	s_nop 0
	global_load_lds_dwordx4 v[188:189], off
	v_lshl_add_u64 v[188:189], s[36:37], 0, v[166:167]
	s_mov_b32 m0, s27
	s_nop 0
	global_load_lds_dwordx4 v[188:189], off
	s_mov_b32 m0, s43
	s_nop 0
	global_load_lds_dwordx4 v[190:191], off
	s_waitcnt vmcnt(8)
	s_waitcnt lgkmcnt(0)
	s_barrier
	s_waitcnt lgkmcnt(0)
	v_mfma_f32_16x16x128_f8f6f4 v[94:97], v[18:25], v[200:207], v[94:97]
	v_mfma_f32_16x16x128_f8f6f4 v[90:93], v[26:33], v[200:207], v[90:93]
	v_mfma_f32_16x16x128_f8f6f4 v[70:73], v[18:25], v[208:215], v[70:73]
	v_mfma_f32_16x16x128_f8f6f4 v[78:81], v[26:33], v[208:215], v[78:81]
	v_mfma_f32_16x16x128_f8f6f4 v[54:57], v[18:25], v[216:223], v[54:57]
	v_mfma_f32_16x16x128_f8f6f4 v[50:53], v[26:33], v[216:223], v[50:53]
	v_mfma_f32_16x16x128_f8f6f4 v[38:41], v[18:25], v[224:231], v[38:41]
	v_mfma_f32_16x16x128_f8f6f4 v[42:45], v[26:33], v[224:231], v[42:45]
	v_mfma_f32_16x16x128_f8f6f4 v[86:89], v[2:9], v[200:207], v[86:89]
	v_mfma_f32_16x16x128_f8f6f4 v[82:85], v[10:17], v[200:207], v[82:85]
	v_mfma_f32_16x16x128_f8f6f4 v[66:69], v[2:9], v[208:215], v[66:69]
	v_mfma_f32_16x16x128_f8f6f4 v[74:77], v[10:17], v[208:215], v[74:77]
	v_mfma_f32_16x16x128_f8f6f4 v[62:65], v[2:9], v[216:223], v[62:65]
	v_mfma_f32_16x16x128_f8f6f4 v[58:61], v[10:17], v[216:223], v[58:61]
	v_mfma_f32_16x16x128_f8f6f4 v[34:37], v[2:9], v[224:231], v[34:37]
	v_mfma_f32_16x16x128_f8f6f4 v[46:49], v[10:17], v[224:231], v[46:49]
	s_barrier
	s_add_i32 s28, 0, 0x18000
	s_add_i32 s58, 0, 0x1c000
	v_add_u32_e32 v14, s28, v193
	v_add_u32_e32 v30, s58, v193
	ds_read_b128 v[2:5], v14
	ds_read_b128 v[6:9], v14 offset:1024
	ds_read_b128 v[10:13], v14 offset:2048
	ds_read_b128 v[14:17], v14 offset:3072
	ds_read_b128 v[18:21], v30
	ds_read_b128 v[22:25], v30 offset:1024
	ds_read_b128 v[26:29], v30 offset:2048
	ds_read_b128 v[30:33], v30 offset:3072
	s_mov_b32 m0, s44
	v_lshl_add_u64 v[232:233], s[36:37], 0, v[170:171]
	ds_read_b128 v[200:203], v199 offset:32768
	ds_read_b128 v[204:207], v199 offset:33792
	ds_read_b128 v[208:211], v199 offset:34816
	ds_read_b128 v[212:215], v199 offset:35840
	ds_read_b128 v[216:219], v199 offset:36864
	ds_read_b128 v[220:223], v199 offset:37888
	ds_read_b128 v[224:227], v199 offset:38912
	ds_read_b128 v[228:231], v199 offset:39936
	global_load_lds_dwordx4 v[232:233], off
	v_lshl_add_u64 v[232:233], s[36:37], 0, v[172:173]
	s_mov_b32 m0, s45
	s_nop 0
	global_load_lds_dwordx4 v[232:233], off
	s_waitcnt vmcnt(8)
	s_waitcnt lgkmcnt(0)
	s_barrier
	s_waitcnt lgkmcnt(0)
	v_mfma_f32_16x16x128_f8f6f4 v[158:161], v[2:9], v[200:207], v[158:161]
	v_mfma_f32_16x16x128_f8f6f4 v[154:157], v[10:17], v[200:207], v[154:157]
	v_mfma_f32_16x16x128_f8f6f4 v[138:141], v[2:9], v[208:215], v[138:141]
	v_mfma_f32_16x16x128_f8f6f4 v[142:145], v[10:17], v[208:215], v[142:145]
	v_mfma_f32_16x16x128_f8f6f4 v[126:129], v[2:9], v[216:223], v[126:129]
	v_mfma_f32_16x16x128_f8f6f4 v[122:125], v[10:17], v[216:223], v[122:125]
	v_mfma_f32_16x16x128_f8f6f4 v[106:109], v[2:9], v[224:231], v[106:109]
	v_mfma_f32_16x16x128_f8f6f4 v[110:113], v[10:17], v[224:231], v[110:113]
	v_mfma_f32_16x16x128_f8f6f4 v[150:153], v[18:25], v[200:207], v[150:153]
	v_mfma_f32_16x16x128_f8f6f4 v[146:149], v[26:33], v[200:207], v[146:149]
	v_mfma_f32_16x16x128_f8f6f4 v[130:133], v[18:25], v[208:215], v[130:133]
	v_mfma_f32_16x16x128_f8f6f4 v[134:137], v[26:33], v[208:215], v[134:137]
	v_mfma_f32_16x16x128_f8f6f4 v[118:121], v[18:25], v[216:223], v[118:121]
	v_mfma_f32_16x16x128_f8f6f4 v[114:117], v[26:33], v[216:223], v[114:117]
	v_mfma_f32_16x16x128_f8f6f4 v[98:101], v[18:25], v[224:231], v[98:101]
	v_mfma_f32_16x16x128_f8f6f4 v[102:105], v[26:33], v[224:231], v[102:105]
	s_barrier
	s_add_i32 s28, s28, s42
	v_lshl_add_u64 v[184:185], v[184:185], 0, s[10:11]
	s_mov_b32 m0, s28
	ds_read_b128 v[200:203], v199 offset:49152
	ds_read_b128 v[204:207], v199 offset:50176
	ds_read_b128 v[208:211], v199 offset:51200
	ds_read_b128 v[212:215], v199 offset:52224
	ds_read_b128 v[216:219], v199 offset:53248
	ds_read_b128 v[220:223], v199 offset:54272
	ds_read_b128 v[224:227], v199 offset:55296
	ds_read_b128 v[228:231], v199 offset:56320
	global_load_lds_dwordx4 v[184:185], off
	s_add_i32 m0, s28, 0x2000
	s_add_u32 s28, s34, 0x20080
	v_lshl_add_u64 v[184:185], v[186:187], 0, s[10:11]
	s_addc_u32 s29, s35, 0
	s_add_i32 s34, s58, s42
	global_load_lds_dwordx4 v[184:185], off
	v_lshl_add_u64 v[184:185], s[28:29], 0, v[162:163]
	s_mov_b32 m0, s34
	s_nop 0
	global_load_lds_dwordx4 v[184:185], off
	v_lshl_add_u64 v[184:185], s[28:29], 0, v[164:165]
	s_add_i32 m0, s34, 0x2000
	s_nop 0
	global_load_lds_dwordx4 v[184:185], off
	v_lshl_add_u64 v[184:185], v[188:189], 0, s[10:11]
	s_mov_b32 m0, s47
	s_nop 0
	global_load_lds_dwordx4 v[184:185], off
	v_lshl_add_u64 v[184:185], v[190:191], 0, s[10:11]
	s_mov_b32 m0, s48
	s_nop 0
	global_load_lds_dwordx4 v[184:185], off
	s_waitcnt vmcnt(8)
	s_waitcnt lgkmcnt(0)
	s_barrier
	s_waitcnt lgkmcnt(0)
	v_mfma_f32_16x16x128_f8f6f4 v[94:97], v[2:9], v[200:207], v[94:97]
	v_mfma_f32_16x16x128_f8f6f4 v[90:93], v[10:17], v[200:207], v[90:93]
	v_mfma_f32_16x16x128_f8f6f4 v[70:73], v[2:9], v[208:215], v[70:73]
	v_mfma_f32_16x16x128_f8f6f4 v[78:81], v[10:17], v[208:215], v[78:81]
	v_mfma_f32_16x16x128_f8f6f4 v[54:57], v[2:9], v[216:223], v[54:57]
	v_mfma_f32_16x16x128_f8f6f4 v[50:53], v[10:17], v[216:223], v[50:53]
	v_mfma_f32_16x16x128_f8f6f4 v[38:41], v[2:9], v[224:231], v[38:41]
	v_mfma_f32_16x16x128_f8f6f4 v[42:45], v[10:17], v[224:231], v[42:45]
	v_mfma_f32_16x16x128_f8f6f4 v[86:89], v[18:25], v[200:207], v[86:89]
	v_mfma_f32_16x16x128_f8f6f4 v[82:85], v[26:33], v[200:207], v[82:85]
	v_mfma_f32_16x16x128_f8f6f4 v[66:69], v[18:25], v[208:215], v[66:69]
	v_mfma_f32_16x16x128_f8f6f4 v[74:77], v[26:33], v[208:215], v[74:77]
	v_mfma_f32_16x16x128_f8f6f4 v[62:65], v[18:25], v[216:223], v[62:65]
	v_mfma_f32_16x16x128_f8f6f4 v[58:61], v[26:33], v[216:223], v[58:61]
	v_mfma_f32_16x16x128_f8f6f4 v[34:37], v[18:25], v[224:231], v[34:37]
	v_mfma_f32_16x16x128_f8f6f4 v[46:49], v[26:33], v[224:231], v[46:49]
	s_barrier
	s_add_i32 s57, s57, 2
	s_add_u32 s55, s55, 0x100
	s_addc_u32 s56, s56, 0
	s_cmp_gt_u32 s57, 5
	s_mov_b64 s[28:29], s[30:31]
	s_cbranch_scc0 .LBB0_554

.Lpk4_entry:
	ds_read_b128 v[18:21], v191
	ds_read_b128 v[22:25], v191 offset:1024
	ds_read_b128 v[26:29], v191 offset:2048
	ds_read_b128 v[30:33], v191 offset:3072
	ds_read_b128 v[2:5], v192
	ds_read_b128 v[6:9], v192 offset:1024
	ds_read_b128 v[10:13], v192 offset:2048
	ds_read_b128 v[14:17], v192 offset:3072
	s_add_u32 s28, s26, 0x100
	s_addc_u32 s29, s27, 0
	s_cmp_eq_u32 s53, 12
	s_cselect_b32 s35, s17, s29
	s_cselect_b32 s34, s49, s28
	s_cselect_b32 s31, s19, s52
	s_cselect_b32 s30, s50, s51
	v_lshl_add_u64 v[218:219], s[26:27], 0, v[172:173]
	s_add_i32 m0, s25, 0xc000
	ds_read_b128 v[180:183], v193
	ds_read_b128 v[184:187], v193 offset:1024
	ds_read_b128 v[194:197], v193 offset:2048
	ds_read_b128 v[198:201], v193 offset:3072
	ds_read_b128 v[202:205], v193 offset:4096
	ds_read_b128 v[206:209], v193 offset:5120
	ds_read_b128 v[210:213], v193 offset:6144
	ds_read_b128 v[214:217], v193 offset:7168
	global_load_lds_dwordx4 v[218:219], off
	v_lshl_add_u64 v[218:219], s[26:27], 0, v[174:175]
	s_add_i32 m0, s25, 0xe000
	s_nop 0
	global_load_lds_dwordx4 v[218:219], off
	s_waitcnt vmcnt(8)
	s_waitcnt lgkmcnt(0)
	s_barrier
	s_waitcnt lgkmcnt(0)
	v_mfma_f32_16x16x128_f8f6f4 v[158:161], v[18:25], v[180:187], 0
	v_mfma_f32_16x16x128_f8f6f4 v[154:157], v[26:33], v[180:187], 0
	v_mfma_f32_16x16x128_f8f6f4 v[146:149], v[18:25], v[194:201], 0
	v_mfma_f32_16x16x128_f8f6f4 v[138:141], v[26:33], v[194:201], 0
	v_mfma_f32_16x16x128_f8f6f4 v[130:133], v[18:25], v[202:209], 0
	v_mfma_f32_16x16x128_f8f6f4 v[122:125], v[26:33], v[202:209], 0
	v_mfma_f32_16x16x128_f8f6f4 v[114:117], v[18:25], v[210:217], 0
	v_mfma_f32_16x16x128_f8f6f4 v[106:109], v[26:33], v[210:217], 0
	v_mfma_f32_16x16x128_f8f6f4 v[150:153], v[2:9], v[180:187], 0
	v_mfma_f32_16x16x128_f8f6f4 v[142:145], v[10:17], v[180:187], 0
	v_mfma_f32_16x16x128_f8f6f4 v[134:137], v[2:9], v[194:201], 0
	v_mfma_f32_16x16x128_f8f6f4 v[126:129], v[10:17], v[194:201], 0
	v_mfma_f32_16x16x128_f8f6f4 v[118:121], v[2:9], v[202:209], 0
	v_mfma_f32_16x16x128_f8f6f4 v[110:113], v[10:17], v[202:209], 0
	v_mfma_f32_16x16x128_f8f6f4 v[102:105], v[2:9], v[210:217], 0
	v_mfma_f32_16x16x128_f8f6f4 v[98:101], v[10:17], v[210:217], 0
	s_barrier
	s_add_i32 s26, s46, s38
	v_lshl_add_u64 v[180:181], s[30:31], 0, v[162:163]
	s_mov_b32 m0, s26
	ds_read_b128 v[194:197], v193 offset:16384
	ds_read_b128 v[198:201], v193 offset:17408
	ds_read_b128 v[202:205], v193 offset:18432
	ds_read_b128 v[206:209], v193 offset:19456
	ds_read_b128 v[210:213], v193 offset:20480
	ds_read_b128 v[214:217], v193 offset:21504
	ds_read_b128 v[218:221], v193 offset:22528
	ds_read_b128 v[222:225], v193 offset:23552
	global_load_lds_dwordx4 v[180:181], off
	s_add_i32 m0, s26, 0x2000
	s_add_u32 s26, s30, 0x40000
	v_lshl_add_u64 v[182:183], s[30:31], 0, v[164:165]
	s_addc_u32 s27, s31, 0
	s_add_i32 s54, s47, s38
	global_load_lds_dwordx4 v[182:183], off
	v_lshl_add_u64 v[184:185], s[26:27], 0, v[162:163]
	s_mov_b32 m0, s54
	v_lshl_add_u64 v[186:187], s[34:35], 0, v[164:165]
	global_load_lds_dwordx4 v[184:185], off
	v_lshl_add_u64 v[184:185], s[26:27], 0, v[164:165]
	s_add_i32 m0, s54, 0x2000
	s_nop 0
	global_load_lds_dwordx4 v[184:185], off
	v_lshl_add_u64 v[184:185], s[34:35], 0, v[162:163]
	s_mov_b32 m0, s25
	s_nop 0
	global_load_lds_dwordx4 v[184:185], off
	s_mov_b32 m0, s39
	s_nop 0
	global_load_lds_dwordx4 v[186:187], off
	s_waitcnt vmcnt(8)
	s_waitcnt lgkmcnt(0)
	s_barrier
	s_waitcnt lgkmcnt(0)
	v_mfma_f32_16x16x128_f8f6f4 v[86:89], v[18:25], v[194:201], 0
	v_mfma_f32_16x16x128_f8f6f4 v[82:85], v[26:33], v[194:201], 0
	v_mfma_f32_16x16x128_f8f6f4 v[70:73], v[18:25], v[202:209], 0
	v_mfma_f32_16x16x128_f8f6f4 v[66:69], v[26:33], v[202:209], 0
	v_mfma_f32_16x16x128_f8f6f4 v[54:57], v[18:25], v[210:217], 0
	v_mfma_f32_16x16x128_f8f6f4 v[50:53], v[26:33], v[210:217], 0
	v_mfma_f32_16x16x128_f8f6f4 v[38:41], v[18:25], v[218:225], 0
	v_mfma_f32_16x16x128_f8f6f4 v[34:37], v[26:33], v[218:225], 0
	v_mfma_f32_16x16x128_f8f6f4 v[94:97], v[2:9], v[194:201], 0
	v_mfma_f32_16x16x128_f8f6f4 v[90:93], v[10:17], v[194:201], 0
	v_mfma_f32_16x16x128_f8f6f4 v[78:81], v[2:9], v[202:209], 0
	v_mfma_f32_16x16x128_f8f6f4 v[74:77], v[10:17], v[202:209], 0
	v_mfma_f32_16x16x128_f8f6f4 v[62:65], v[2:9], v[210:217], 0
	v_mfma_f32_16x16x128_f8f6f4 v[58:61], v[10:17], v[210:217], 0
	v_mfma_f32_16x16x128_f8f6f4 v[46:49], v[2:9], v[218:225], 0
	v_mfma_f32_16x16x128_f8f6f4 v[42:45], v[10:17], v[218:225], 0
	s_barrier
	s_add_i32 s26, 0, 0x18000
	s_add_i32 s54, 0, 0x1c000
	v_add_u32_e32 v14, s26, v189
	v_add_u32_e32 v30, s54, v189
	ds_read_b128 v[2:5], v14
	ds_read_b128 v[6:9], v14 offset:1024
	ds_read_b128 v[10:13], v14 offset:2048
	ds_read_b128 v[14:17], v14 offset:3072
	ds_read_b128 v[18:21], v30
	ds_read_b128 v[22:25], v30 offset:1024
	ds_read_b128 v[26:29], v30 offset:2048
	ds_read_b128 v[30:33], v30 offset:3072
	s_mov_b32 m0, s40
	v_lshl_add_u64 v[226:227], s[34:35], 0, v[166:167]
	ds_read_b128 v[194:197], v193 offset:32768
	ds_read_b128 v[198:201], v193 offset:33792
	ds_read_b128 v[202:205], v193 offset:34816
	ds_read_b128 v[206:209], v193 offset:35840
	ds_read_b128 v[210:213], v193 offset:36864
	ds_read_b128 v[214:217], v193 offset:37888
	ds_read_b128 v[218:221], v193 offset:38912
	ds_read_b128 v[222:225], v193 offset:39936
	global_load_lds_dwordx4 v[226:227], off
	v_lshl_add_u64 v[226:227], s[34:35], 0, v[168:169]
	s_mov_b32 m0, s41
	s_nop 0
	global_load_lds_dwordx4 v[226:227], off
	s_waitcnt vmcnt(8)
	s_waitcnt lgkmcnt(0)
	s_barrier
	s_waitcnt lgkmcnt(0)
	v_mfma_f32_16x16x128_f8f6f4 v[158:161], v[2:9], v[194:201], v[158:161]
	v_mfma_f32_16x16x128_f8f6f4 v[154:157], v[10:17], v[194:201], v[154:157]
	v_mfma_f32_16x16x128_f8f6f4 v[146:149], v[2:9], v[202:209], v[146:149]
	v_mfma_f32_16x16x128_f8f6f4 v[138:141], v[10:17], v[202:209], v[138:141]
	v_mfma_f32_16x16x128_f8f6f4 v[130:133], v[2:9], v[210:217], v[130:133]
	v_mfma_f32_16x16x128_f8f6f4 v[122:125], v[10:17], v[210:217], v[122:125]
	v_mfma_f32_16x16x128_f8f6f4 v[114:117], v[2:9], v[218:225], v[114:117]
	v_mfma_f32_16x16x128_f8f6f4 v[106:109], v[10:17], v[218:225], v[106:109]
	v_mfma_f32_16x16x128_f8f6f4 v[150:153], v[18:25], v[194:201], v[150:153]
	v_mfma_f32_16x16x128_f8f6f4 v[142:145], v[26:33], v[194:201], v[142:145]
	v_mfma_f32_16x16x128_f8f6f4 v[134:137], v[18:25], v[202:209], v[134:137]
	v_mfma_f32_16x16x128_f8f6f4 v[126:129], v[26:33], v[202:209], v[126:129]
	v_mfma_f32_16x16x128_f8f6f4 v[118:121], v[18:25], v[210:217], v[118:121]
	v_mfma_f32_16x16x128_f8f6f4 v[110:113], v[26:33], v[210:217], v[110:113]
	v_mfma_f32_16x16x128_f8f6f4 v[102:105], v[18:25], v[218:225], v[102:105]
	v_mfma_f32_16x16x128_f8f6f4 v[98:101], v[26:33], v[218:225], v[98:101]
	s_barrier
	s_add_i32 s26, s26, s38
	v_lshl_add_u64 v[180:181], v[180:181], 0, s[8:9]
	s_mov_b32 m0, s26
	ds_read_b128 v[194:197], v193 offset:49152
	ds_read_b128 v[198:201], v193 offset:50176
	ds_read_b128 v[202:205], v193 offset:51200
	ds_read_b128 v[206:209], v193 offset:52224
	ds_read_b128 v[210:213], v193 offset:53248
	ds_read_b128 v[214:217], v193 offset:54272
	ds_read_b128 v[218:221], v193 offset:55296
	ds_read_b128 v[222:225], v193 offset:56320
	global_load_lds_dwordx4 v[180:181], off
	s_add_i32 m0, s26, 0x2000
	s_add_u32 s26, s30, 0x40080
	v_lshl_add_u64 v[180:181], v[182:183], 0, s[8:9]
	s_addc_u32 s27, s31, 0
	s_add_i32 s30, s54, s38
	global_load_lds_dwordx4 v[180:181], off
	v_lshl_add_u64 v[180:181], s[26:27], 0, v[162:163]
	s_mov_b32 m0, s30
	s_nop 0
	global_load_lds_dwordx4 v[180:181], off
	v_lshl_add_u64 v[180:181], s[26:27], 0, v[164:165]
	s_add_i32 m0, s30, 0x2000
	s_nop 0
	global_load_lds_dwordx4 v[180:181], off
	v_lshl_add_u64 v[180:181], v[184:185], 0, s[8:9]
	s_mov_b32 m0, s44
	s_nop 0
	global_load_lds_dwordx4 v[180:181], off
	v_lshl_add_u64 v[180:181], v[186:187], 0, s[8:9]
	s_mov_b32 m0, s45
	s_nop 0
	global_load_lds_dwordx4 v[180:181], off
	s_waitcnt vmcnt(8)
	s_waitcnt lgkmcnt(0)
	s_barrier
	s_waitcnt lgkmcnt(0)
	v_mfma_f32_16x16x128_f8f6f4 v[86:89], v[2:9], v[194:201], v[86:89]
	v_mfma_f32_16x16x128_f8f6f4 v[82:85], v[10:17], v[194:201], v[82:85]
	v_mfma_f32_16x16x128_f8f6f4 v[70:73], v[2:9], v[202:209], v[70:73]
	v_mfma_f32_16x16x128_f8f6f4 v[66:69], v[10:17], v[202:209], v[66:69]
	v_mfma_f32_16x16x128_f8f6f4 v[54:57], v[2:9], v[210:217], v[54:57]
	v_mfma_f32_16x16x128_f8f6f4 v[50:53], v[10:17], v[210:217], v[50:53]
	v_mfma_f32_16x16x128_f8f6f4 v[38:41], v[2:9], v[218:225], v[38:41]
	v_mfma_f32_16x16x128_f8f6f4 v[34:37], v[10:17], v[218:225], v[34:37]
	v_mfma_f32_16x16x128_f8f6f4 v[94:97], v[18:25], v[194:201], v[94:97]
	v_mfma_f32_16x16x128_f8f6f4 v[90:93], v[26:33], v[194:201], v[90:93]
	v_mfma_f32_16x16x128_f8f6f4 v[78:81], v[18:25], v[202:209], v[78:81]
	v_mfma_f32_16x16x128_f8f6f4 v[74:77], v[26:33], v[202:209], v[74:77]
	v_mfma_f32_16x16x128_f8f6f4 v[62:65], v[18:25], v[210:217], v[62:65]
	v_mfma_f32_16x16x128_f8f6f4 v[58:61], v[26:33], v[210:217], v[58:61]
	v_mfma_f32_16x16x128_f8f6f4 v[46:49], v[18:25], v[218:225], v[46:49]
	v_mfma_f32_16x16x128_f8f6f4 v[42:45], v[26:33], v[218:225], v[42:45]
	s_barrier
	s_add_i32 s53, s53, 2
	s_add_u32 s51, s51, 0x100
	s_addc_u32 s52, s52, 0
	s_cmp_gt_u32 s53, 13
	s_mov_b64 s[26:27], s[28:29]
	s_cbranch_scc0 .LBB0_633
	s_branch .Lpk4_exit
.LBB0_633:
	ds_read_b128 v[18:21], v191
	ds_read_b128 v[22:25], v191 offset:1024
	ds_read_b128 v[26:29], v191 offset:2048
	ds_read_b128 v[30:33], v191 offset:3072
	ds_read_b128 v[2:5], v192
	ds_read_b128 v[6:9], v192 offset:1024
	ds_read_b128 v[10:13], v192 offset:2048
	ds_read_b128 v[14:17], v192 offset:3072
	s_add_u32 s28, s26, 0x100
	s_addc_u32 s29, s27, 0
	s_cmp_eq_u32 s53, 12
	s_cselect_b32 s35, s17, s29
	s_cselect_b32 s34, s49, s28
	s_cselect_b32 s31, s19, s52
	s_cselect_b32 s30, s50, s51
	v_lshl_add_u64 v[218:219], s[26:27], 0, v[172:173]
	s_add_i32 m0, s25, 0xc000
	ds_read_b128 v[180:183], v193
	ds_read_b128 v[184:187], v193 offset:1024
	ds_read_b128 v[194:197], v193 offset:2048
	ds_read_b128 v[198:201], v193 offset:3072
	ds_read_b128 v[202:205], v193 offset:4096
	ds_read_b128 v[206:209], v193 offset:5120
	ds_read_b128 v[210:213], v193 offset:6144
	ds_read_b128 v[214:217], v193 offset:7168
	global_load_lds_dwordx4 v[218:219], off
	v_lshl_add_u64 v[218:219], s[26:27], 0, v[174:175]
	s_add_i32 m0, s25, 0xe000
	s_nop 0
	global_load_lds_dwordx4 v[218:219], off
	s_waitcnt vmcnt(8)
	s_waitcnt lgkmcnt(0)
	s_barrier
	s_waitcnt lgkmcnt(0)
	v_mfma_f32_16x16x128_f8f6f4 v[158:161], v[18:25], v[180:187], v[158:161]
	v_mfma_f32_16x16x128_f8f6f4 v[154:157], v[26:33], v[180:187], v[154:157]
	v_mfma_f32_16x16x128_f8f6f4 v[146:149], v[18:25], v[194:201], v[146:149]
	v_mfma_f32_16x16x128_f8f6f4 v[138:141], v[26:33], v[194:201], v[138:141]
	v_mfma_f32_16x16x128_f8f6f4 v[130:133], v[18:25], v[202:209], v[130:133]
	v_mfma_f32_16x16x128_f8f6f4 v[122:125], v[26:33], v[202:209], v[122:125]
	v_mfma_f32_16x16x128_f8f6f4 v[114:117], v[18:25], v[210:217], v[114:117]
	v_mfma_f32_16x16x128_f8f6f4 v[106:109], v[26:33], v[210:217], v[106:109]
	v_mfma_f32_16x16x128_f8f6f4 v[150:153], v[2:9], v[180:187], v[150:153]
	v_mfma_f32_16x16x128_f8f6f4 v[142:145], v[10:17], v[180:187], v[142:145]
	v_mfma_f32_16x16x128_f8f6f4 v[134:137], v[2:9], v[194:201], v[134:137]
	v_mfma_f32_16x16x128_f8f6f4 v[126:129], v[10:17], v[194:201], v[126:129]
	v_mfma_f32_16x16x128_f8f6f4 v[118:121], v[2:9], v[202:209], v[118:121]
	v_mfma_f32_16x16x128_f8f6f4 v[110:113], v[10:17], v[202:209], v[110:113]
	v_mfma_f32_16x16x128_f8f6f4 v[102:105], v[2:9], v[210:217], v[102:105]
	v_mfma_f32_16x16x128_f8f6f4 v[98:101], v[10:17], v[210:217], v[98:101]
	s_barrier
	s_add_i32 s26, s46, s38
	v_lshl_add_u64 v[180:181], s[30:31], 0, v[162:163]
	s_mov_b32 m0, s26
	ds_read_b128 v[194:197], v193 offset:16384
	ds_read_b128 v[198:201], v193 offset:17408
	ds_read_b128 v[202:205], v193 offset:18432
	ds_read_b128 v[206:209], v193 offset:19456
	ds_read_b128 v[210:213], v193 offset:20480
	ds_read_b128 v[214:217], v193 offset:21504
	ds_read_b128 v[218:221], v193 offset:22528
	ds_read_b128 v[222:225], v193 offset:23552
	global_load_lds_dwordx4 v[180:181], off
	s_add_i32 m0, s26, 0x2000
	s_add_u32 s26, s30, 0x40000
	v_lshl_add_u64 v[182:183], s[30:31], 0, v[164:165]
	s_addc_u32 s27, s31, 0
	s_add_i32 s54, s47, s38
	global_load_lds_dwordx4 v[182:183], off
	v_lshl_add_u64 v[184:185], s[26:27], 0, v[162:163]
	s_mov_b32 m0, s54
	v_lshl_add_u64 v[186:187], s[34:35], 0, v[164:165]
	global_load_lds_dwordx4 v[184:185], off
	v_lshl_add_u64 v[184:185], s[26:27], 0, v[164:165]
	s_add_i32 m0, s54, 0x2000
	s_nop 0
	global_load_lds_dwordx4 v[184:185], off
	v_lshl_add_u64 v[184:185], s[34:35], 0, v[162:163]
	s_mov_b32 m0, s25
	s_nop 0
	global_load_lds_dwordx4 v[184:185], off
	s_mov_b32 m0, s39
	s_nop 0
	global_load_lds_dwordx4 v[186:187], off
	s_waitcnt vmcnt(8)
	s_waitcnt lgkmcnt(0)
	s_barrier
	s_waitcnt lgkmcnt(0)
	v_mfma_f32_16x16x128_f8f6f4 v[86:89], v[18:25], v[194:201], v[86:89]
	v_mfma_f32_16x16x128_f8f6f4 v[82:85], v[26:33], v[194:201], v[82:85]
	v_mfma_f32_16x16x128_f8f6f4 v[70:73], v[18:25], v[202:209], v[70:73]
	v_mfma_f32_16x16x128_f8f6f4 v[66:69], v[26:33], v[202:209], v[66:69]
	v_mfma_f32_16x16x128_f8f6f4 v[54:57], v[18:25], v[210:217], v[54:57]
	v_mfma_f32_16x16x128_f8f6f4 v[50:53], v[26:33], v[210:217], v[50:53]
	v_mfma_f32_16x16x128_f8f6f4 v[38:41], v[18:25], v[218:225], v[38:41]
	v_mfma_f32_16x16x128_f8f6f4 v[34:37], v[26:33], v[218:225], v[34:37]
	v_mfma_f32_16x16x128_f8f6f4 v[94:97], v[2:9], v[194:201], v[94:97]
	v_mfma_f32_16x16x128_f8f6f4 v[90:93], v[10:17], v[194:201], v[90:93]
	v_mfma_f32_16x16x128_f8f6f4 v[78:81], v[2:9], v[202:209], v[78:81]
	v_mfma_f32_16x16x128_f8f6f4 v[74:77], v[10:17], v[202:209], v[74:77]
	v_mfma_f32_16x16x128_f8f6f4 v[62:65], v[2:9], v[210:217], v[62:65]
	v_mfma_f32_16x16x128_f8f6f4 v[58:61], v[10:17], v[210:217], v[58:61]
	v_mfma_f32_16x16x128_f8f6f4 v[46:49], v[2:9], v[218:225], v[46:49]
	v_mfma_f32_16x16x128_f8f6f4 v[42:45], v[10:17], v[218:225], v[42:45]
	s_barrier
	s_add_i32 s26, 0, 0x18000
	s_add_i32 s54, 0, 0x1c000
	v_add_u32_e32 v14, s26, v189
	v_add_u32_e32 v30, s54, v189
	ds_read_b128 v[2:5], v14
	ds_read_b128 v[6:9], v14 offset:1024
	ds_read_b128 v[10:13], v14 offset:2048
	ds_read_b128 v[14:17], v14 offset:3072
	ds_read_b128 v[18:21], v30
	ds_read_b128 v[22:25], v30 offset:1024
	ds_read_b128 v[26:29], v30 offset:2048
	ds_read_b128 v[30:33], v30 offset:3072
	s_mov_b32 m0, s40
	v_lshl_add_u64 v[226:227], s[34:35], 0, v[166:167]
	ds_read_b128 v[194:197], v193 offset:32768
	ds_read_b128 v[198:201], v193 offset:33792
	ds_read_b128 v[202:205], v193 offset:34816
	ds_read_b128 v[206:209], v193 offset:35840
	ds_read_b128 v[210:213], v193 offset:36864
	ds_read_b128 v[214:217], v193 offset:37888
	ds_read_b128 v[218:221], v193 offset:38912
	ds_read_b128 v[222:225], v193 offset:39936
	global_load_lds_dwordx4 v[226:227], off
	v_lshl_add_u64 v[226:227], s[34:35], 0, v[168:169]
	s_mov_b32 m0, s41
	s_nop 0
	global_load_lds_dwordx4 v[226:227], off
	s_waitcnt vmcnt(8)
	s_waitcnt lgkmcnt(0)
	s_barrier
	s_waitcnt lgkmcnt(0)
	v_mfma_f32_16x16x128_f8f6f4 v[158:161], v[2:9], v[194:201], v[158:161]
	v_mfma_f32_16x16x128_f8f6f4 v[154:157], v[10:17], v[194:201], v[154:157]
	v_mfma_f32_16x16x128_f8f6f4 v[146:149], v[2:9], v[202:209], v[146:149]
	v_mfma_f32_16x16x128_f8f6f4 v[138:141], v[10:17], v[202:209], v[138:141]
	v_mfma_f32_16x16x128_f8f6f4 v[130:133], v[2:9], v[210:217], v[130:133]
	v_mfma_f32_16x16x128_f8f6f4 v[122:125], v[10:17], v[210:217], v[122:125]
	v_mfma_f32_16x16x128_f8f6f4 v[114:117], v[2:9], v[218:225], v[114:117]
	v_mfma_f32_16x16x128_f8f6f4 v[106:109], v[10:17], v[218:225], v[106:109]
	v_mfma_f32_16x16x128_f8f6f4 v[150:153], v[18:25], v[194:201], v[150:153]
	v_mfma_f32_16x16x128_f8f6f4 v[142:145], v[26:33], v[194:201], v[142:145]
	v_mfma_f32_16x16x128_f8f6f4 v[134:137], v[18:25], v[202:209], v[134:137]
	v_mfma_f32_16x16x128_f8f6f4 v[126:129], v[26:33], v[202:209], v[126:129]
	v_mfma_f32_16x16x128_f8f6f4 v[118:121], v[18:25], v[210:217], v[118:121]
	v_mfma_f32_16x16x128_f8f6f4 v[110:113], v[26:33], v[210:217], v[110:113]
	v_mfma_f32_16x16x128_f8f6f4 v[102:105], v[18:25], v[218:225], v[102:105]
	v_mfma_f32_16x16x128_f8f6f4 v[98:101], v[26:33], v[218:225], v[98:101]
	s_barrier
	s_add_i32 s26, s26, s38
	v_lshl_add_u64 v[180:181], v[180:181], 0, s[8:9]
	s_mov_b32 m0, s26
	ds_read_b128 v[194:197], v193 offset:49152
	ds_read_b128 v[198:201], v193 offset:50176
	ds_read_b128 v[202:205], v193 offset:51200
	ds_read_b128 v[206:209], v193 offset:52224
	ds_read_b128 v[210:213], v193 offset:53248
	ds_read_b128 v[214:217], v193 offset:54272
	ds_read_b128 v[218:221], v193 offset:55296
	ds_read_b128 v[222:225], v193 offset:56320
	global_load_lds_dwordx4 v[180:181], off
	s_add_i32 m0, s26, 0x2000
	s_add_u32 s26, s30, 0x40080
	v_lshl_add_u64 v[180:181], v[182:183], 0, s[8:9]
	s_addc_u32 s27, s31, 0
	s_add_i32 s30, s54, s38
	global_load_lds_dwordx4 v[180:181], off
	v_lshl_add_u64 v[180:181], s[26:27], 0, v[162:163]
	s_mov_b32 m0, s30
	s_nop 0
	global_load_lds_dwordx4 v[180:181], off
	v_lshl_add_u64 v[180:181], s[26:27], 0, v[164:165]
	s_add_i32 m0, s30, 0x2000
	s_nop 0
	global_load_lds_dwordx4 v[180:181], off
	v_lshl_add_u64 v[180:181], v[184:185], 0, s[8:9]
	s_mov_b32 m0, s44
	s_nop 0
	global_load_lds_dwordx4 v[180:181], off
	v_lshl_add_u64 v[180:181], v[186:187], 0, s[8:9]
	s_mov_b32 m0, s45
	s_nop 0
	global_load_lds_dwordx4 v[180:181], off
	s_waitcnt vmcnt(8)
	s_waitcnt lgkmcnt(0)
	s_barrier
	s_waitcnt lgkmcnt(0)
	v_mfma_f32_16x16x128_f8f6f4 v[86:89], v[2:9], v[194:201], v[86:89]
	v_mfma_f32_16x16x128_f8f6f4 v[82:85], v[10:17], v[194:201], v[82:85]
	v_mfma_f32_16x16x128_f8f6f4 v[70:73], v[2:9], v[202:209], v[70:73]
	v_mfma_f32_16x16x128_f8f6f4 v[66:69], v[10:17], v[202:209], v[66:69]
	v_mfma_f32_16x16x128_f8f6f4 v[54:57], v[2:9], v[210:217], v[54:57]
	v_mfma_f32_16x16x128_f8f6f4 v[50:53], v[10:17], v[210:217], v[50:53]
	v_mfma_f32_16x16x128_f8f6f4 v[38:41], v[2:9], v[218:225], v[38:41]
	v_mfma_f32_16x16x128_f8f6f4 v[34:37], v[10:17], v[218:225], v[34:37]
	v_mfma_f32_16x16x128_f8f6f4 v[94:97], v[18:25], v[194:201], v[94:97]
	v_mfma_f32_16x16x128_f8f6f4 v[90:93], v[26:33], v[194:201], v[90:93]
	v_mfma_f32_16x16x128_f8f6f4 v[78:81], v[18:25], v[202:209], v[78:81]
	v_mfma_f32_16x16x128_f8f6f4 v[74:77], v[26:33], v[202:209], v[74:77]
	v_mfma_f32_16x16x128_f8f6f4 v[62:65], v[18:25], v[210:217], v[62:65]
	v_mfma_f32_16x16x128_f8f6f4 v[58:61], v[26:33], v[210:217], v[58:61]
	v_mfma_f32_16x16x128_f8f6f4 v[46:49], v[18:25], v[218:225], v[46:49]
	v_mfma_f32_16x16x128_f8f6f4 v[42:45], v[26:33], v[218:225], v[42:45]
	s_barrier
	s_add_i32 s53, s53, 2
	s_add_u32 s51, s51, 0x100
	s_addc_u32 s52, s52, 0
	s_cmp_gt_u32 s53, 13
	s_mov_b64 s[26:27], s[28:29]
	s_cbranch_scc0 .LBB0_633

.Lpk5_entry:
	s_mov_b64 s[10:11], s[40:41]
	ds_read_b128 v[18:21], v232
	ds_read_b128 v[22:25], v232 offset:1024
	ds_read_b128 v[26:29], v232 offset:2048
	ds_read_b128 v[30:33], v232 offset:3072
	ds_read_b128 v[2:5], v233
	ds_read_b128 v[6:9], v233 offset:1024
	ds_read_b128 v[10:13], v233 offset:2048
	ds_read_b128 v[14:17], v233 offset:3072
	s_add_u32 s40, s10, 0x100
	s_addc_u32 s41, s11, 0
	s_add_u32 s44, s25, s10
	s_addc_u32 s45, s27, s11
	s_cmpk_eq_i32 s10, 0x700
	s_cselect_b64 s[8:9], -1, 0
	s_and_b64 s[42:43], s[8:9], exec
	s_cselect_b32 s63, 0, s40
	s_cselect_b32 s62, 0, s41
	s_cselect_b32 s43, s29, s45
	s_cselect_b32 s42, s28, s44
	s_add_u32 s44, s12, s63
	v_cndmask_b32_e64 v66, v214, v236, s[8:9]
	s_addc_u32 s45, s13, s62
	v_cndmask_b32_e64 v68, v212, v237, s[8:9]
	v_lshl_add_u64 v[220:221], v[216:217], 0, s[10:11]
	s_add_i32 m0, s35, 0xc000
	s_waitcnt lgkmcnt(0)
	ds_read_b128 v[34:37], v234
	ds_read_b128 v[38:41], v234 offset:1024
	ds_read_b128 v[42:45], v234 offset:2048
	ds_read_b128 v[46:49], v234 offset:3072
	ds_read_b128 v[50:53], v234 offset:4096
	ds_read_b128 v[54:57], v234 offset:5120
	ds_read_b128 v[58:61], v234 offset:6144
	ds_read_b128 v[62:65], v234 offset:7168
	global_load_lds_dwordx4 v[220:221], off
	v_lshl_add_u64 v[220:221], v[218:219], 0, s[10:11]
	s_add_i32 m0, s35, 0xe000
	s_nop 0
	global_load_lds_dwordx4 v[220:221], off
	s_waitcnt vmcnt(8)
	s_waitcnt lgkmcnt(0)
	s_barrier
	s_waitcnt lgkmcnt(0)
	v_mfma_f32_16x16x128_f8f6f4 v[194:197], v[18:25], v[34:41], 0
	v_mfma_f32_16x16x128_f8f6f4 v[190:193], v[26:33], v[34:41], 0
	v_mfma_f32_16x16x128_f8f6f4 v[170:173], v[18:25], v[42:49], 0
	v_mfma_f32_16x16x128_f8f6f4 v[178:181], v[26:33], v[42:49], 0
	v_mfma_f32_16x16x128_f8f6f4 v[162:165], v[18:25], v[50:57], 0
	v_mfma_f32_16x16x128_f8f6f4 v[158:161], v[26:33], v[50:57], 0
	v_mfma_f32_16x16x128_f8f6f4 v[138:141], v[18:25], v[58:65], 0
	v_mfma_f32_16x16x128_f8f6f4 v[146:149], v[26:33], v[58:65], 0
	v_mfma_f32_16x16x128_f8f6f4 v[186:189], v[2:9], v[34:41], 0
	v_mfma_f32_16x16x128_f8f6f4 v[182:185], v[10:17], v[34:41], 0
	v_mfma_f32_16x16x128_f8f6f4 v[166:169], v[2:9], v[42:49], 0
	v_mfma_f32_16x16x128_f8f6f4 v[174:177], v[10:17], v[42:49], 0
	v_mfma_f32_16x16x128_f8f6f4 v[154:157], v[2:9], v[50:57], 0
	v_mfma_f32_16x16x128_f8f6f4 v[150:153], v[10:17], v[50:57], 0
	v_mfma_f32_16x16x128_f8f6f4 v[134:137], v[2:9], v[58:65], 0
	v_mfma_f32_16x16x128_f8f6f4 v[142:145], v[10:17], v[58:65], 0
	s_barrier
	s_add_i32 s10, s54, s46
	v_lshl_add_u64 v[220:221], s[42:43], 0, v[198:199]
	s_mov_b32 m0, s10
	ds_read_b128 v[58:61], v234 offset:16384
	ds_read_b128 v[62:65], v234 offset:17408
	ds_read_b128 v[50:53], v234 offset:18432
	ds_read_b128 v[54:57], v234 offset:19456
	ds_read_b128 v[42:45], v234 offset:20480
	ds_read_b128 v[46:49], v234 offset:21504
	ds_read_b128 v[34:37], v234 offset:22528
	ds_read_b128 v[38:41], v234 offset:23552
	global_load_lds_dwordx4 v[220:221], off
	s_add_i32 m0, s10, 0x2000
	s_add_u32 s10, s42, 0x40000
	v_lshl_add_u64 v[222:223], s[42:43], 0, v[202:203]
	s_addc_u32 s11, s43, 0
	s_add_i32 s62, s55, s46
	global_load_lds_dwordx4 v[222:223], off
	v_lshl_add_u64 v[240:241], s[10:11], 0, v[198:199]
	s_mov_b32 m0, s62
	s_andn2_b64 vcc, exec, s[38:39]
	global_load_lds_dwordx4 v[240:241], off
	v_lshl_add_u64 v[240:241], s[10:11], 0, v[202:203]
	s_add_i32 m0, s62, 0x2000
	v_cmp_ne_u32_e64 s[10:11], 1, v201
	global_load_lds_dwordx4 v[240:241], off
	s_mov_b32 m0, s35
	s_nop 0
	global_load_lds_dwordx4 v66, s[44:45]
	s_mov_b32 m0, s48
	s_nop 0
	global_load_lds_dwordx4 v68, s[44:45]
	s_waitcnt vmcnt(8)
	s_waitcnt lgkmcnt(0)
	s_barrier
	s_cbranch_vccnz .Lpk5_hz
	s_waitcnt lgkmcnt(0)
	v_mfma_f32_16x16x128_f8f6f4 v[130:133], v[18:25], v[58:65], 0
	v_mfma_f32_16x16x128_f8f6f4 v[126:129], v[26:33], v[58:65], 0
	v_mfma_f32_16x16x128_f8f6f4 v[106:109], v[18:25], v[50:57], 0
	v_mfma_f32_16x16x128_f8f6f4 v[114:117], v[26:33], v[50:57], 0
	v_mfma_f32_16x16x128_f8f6f4 v[98:101], v[18:25], v[42:49], 0
	v_mfma_f32_16x16x128_f8f6f4 v[90:93], v[26:33], v[42:49], 0
	v_mfma_f32_16x16x128_f8f6f4 v[70:73], v[18:25], v[34:41], 0
	v_mfma_f32_16x16x128_f8f6f4 v[78:81], v[26:33], v[34:41], 0
	v_mfma_f32_16x16x128_f8f6f4 v[122:125], v[2:9], v[58:65], 0
	v_mfma_f32_16x16x128_f8f6f4 v[118:121], v[10:17], v[58:65], 0
	v_mfma_f32_16x16x128_f8f6f4 v[102:105], v[2:9], v[50:57], 0
	v_mfma_f32_16x16x128_f8f6f4 v[110:113], v[10:17], v[50:57], 0
	v_mfma_f32_16x16x128_f8f6f4 v[94:97], v[2:9], v[42:49], 0
	v_mfma_f32_16x16x128_f8f6f4 v[86:89], v[10:17], v[42:49], 0
	v_mfma_f32_16x16x128_f8f6f4 v[74:77], v[2:9], v[34:41], 0
	v_mfma_f32_16x16x128_f8f6f4 v[82:85], v[10:17], v[34:41], 0
.Lpk5_920:
	v_mov_b32_e32 v69, v67
	v_lshl_add_u64 v[240:241], s[44:45], 0, v[66:67]
	v_lshl_add_u64 v[68:69], s[44:45], 0, v[68:69]
	v_cndmask_b32_e64 v66, v210, v238, s[8:9]
	v_cndmask_b32_e64 v209, v208, v239, s[8:9]
	s_barrier
	s_add_i32 s8, 0, 0x18000
	s_add_i32 s62, 0, 0x1c000
	v_add_u32_e32 v2, s8, v215
	v_add_u32_e32 v14, s62, v215
	ds_read_b128 v[18:21], v2
	ds_read_b128 v[22:25], v2 offset:1024
	ds_read_b128 v[26:29], v2 offset:2048
	ds_read_b128 v[30:33], v2 offset:3072
	ds_read_b128 v[2:5], v14
	ds_read_b128 v[6:9], v14 offset:1024
	ds_read_b128 v[10:13], v14 offset:2048
	ds_read_b128 v[14:17], v14 offset:3072
	s_mov_b32 m0, s49
	s_waitcnt lgkmcnt(0)
	ds_read_b128 v[34:37], v234 offset:32768
	ds_read_b128 v[38:41], v234 offset:33792
	ds_read_b128 v[42:45], v234 offset:34816
	ds_read_b128 v[46:49], v234 offset:35840
	ds_read_b128 v[50:53], v234 offset:36864
	ds_read_b128 v[54:57], v234 offset:37888
	ds_read_b128 v[58:61], v234 offset:38912
	ds_read_b128 v[62:65], v234 offset:39936
	global_load_lds_dwordx4 v66, s[44:45]
	s_mov_b32 m0, s50
	s_nop 0
	global_load_lds_dwordx4 v209, s[44:45]
	s_waitcnt vmcnt(8)
	s_waitcnt lgkmcnt(0)
	s_barrier
	s_waitcnt lgkmcnt(0)
	v_mfma_f32_16x16x128_f8f6f4 v[194:197], v[18:25], v[34:41], v[194:197]
	v_mfma_f32_16x16x128_f8f6f4 v[190:193], v[26:33], v[34:41], v[190:193]
	v_mfma_f32_16x16x128_f8f6f4 v[170:173], v[18:25], v[42:49], v[170:173]
	v_mfma_f32_16x16x128_f8f6f4 v[178:181], v[26:33], v[42:49], v[178:181]
	v_mfma_f32_16x16x128_f8f6f4 v[162:165], v[18:25], v[50:57], v[162:165]
	v_mfma_f32_16x16x128_f8f6f4 v[158:161], v[26:33], v[50:57], v[158:161]
	v_mfma_f32_16x16x128_f8f6f4 v[138:141], v[18:25], v[58:65], v[138:141]
	v_mfma_f32_16x16x128_f8f6f4 v[146:149], v[26:33], v[58:65], v[146:149]
	v_mfma_f32_16x16x128_f8f6f4 v[186:189], v[2:9], v[34:41], v[186:189]
	v_mfma_f32_16x16x128_f8f6f4 v[182:185], v[10:17], v[34:41], v[182:185]
	v_mfma_f32_16x16x128_f8f6f4 v[166:169], v[2:9], v[42:49], v[166:169]
	v_mfma_f32_16x16x128_f8f6f4 v[174:177], v[10:17], v[42:49], v[174:177]
	v_mfma_f32_16x16x128_f8f6f4 v[154:157], v[2:9], v[50:57], v[154:157]
	v_mfma_f32_16x16x128_f8f6f4 v[150:153], v[10:17], v[50:57], v[150:153]
	v_mfma_f32_16x16x128_f8f6f4 v[134:137], v[2:9], v[58:65], v[134:137]
	v_mfma_f32_16x16x128_f8f6f4 v[142:145], v[10:17], v[58:65], v[142:145]
	s_barrier
	s_add_i32 s8, s8, s46
	v_lshl_add_u64 v[220:221], v[220:221], 0, s[4:5]
	s_mov_b32 m0, s8
	ds_read_b128 v[58:61], v234 offset:49152
	ds_read_b128 v[62:65], v234 offset:50176
	ds_read_b128 v[50:53], v234 offset:51200
	ds_read_b128 v[54:57], v234 offset:52224
	ds_read_b128 v[42:45], v234 offset:53248
	ds_read_b128 v[46:49], v234 offset:54272
	ds_read_b128 v[34:37], v234 offset:55296
	ds_read_b128 v[38:41], v234 offset:56320
	global_load_lds_dwordx4 v[220:221], off
	s_add_i32 m0, s8, 0x2000
	s_add_u32 s8, s42, 0x40080
	v_lshl_add_u64 v[220:221], v[222:223], 0, s[4:5]
	s_addc_u32 s9, s43, 0
	s_add_i32 s42, s62, s46
	global_load_lds_dwordx4 v[220:221], off
	v_lshl_add_u64 v[220:221], s[8:9], 0, v[198:199]
	s_mov_b32 m0, s42
	v_lshl_add_u64 v[68:69], v[68:69], 0, s[4:5]
	global_load_lds_dwordx4 v[220:221], off
	v_lshl_add_u64 v[220:221], s[8:9], 0, v[202:203]
	s_add_i32 m0, s42, 0x2000
	s_and_b64 vcc, exec, s[10:11]
	global_load_lds_dwordx4 v[220:221], off
	v_lshl_add_u64 v[220:221], v[240:241], 0, s[4:5]
	s_mov_b32 m0, s51
	s_nop 0
	global_load_lds_dwordx4 v[220:221], off
	s_mov_b32 m0, s52
	s_nop 0
	global_load_lds_dwordx4 v[68:69], off
	s_waitcnt vmcnt(8)
	s_waitcnt lgkmcnt(0)
	s_barrier
	s_cbranch_vccnz .LBB0_917
	s_waitcnt lgkmcnt(0)
	v_mfma_f32_16x16x128_f8f6f4 v[130:133], v[18:25], v[58:65], v[130:133]
	v_mfma_f32_16x16x128_f8f6f4 v[126:129], v[26:33], v[58:65], v[126:129]
	v_mfma_f32_16x16x128_f8f6f4 v[106:109], v[18:25], v[50:57], v[106:109]
	v_mfma_f32_16x16x128_f8f6f4 v[114:117], v[26:33], v[50:57], v[114:117]
	v_mfma_f32_16x16x128_f8f6f4 v[98:101], v[18:25], v[42:49], v[98:101]
	v_mfma_f32_16x16x128_f8f6f4 v[90:93], v[26:33], v[42:49], v[90:93]
	v_mfma_f32_16x16x128_f8f6f4 v[70:73], v[18:25], v[34:41], v[70:73]
	v_mfma_f32_16x16x128_f8f6f4 v[78:81], v[26:33], v[34:41], v[78:81]
	v_mfma_f32_16x16x128_f8f6f4 v[122:125], v[2:9], v[58:65], v[122:125]
	v_mfma_f32_16x16x128_f8f6f4 v[118:121], v[10:17], v[58:65], v[118:121]
	v_mfma_f32_16x16x128_f8f6f4 v[102:105], v[2:9], v[50:57], v[102:105]
	v_mfma_f32_16x16x128_f8f6f4 v[110:113], v[10:17], v[50:57], v[110:113]
	v_mfma_f32_16x16x128_f8f6f4 v[94:97], v[2:9], v[42:49], v[94:97]
	v_mfma_f32_16x16x128_f8f6f4 v[86:89], v[10:17], v[42:49], v[86:89]
	v_mfma_f32_16x16x128_f8f6f4 v[74:77], v[2:9], v[34:41], v[74:77]
	v_mfma_f32_16x16x128_f8f6f4 v[82:85], v[10:17], v[34:41], v[82:85]
	s_branch .LBB0_917

.LBB0_918:
	s_mov_b64 s[10:11], s[40:41]
	ds_read_b128 v[18:21], v232
	ds_read_b128 v[22:25], v232 offset:1024
	ds_read_b128 v[26:29], v232 offset:2048
	ds_read_b128 v[30:33], v232 offset:3072
	ds_read_b128 v[2:5], v233
	ds_read_b128 v[6:9], v233 offset:1024
	ds_read_b128 v[10:13], v233 offset:2048
	ds_read_b128 v[14:17], v233 offset:3072
	s_add_u32 s40, s10, 0x100
	s_addc_u32 s41, s11, 0
	s_add_u32 s44, s25, s10
	s_addc_u32 s45, s27, s11
	s_cmpk_eq_i32 s10, 0x700
	s_cselect_b64 s[8:9], -1, 0
	s_and_b64 s[42:43], s[8:9], exec
	s_cselect_b32 s63, 0, s40
	s_cselect_b32 s62, 0, s41
	s_cselect_b32 s43, s29, s45
	s_cselect_b32 s42, s28, s44
	s_add_u32 s44, s12, s63
	v_cndmask_b32_e64 v66, v214, v236, s[8:9]
	s_addc_u32 s45, s13, s62
	v_cndmask_b32_e64 v68, v212, v237, s[8:9]
	v_lshl_add_u64 v[220:221], v[216:217], 0, s[10:11]
	s_add_i32 m0, s35, 0xc000
	s_waitcnt lgkmcnt(0)
	ds_read_b128 v[34:37], v234
	ds_read_b128 v[38:41], v234 offset:1024
	ds_read_b128 v[42:45], v234 offset:2048
	ds_read_b128 v[46:49], v234 offset:3072
	ds_read_b128 v[50:53], v234 offset:4096
	ds_read_b128 v[54:57], v234 offset:5120
	ds_read_b128 v[58:61], v234 offset:6144
	ds_read_b128 v[62:65], v234 offset:7168
	global_load_lds_dwordx4 v[220:221], off
	v_lshl_add_u64 v[220:221], v[218:219], 0, s[10:11]
	s_add_i32 m0, s35, 0xe000
	s_nop 0
	global_load_lds_dwordx4 v[220:221], off
	s_waitcnt vmcnt(8)
	s_waitcnt lgkmcnt(0)
	s_barrier
	s_waitcnt lgkmcnt(0)
	v_mfma_f32_16x16x128_f8f6f4 v[194:197], v[18:25], v[34:41], v[194:197]
	v_mfma_f32_16x16x128_f8f6f4 v[190:193], v[26:33], v[34:41], v[190:193]
	v_mfma_f32_16x16x128_f8f6f4 v[170:173], v[18:25], v[42:49], v[170:173]
	v_mfma_f32_16x16x128_f8f6f4 v[178:181], v[26:33], v[42:49], v[178:181]
	v_mfma_f32_16x16x128_f8f6f4 v[162:165], v[18:25], v[50:57], v[162:165]
	v_mfma_f32_16x16x128_f8f6f4 v[158:161], v[26:33], v[50:57], v[158:161]
	v_mfma_f32_16x16x128_f8f6f4 v[138:141], v[18:25], v[58:65], v[138:141]
	v_mfma_f32_16x16x128_f8f6f4 v[146:149], v[26:33], v[58:65], v[146:149]
	v_mfma_f32_16x16x128_f8f6f4 v[186:189], v[2:9], v[34:41], v[186:189]
	v_mfma_f32_16x16x128_f8f6f4 v[182:185], v[10:17], v[34:41], v[182:185]
	v_mfma_f32_16x16x128_f8f6f4 v[166:169], v[2:9], v[42:49], v[166:169]
	v_mfma_f32_16x16x128_f8f6f4 v[174:177], v[10:17], v[42:49], v[174:177]
	v_mfma_f32_16x16x128_f8f6f4 v[154:157], v[2:9], v[50:57], v[154:157]
	v_mfma_f32_16x16x128_f8f6f4 v[150:153], v[10:17], v[50:57], v[150:153]
	v_mfma_f32_16x16x128_f8f6f4 v[134:137], v[2:9], v[58:65], v[134:137]
	v_mfma_f32_16x16x128_f8f6f4 v[142:145], v[10:17], v[58:65], v[142:145]
	s_barrier
	s_add_i32 s10, s54, s46
	v_lshl_add_u64 v[220:221], s[42:43], 0, v[198:199]
	s_mov_b32 m0, s10
	ds_read_b128 v[58:61], v234 offset:16384
	ds_read_b128 v[62:65], v234 offset:17408
	ds_read_b128 v[50:53], v234 offset:18432
	ds_read_b128 v[54:57], v234 offset:19456
	ds_read_b128 v[42:45], v234 offset:20480
	ds_read_b128 v[46:49], v234 offset:21504
	ds_read_b128 v[34:37], v234 offset:22528
	ds_read_b128 v[38:41], v234 offset:23552
	global_load_lds_dwordx4 v[220:221], off
	s_add_i32 m0, s10, 0x2000
	s_add_u32 s10, s42, 0x40000
	v_lshl_add_u64 v[222:223], s[42:43], 0, v[202:203]
	s_addc_u32 s11, s43, 0
	s_add_i32 s62, s55, s46
	global_load_lds_dwordx4 v[222:223], off
	v_lshl_add_u64 v[240:241], s[10:11], 0, v[198:199]
	s_mov_b32 m0, s62
	s_andn2_b64 vcc, exec, s[38:39]
	global_load_lds_dwordx4 v[240:241], off
	v_lshl_add_u64 v[240:241], s[10:11], 0, v[202:203]
	s_add_i32 m0, s62, 0x2000
	v_cmp_ne_u32_e64 s[10:11], 1, v201
	global_load_lds_dwordx4 v[240:241], off
	s_mov_b32 m0, s35
	s_nop 0
	global_load_lds_dwordx4 v66, s[44:45]
	s_mov_b32 m0, s48
	s_nop 0
	global_load_lds_dwordx4 v68, s[44:45]
	s_waitcnt vmcnt(8)
	s_waitcnt lgkmcnt(0)
	s_barrier
	s_cbranch_vccnz .LBB0_920
	s_waitcnt lgkmcnt(0)
	v_mfma_f32_16x16x128_f8f6f4 v[130:133], v[18:25], v[58:65], v[130:133]
	v_mfma_f32_16x16x128_f8f6f4 v[126:129], v[26:33], v[58:65], v[126:129]
	v_mfma_f32_16x16x128_f8f6f4 v[106:109], v[18:25], v[50:57], v[106:109]
	v_mfma_f32_16x16x128_f8f6f4 v[114:117], v[26:33], v[50:57], v[114:117]
	v_mfma_f32_16x16x128_f8f6f4 v[98:101], v[18:25], v[42:49], v[98:101]
	v_mfma_f32_16x16x128_f8f6f4 v[90:93], v[26:33], v[42:49], v[90:93]
	v_mfma_f32_16x16x128_f8f6f4 v[70:73], v[18:25], v[34:41], v[70:73]
	v_mfma_f32_16x16x128_f8f6f4 v[78:81], v[26:33], v[34:41], v[78:81]
	v_mfma_f32_16x16x128_f8f6f4 v[122:125], v[2:9], v[58:65], v[122:125]
	v_mfma_f32_16x16x128_f8f6f4 v[118:121], v[10:17], v[58:65], v[118:121]
	v_mfma_f32_16x16x128_f8f6f4 v[102:105], v[2:9], v[50:57], v[102:105]
	v_mfma_f32_16x16x128_f8f6f4 v[110:113], v[10:17], v[50:57], v[110:113]
	v_mfma_f32_16x16x128_f8f6f4 v[94:97], v[2:9], v[42:49], v[94:97]
	v_mfma_f32_16x16x128_f8f6f4 v[86:89], v[10:17], v[42:49], v[86:89]
	v_mfma_f32_16x16x128_f8f6f4 v[74:77], v[2:9], v[34:41], v[74:77]
	v_mfma_f32_16x16x128_f8f6f4 v[82:85], v[10:17], v[34:41], v[82:85]

.Lpk6_entry:
	s_mov_b64 s[10:11], s[38:39]
	ds_read_b128 v[18:21], v232
	ds_read_b128 v[22:25], v232 offset:1024
	ds_read_b128 v[26:29], v232 offset:2048
	ds_read_b128 v[30:33], v232 offset:3072
	ds_read_b128 v[2:5], v233
	ds_read_b128 v[6:9], v233 offset:1024
	ds_read_b128 v[10:13], v233 offset:2048
	ds_read_b128 v[14:17], v233 offset:3072
	s_add_u32 s38, s10, 0x100
	s_addc_u32 s39, s11, 0
	s_add_u32 s42, s25, s10
	s_addc_u32 s43, s27, s11
	s_cmpk_eq_i32 s10, 0x700
	s_cselect_b64 s[8:9], -1, 0
	s_and_b64 s[40:41], s[8:9], exec
	s_cselect_b32 s63, 0, s38
	s_cselect_b32 s62, 0, s39
	s_cselect_b32 s41, s29, s43
	s_cselect_b32 s40, s28, s42
	s_add_u32 s42, s12, s63
	v_cndmask_b32_e64 v66, v214, v236, s[8:9]
	s_addc_u32 s43, s13, s62
	v_cndmask_b32_e64 v68, v212, v237, s[8:9]
	v_lshl_add_u64 v[220:221], v[216:217], 0, s[10:11]
	s_add_i32 m0, s31, 0xc000
	s_waitcnt lgkmcnt(0)
	ds_read_b128 v[34:37], v234
	ds_read_b128 v[38:41], v234 offset:1024
	ds_read_b128 v[42:45], v234 offset:2048
	ds_read_b128 v[46:49], v234 offset:3072
	ds_read_b128 v[50:53], v234 offset:4096
	ds_read_b128 v[54:57], v234 offset:5120
	ds_read_b128 v[58:61], v234 offset:6144
	ds_read_b128 v[62:65], v234 offset:7168
	global_load_lds_dwordx4 v[220:221], off
	v_lshl_add_u64 v[220:221], v[218:219], 0, s[10:11]
	s_add_i32 m0, s31, 0xe000
	s_nop 0
	global_load_lds_dwordx4 v[220:221], off
	s_waitcnt vmcnt(8)
	s_waitcnt lgkmcnt(0)
	s_barrier
	s_waitcnt lgkmcnt(0)
	v_mfma_f32_16x16x128_f8f6f4 v[194:197], v[18:25], v[34:41], 0
	v_mfma_f32_16x16x128_f8f6f4 v[190:193], v[26:33], v[34:41], 0
	v_mfma_f32_16x16x128_f8f6f4 v[170:173], v[18:25], v[42:49], 0
	v_mfma_f32_16x16x128_f8f6f4 v[178:181], v[26:33], v[42:49], 0
	v_mfma_f32_16x16x128_f8f6f4 v[162:165], v[18:25], v[50:57], 0
	v_mfma_f32_16x16x128_f8f6f4 v[158:161], v[26:33], v[50:57], 0
	v_mfma_f32_16x16x128_f8f6f4 v[138:141], v[18:25], v[58:65], 0
	v_mfma_f32_16x16x128_f8f6f4 v[146:149], v[26:33], v[58:65], 0
	v_mfma_f32_16x16x128_f8f6f4 v[186:189], v[2:9], v[34:41], 0
	v_mfma_f32_16x16x128_f8f6f4 v[182:185], v[10:17], v[34:41], 0
	v_mfma_f32_16x16x128_f8f6f4 v[166:169], v[2:9], v[42:49], 0
	v_mfma_f32_16x16x128_f8f6f4 v[174:177], v[10:17], v[42:49], 0
	v_mfma_f32_16x16x128_f8f6f4 v[154:157], v[2:9], v[50:57], 0
	v_mfma_f32_16x16x128_f8f6f4 v[150:153], v[10:17], v[50:57], 0
	v_mfma_f32_16x16x128_f8f6f4 v[134:137], v[2:9], v[58:65], 0
	v_mfma_f32_16x16x128_f8f6f4 v[142:145], v[10:17], v[58:65], 0
	s_barrier
	s_add_i32 s10, s52, s44
	v_lshl_add_u64 v[220:221], s[40:41], 0, v[202:203]
	s_mov_b32 m0, s10
	ds_read_b128 v[58:61], v234 offset:16384
	ds_read_b128 v[62:65], v234 offset:17408
	ds_read_b128 v[50:53], v234 offset:18432
	ds_read_b128 v[54:57], v234 offset:19456
	ds_read_b128 v[42:45], v234 offset:20480
	ds_read_b128 v[46:49], v234 offset:21504
	ds_read_b128 v[34:37], v234 offset:22528
	ds_read_b128 v[38:41], v234 offset:23552
	global_load_lds_dwordx4 v[220:221], off
	s_add_i32 m0, s10, 0x2000
	s_add_u32 s10, s40, 0x40000
	v_lshl_add_u64 v[222:223], s[40:41], 0, v[198:199]
	s_addc_u32 s11, s41, 0
	s_add_i32 s62, s53, s44
	global_load_lds_dwordx4 v[222:223], off
	v_lshl_add_u64 v[240:241], s[10:11], 0, v[202:203]
	s_mov_b32 m0, s62
	s_andn2_b64 vcc, exec, s[36:37]
	global_load_lds_dwordx4 v[240:241], off
	v_lshl_add_u64 v[240:241], s[10:11], 0, v[198:199]
	s_add_i32 m0, s62, 0x2000
	v_cmp_ne_u32_e64 s[10:11], 1, v201
	global_load_lds_dwordx4 v[240:241], off
	s_mov_b32 m0, s31
	s_nop 0
	global_load_lds_dwordx4 v66, s[42:43]
	s_mov_b32 m0, s46
	s_nop 0
	global_load_lds_dwordx4 v68, s[42:43]
	s_waitcnt vmcnt(8)
	s_waitcnt lgkmcnt(0)
	s_barrier
	s_cbranch_vccnz .Lpk6_hz
	s_waitcnt lgkmcnt(0)
	v_mfma_f32_16x16x128_f8f6f4 v[130:133], v[18:25], v[58:65], 0
	v_mfma_f32_16x16x128_f8f6f4 v[126:129], v[26:33], v[58:65], 0
	v_mfma_f32_16x16x128_f8f6f4 v[106:109], v[18:25], v[50:57], 0
	v_mfma_f32_16x16x128_f8f6f4 v[114:117], v[26:33], v[50:57], 0
	v_mfma_f32_16x16x128_f8f6f4 v[98:101], v[18:25], v[42:49], 0
	v_mfma_f32_16x16x128_f8f6f4 v[90:93], v[26:33], v[42:49], 0
	v_mfma_f32_16x16x128_f8f6f4 v[70:73], v[18:25], v[34:41], 0
	v_mfma_f32_16x16x128_f8f6f4 v[78:81], v[26:33], v[34:41], 0
	v_mfma_f32_16x16x128_f8f6f4 v[122:125], v[2:9], v[58:65], 0
	v_mfma_f32_16x16x128_f8f6f4 v[118:121], v[10:17], v[58:65], 0
	v_mfma_f32_16x16x128_f8f6f4 v[102:105], v[2:9], v[50:57], 0
	v_mfma_f32_16x16x128_f8f6f4 v[110:113], v[10:17], v[50:57], 0
	v_mfma_f32_16x16x128_f8f6f4 v[94:97], v[2:9], v[42:49], 0
	v_mfma_f32_16x16x128_f8f6f4 v[86:89], v[10:17], v[42:49], 0
	v_mfma_f32_16x16x128_f8f6f4 v[74:77], v[2:9], v[34:41], 0
	v_mfma_f32_16x16x128_f8f6f4 v[82:85], v[10:17], v[34:41], 0
.Lpk6_957:
	v_mov_b32_e32 v69, v67
	v_lshl_add_u64 v[240:241], s[42:43], 0, v[66:67]
	v_lshl_add_u64 v[68:69], s[42:43], 0, v[68:69]
	v_cndmask_b32_e64 v66, v210, v238, s[8:9]
	v_cndmask_b32_e64 v209, v208, v239, s[8:9]
	s_barrier
	s_add_i32 s8, 0, 0x18000
	s_add_i32 s62, 0, 0x1c000
	v_add_u32_e32 v2, s8, v215
	v_add_u32_e32 v14, s62, v215
	ds_read_b128 v[18:21], v2
	ds_read_b128 v[22:25], v2 offset:1024
	ds_read_b128 v[26:29], v2 offset:2048
	ds_read_b128 v[30:33], v2 offset:3072
	ds_read_b128 v[2:5], v14
	ds_read_b128 v[6:9], v14 offset:1024
	ds_read_b128 v[10:13], v14 offset:2048
	ds_read_b128 v[14:17], v14 offset:3072
	s_mov_b32 m0, s47
	s_waitcnt lgkmcnt(0)
	ds_read_b128 v[34:37], v234 offset:32768
	ds_read_b128 v[38:41], v234 offset:33792
	ds_read_b128 v[42:45], v234 offset:34816
	ds_read_b128 v[46:49], v234 offset:35840
	ds_read_b128 v[50:53], v234 offset:36864
	ds_read_b128 v[54:57], v234 offset:37888
	ds_read_b128 v[58:61], v234 offset:38912
	ds_read_b128 v[62:65], v234 offset:39936
	global_load_lds_dwordx4 v66, s[42:43]
	s_mov_b32 m0, s48
	s_nop 0
	global_load_lds_dwordx4 v209, s[42:43]
	s_waitcnt vmcnt(8)
	s_waitcnt lgkmcnt(0)
	s_barrier
	s_waitcnt lgkmcnt(0)
	v_mfma_f32_16x16x128_f8f6f4 v[194:197], v[18:25], v[34:41], v[194:197]
	v_mfma_f32_16x16x128_f8f6f4 v[190:193], v[26:33], v[34:41], v[190:193]
	v_mfma_f32_16x16x128_f8f6f4 v[170:173], v[18:25], v[42:49], v[170:173]
	v_mfma_f32_16x16x128_f8f6f4 v[178:181], v[26:33], v[42:49], v[178:181]
	v_mfma_f32_16x16x128_f8f6f4 v[162:165], v[18:25], v[50:57], v[162:165]
	v_mfma_f32_16x16x128_f8f6f4 v[158:161], v[26:33], v[50:57], v[158:161]
	v_mfma_f32_16x16x128_f8f6f4 v[138:141], v[18:25], v[58:65], v[138:141]
	v_mfma_f32_16x16x128_f8f6f4 v[146:149], v[26:33], v[58:65], v[146:149]
	v_mfma_f32_16x16x128_f8f6f4 v[186:189], v[2:9], v[34:41], v[186:189]
	v_mfma_f32_16x16x128_f8f6f4 v[182:185], v[10:17], v[34:41], v[182:185]
	v_mfma_f32_16x16x128_f8f6f4 v[166:169], v[2:9], v[42:49], v[166:169]
	v_mfma_f32_16x16x128_f8f6f4 v[174:177], v[10:17], v[42:49], v[174:177]
	v_mfma_f32_16x16x128_f8f6f4 v[154:157], v[2:9], v[50:57], v[154:157]
	v_mfma_f32_16x16x128_f8f6f4 v[150:153], v[10:17], v[50:57], v[150:153]
	v_mfma_f32_16x16x128_f8f6f4 v[134:137], v[2:9], v[58:65], v[134:137]
	v_mfma_f32_16x16x128_f8f6f4 v[142:145], v[10:17], v[58:65], v[142:145]
	s_barrier
	s_add_i32 s8, s8, s44
	v_lshl_add_u64 v[220:221], v[220:221], 0, s[4:5]
	s_mov_b32 m0, s8
	ds_read_b128 v[58:61], v234 offset:49152
	ds_read_b128 v[62:65], v234 offset:50176
	ds_read_b128 v[50:53], v234 offset:51200
	ds_read_b128 v[54:57], v234 offset:52224
	ds_read_b128 v[42:45], v234 offset:53248
	ds_read_b128 v[46:49], v234 offset:54272
	ds_read_b128 v[34:37], v234 offset:55296
	ds_read_b128 v[38:41], v234 offset:56320
	global_load_lds_dwordx4 v[220:221], off
	s_add_i32 m0, s8, 0x2000
	s_add_u32 s8, s40, 0x40080
	v_lshl_add_u64 v[220:221], v[222:223], 0, s[4:5]
	s_addc_u32 s9, s41, 0
	s_add_i32 s40, s62, s44
	global_load_lds_dwordx4 v[220:221], off
	v_lshl_add_u64 v[220:221], s[8:9], 0, v[202:203]
	s_mov_b32 m0, s40
	v_lshl_add_u64 v[68:69], v[68:69], 0, s[4:5]
	global_load_lds_dwordx4 v[220:221], off
	v_lshl_add_u64 v[220:221], s[8:9], 0, v[198:199]
	s_add_i32 m0, s40, 0x2000
	s_and_b64 vcc, exec, s[10:11]
	global_load_lds_dwordx4 v[220:221], off
	v_lshl_add_u64 v[220:221], v[240:241], 0, s[4:5]
	s_mov_b32 m0, s49
	s_nop 0
	global_load_lds_dwordx4 v[220:221], off
	s_mov_b32 m0, s50
	s_nop 0
	global_load_lds_dwordx4 v[68:69], off
	s_waitcnt vmcnt(8)
	s_waitcnt lgkmcnt(0)
	s_barrier
	s_cbranch_vccnz .LBB0_954
	s_waitcnt lgkmcnt(0)
	v_mfma_f32_16x16x128_f8f6f4 v[130:133], v[18:25], v[58:65], v[130:133]
	v_mfma_f32_16x16x128_f8f6f4 v[126:129], v[26:33], v[58:65], v[126:129]
	v_mfma_f32_16x16x128_f8f6f4 v[106:109], v[18:25], v[50:57], v[106:109]
	v_mfma_f32_16x16x128_f8f6f4 v[114:117], v[26:33], v[50:57], v[114:117]
	v_mfma_f32_16x16x128_f8f6f4 v[98:101], v[18:25], v[42:49], v[98:101]
	v_mfma_f32_16x16x128_f8f6f4 v[90:93], v[26:33], v[42:49], v[90:93]
	v_mfma_f32_16x16x128_f8f6f4 v[70:73], v[18:25], v[34:41], v[70:73]
	v_mfma_f32_16x16x128_f8f6f4 v[78:81], v[26:33], v[34:41], v[78:81]
	v_mfma_f32_16x16x128_f8f6f4 v[122:125], v[2:9], v[58:65], v[122:125]
	v_mfma_f32_16x16x128_f8f6f4 v[118:121], v[10:17], v[58:65], v[118:121]
	v_mfma_f32_16x16x128_f8f6f4 v[102:105], v[2:9], v[50:57], v[102:105]
	v_mfma_f32_16x16x128_f8f6f4 v[110:113], v[10:17], v[50:57], v[110:113]
	v_mfma_f32_16x16x128_f8f6f4 v[94:97], v[2:9], v[42:49], v[94:97]
	v_mfma_f32_16x16x128_f8f6f4 v[86:89], v[10:17], v[42:49], v[86:89]
	v_mfma_f32_16x16x128_f8f6f4 v[74:77], v[2:9], v[34:41], v[74:77]
	v_mfma_f32_16x16x128_f8f6f4 v[82:85], v[10:17], v[34:41], v[82:85]
	s_branch .LBB0_954

.LBB0_955:
	s_mov_b64 s[10:11], s[38:39]
	ds_read_b128 v[18:21], v232
	ds_read_b128 v[22:25], v232 offset:1024
	ds_read_b128 v[26:29], v232 offset:2048
	ds_read_b128 v[30:33], v232 offset:3072
	ds_read_b128 v[2:5], v233
	ds_read_b128 v[6:9], v233 offset:1024
	ds_read_b128 v[10:13], v233 offset:2048
	ds_read_b128 v[14:17], v233 offset:3072
	s_add_u32 s38, s10, 0x100
	s_addc_u32 s39, s11, 0
	s_add_u32 s42, s25, s10
	s_addc_u32 s43, s27, s11
	s_cmpk_eq_i32 s10, 0x700
	s_cselect_b64 s[8:9], -1, 0
	s_and_b64 s[40:41], s[8:9], exec
	s_cselect_b32 s63, 0, s38
	s_cselect_b32 s62, 0, s39
	s_cselect_b32 s41, s29, s43
	s_cselect_b32 s40, s28, s42
	s_add_u32 s42, s12, s63
	v_cndmask_b32_e64 v66, v214, v236, s[8:9]
	s_addc_u32 s43, s13, s62
	v_cndmask_b32_e64 v68, v212, v237, s[8:9]
	v_lshl_add_u64 v[220:221], v[216:217], 0, s[10:11]
	s_add_i32 m0, s31, 0xc000
	s_waitcnt lgkmcnt(0)
	ds_read_b128 v[34:37], v234
	ds_read_b128 v[38:41], v234 offset:1024
	ds_read_b128 v[42:45], v234 offset:2048
	ds_read_b128 v[46:49], v234 offset:3072
	ds_read_b128 v[50:53], v234 offset:4096
	ds_read_b128 v[54:57], v234 offset:5120
	ds_read_b128 v[58:61], v234 offset:6144
	ds_read_b128 v[62:65], v234 offset:7168
	global_load_lds_dwordx4 v[220:221], off
	v_lshl_add_u64 v[220:221], v[218:219], 0, s[10:11]
	s_add_i32 m0, s31, 0xe000
	s_nop 0
	global_load_lds_dwordx4 v[220:221], off
	s_waitcnt vmcnt(8)
	s_waitcnt lgkmcnt(0)
	s_barrier
	s_waitcnt lgkmcnt(0)
	v_mfma_f32_16x16x128_f8f6f4 v[194:197], v[18:25], v[34:41], v[194:197]
	v_mfma_f32_16x16x128_f8f6f4 v[190:193], v[26:33], v[34:41], v[190:193]
	v_mfma_f32_16x16x128_f8f6f4 v[170:173], v[18:25], v[42:49], v[170:173]
	v_mfma_f32_16x16x128_f8f6f4 v[178:181], v[26:33], v[42:49], v[178:181]
	v_mfma_f32_16x16x128_f8f6f4 v[162:165], v[18:25], v[50:57], v[162:165]
	v_mfma_f32_16x16x128_f8f6f4 v[158:161], v[26:33], v[50:57], v[158:161]
	v_mfma_f32_16x16x128_f8f6f4 v[138:141], v[18:25], v[58:65], v[138:141]
	v_mfma_f32_16x16x128_f8f6f4 v[146:149], v[26:33], v[58:65], v[146:149]
	v_mfma_f32_16x16x128_f8f6f4 v[186:189], v[2:9], v[34:41], v[186:189]
	v_mfma_f32_16x16x128_f8f6f4 v[182:185], v[10:17], v[34:41], v[182:185]
	v_mfma_f32_16x16x128_f8f6f4 v[166:169], v[2:9], v[42:49], v[166:169]
	v_mfma_f32_16x16x128_f8f6f4 v[174:177], v[10:17], v[42:49], v[174:177]
	v_mfma_f32_16x16x128_f8f6f4 v[154:157], v[2:9], v[50:57], v[154:157]
	v_mfma_f32_16x16x128_f8f6f4 v[150:153], v[10:17], v[50:57], v[150:153]
	v_mfma_f32_16x16x128_f8f6f4 v[134:137], v[2:9], v[58:65], v[134:137]
	v_mfma_f32_16x16x128_f8f6f4 v[142:145], v[10:17], v[58:65], v[142:145]
	s_barrier
	s_add_i32 s10, s52, s44
	v_lshl_add_u64 v[220:221], s[40:41], 0, v[202:203]
	s_mov_b32 m0, s10
	ds_read_b128 v[58:61], v234 offset:16384
	ds_read_b128 v[62:65], v234 offset:17408
	ds_read_b128 v[50:53], v234 offset:18432
	ds_read_b128 v[54:57], v234 offset:19456
	ds_read_b128 v[42:45], v234 offset:20480
	ds_read_b128 v[46:49], v234 offset:21504
	ds_read_b128 v[34:37], v234 offset:22528
	ds_read_b128 v[38:41], v234 offset:23552
	global_load_lds_dwordx4 v[220:221], off
	s_add_i32 m0, s10, 0x2000
	s_add_u32 s10, s40, 0x40000
	v_lshl_add_u64 v[222:223], s[40:41], 0, v[198:199]
	s_addc_u32 s11, s41, 0
	s_add_i32 s62, s53, s44
	global_load_lds_dwordx4 v[222:223], off
	v_lshl_add_u64 v[240:241], s[10:11], 0, v[202:203]
	s_mov_b32 m0, s62
	s_andn2_b64 vcc, exec, s[36:37]
	global_load_lds_dwordx4 v[240:241], off
	v_lshl_add_u64 v[240:241], s[10:11], 0, v[198:199]
	s_add_i32 m0, s62, 0x2000
	v_cmp_ne_u32_e64 s[10:11], 1, v201
	global_load_lds_dwordx4 v[240:241], off
	s_mov_b32 m0, s31
	s_nop 0
	global_load_lds_dwordx4 v66, s[42:43]
	s_mov_b32 m0, s46
	s_nop 0
	global_load_lds_dwordx4 v68, s[42:43]
	s_waitcnt vmcnt(8)
	s_waitcnt lgkmcnt(0)
	s_barrier
	s_cbranch_vccnz .LBB0_957
	s_waitcnt lgkmcnt(0)
	v_mfma_f32_16x16x128_f8f6f4 v[130:133], v[18:25], v[58:65], v[130:133]
	v_mfma_f32_16x16x128_f8f6f4 v[126:129], v[26:33], v[58:65], v[126:129]
	v_mfma_f32_16x16x128_f8f6f4 v[106:109], v[18:25], v[50:57], v[106:109]
	v_mfma_f32_16x16x128_f8f6f4 v[114:117], v[26:33], v[50:57], v[114:117]
	v_mfma_f32_16x16x128_f8f6f4 v[98:101], v[18:25], v[42:49], v[98:101]
	v_mfma_f32_16x16x128_f8f6f4 v[90:93], v[26:33], v[42:49], v[90:93]
	v_mfma_f32_16x16x128_f8f6f4 v[70:73], v[18:25], v[34:41], v[70:73]
	v_mfma_f32_16x16x128_f8f6f4 v[78:81], v[26:33], v[34:41], v[78:81]
	v_mfma_f32_16x16x128_f8f6f4 v[122:125], v[2:9], v[58:65], v[122:125]
	v_mfma_f32_16x16x128_f8f6f4 v[118:121], v[10:17], v[58:65], v[118:121]
	v_mfma_f32_16x16x128_f8f6f4 v[102:105], v[2:9], v[50:57], v[102:105]
	v_mfma_f32_16x16x128_f8f6f4 v[110:113], v[10:17], v[50:57], v[110:113]
	v_mfma_f32_16x16x128_f8f6f4 v[94:97], v[2:9], v[42:49], v[94:97]
	v_mfma_f32_16x16x128_f8f6f4 v[86:89], v[10:17], v[42:49], v[86:89]
	v_mfma_f32_16x16x128_f8f6f4 v[74:77], v[2:9], v[34:41], v[74:77]
	v_mfma_f32_16x16x128_f8f6f4 v[82:85], v[10:17], v[34:41], v[82:85]

.Lpk7_entry:
	ds_read_b128 v[18:21], v239
	ds_read_b128 v[22:25], v239 offset:1024
	ds_read_b128 v[26:29], v239 offset:2048
	ds_read_b128 v[30:33], v239 offset:3072
	ds_read_b128 v[2:5], v240
	ds_read_b128 v[6:9], v240 offset:1024
	ds_read_b128 v[10:13], v240 offset:2048
	ds_read_b128 v[14:17], v240 offset:3072
	s_mov_b64 s[8:9], s[28:29]
	s_add_u32 s28, s8, 0x100
	s_addc_u32 s29, s9, 0
	s_cmp_eq_u32 s63, 12
	s_cselect_b32 s39, s23, s29
	s_cselect_b32 s38, s22, s28
	s_cselect_b32 s37, s25, s21
	s_cselect_b32 s36, s24, s19
	v_lshl_add_u64 v[68:69], s[8:9], 0, v[216:217]
	s_add_i32 m0, s27, 0xc000
	s_waitcnt lgkmcnt(0)
	ds_read_b128 v[34:37], v241
	ds_read_b128 v[38:41], v241 offset:1024
	ds_read_b128 v[42:45], v241 offset:2048
	ds_read_b128 v[46:49], v241 offset:3072
	ds_read_b128 v[50:53], v241 offset:4096
	ds_read_b128 v[54:57], v241 offset:5120
	ds_read_b128 v[58:61], v241 offset:6144
	ds_read_b128 v[62:65], v241 offset:7168
	global_load_lds_dwordx4 v[68:69], off
	v_lshl_add_u64 v[68:69], s[8:9], 0, v[218:219]
	s_add_i32 m0, s27, 0xe000
	s_nop 0
	global_load_lds_dwordx4 v[68:69], off
	s_waitcnt vmcnt(8)
	s_waitcnt lgkmcnt(0)
	s_barrier
	s_waitcnt lgkmcnt(0)
	v_mfma_f32_16x16x128_f8f6f4 v[194:197], v[18:25], v[34:41], 0
	v_mfma_f32_16x16x128_f8f6f4 v[190:193], v[26:33], v[34:41], 0
	v_mfma_f32_16x16x128_f8f6f4 v[174:177], v[18:25], v[42:49], 0
	v_mfma_f32_16x16x128_f8f6f4 v[182:185], v[26:33], v[42:49], 0
	v_mfma_f32_16x16x128_f8f6f4 v[166:169], v[18:25], v[50:57], 0
	v_mfma_f32_16x16x128_f8f6f4 v[158:161], v[26:33], v[50:57], 0
	v_mfma_f32_16x16x128_f8f6f4 v[142:145], v[18:25], v[58:65], 0
	v_mfma_f32_16x16x128_f8f6f4 v[150:153], v[26:33], v[58:65], 0
	v_mfma_f32_16x16x128_f8f6f4 v[186:189], v[2:9], v[34:41], 0
	v_mfma_f32_16x16x128_f8f6f4 v[178:181], v[10:17], v[34:41], 0
	v_mfma_f32_16x16x128_f8f6f4 v[162:165], v[2:9], v[42:49], 0
	v_mfma_f32_16x16x128_f8f6f4 v[170:173], v[10:17], v[42:49], 0
	v_mfma_f32_16x16x128_f8f6f4 v[154:157], v[2:9], v[50:57], 0
	v_mfma_f32_16x16x128_f8f6f4 v[146:149], v[10:17], v[50:57], 0
	v_mfma_f32_16x16x128_f8f6f4 v[138:141], v[2:9], v[58:65], 0
	v_mfma_f32_16x16x128_f8f6f4 v[134:137], v[10:17], v[58:65], 0
	s_barrier
	s_add_i32 s8, s54, s41
	v_lshl_add_u64 v[68:69], s[36:37], 0, v[202:203]
	s_mov_b32 m0, s8
	ds_read_b128 v[58:61], v241 offset:16384
	ds_read_b128 v[62:65], v241 offset:17408
	ds_read_b128 v[50:53], v241 offset:18432
	ds_read_b128 v[54:57], v241 offset:19456
	ds_read_b128 v[42:45], v241 offset:20480
	ds_read_b128 v[46:49], v241 offset:21504
	ds_read_b128 v[34:37], v241 offset:22528
	ds_read_b128 v[38:41], v241 offset:23552
	global_load_lds_dwordx4 v[68:69], off
	s_add_i32 m0, s8, 0x2000
	s_add_u32 s8, s36, 0x40000
	v_lshl_add_u64 v[220:221], s[36:37], 0, v[204:205]
	s_addc_u32 s9, s37, 0
	s_add_i32 s64, s55, s41
	global_load_lds_dwordx4 v[220:221], off
	v_lshl_add_u64 v[222:223], s[8:9], 0, v[202:203]
	s_mov_b32 m0, s64
	v_lshl_add_u64 v[224:225], s[38:39], 0, v[208:209]
	global_load_lds_dwordx4 v[222:223], off
	v_lshl_add_u64 v[222:223], s[8:9], 0, v[204:205]
	s_add_i32 m0, s64, 0x2000
	v_cmp_ne_u32_e64 s[8:9], 1, v242
	global_load_lds_dwordx4 v[222:223], off
	v_lshl_add_u64 v[222:223], s[38:39], 0, v[206:207]
	s_mov_b32 m0, s27
	s_andn2_b64 vcc, exec, s[34:35]
	global_load_lds_dwordx4 v[222:223], off
	s_mov_b32 m0, s47
	s_nop 0
	global_load_lds_dwordx4 v[224:225], off
	s_waitcnt vmcnt(8)
	s_waitcnt lgkmcnt(0)
	s_barrier
	s_cbranch_vccnz .Lpk7_hz
	s_waitcnt lgkmcnt(0)
	v_mfma_f32_16x16x128_f8f6f4 v[130:133], v[18:25], v[58:65], 0
	v_mfma_f32_16x16x128_f8f6f4 v[126:129], v[26:33], v[58:65], 0
	v_mfma_f32_16x16x128_f8f6f4 v[110:113], v[18:25], v[50:57], 0
	v_mfma_f32_16x16x128_f8f6f4 v[114:117], v[26:33], v[50:57], 0
	v_mfma_f32_16x16x128_f8f6f4 v[98:101], v[18:25], v[42:49], 0
	v_mfma_f32_16x16x128_f8f6f4 v[90:93], v[26:33], v[42:49], 0
	v_mfma_f32_16x16x128_f8f6f4 v[78:81], v[18:25], v[34:41], 0
	v_mfma_f32_16x16x128_f8f6f4 v[82:85], v[26:33], v[34:41], 0
	v_mfma_f32_16x16x128_f8f6f4 v[122:125], v[2:9], v[58:65], 0
	v_mfma_f32_16x16x128_f8f6f4 v[118:121], v[10:17], v[58:65], 0
	v_mfma_f32_16x16x128_f8f6f4 v[102:105], v[2:9], v[50:57], 0
	v_mfma_f32_16x16x128_f8f6f4 v[106:109], v[10:17], v[50:57], 0
	v_mfma_f32_16x16x128_f8f6f4 v[94:97], v[2:9], v[42:49], 0
	v_mfma_f32_16x16x128_f8f6f4 v[86:89], v[10:17], v[42:49], 0
	v_mfma_f32_16x16x128_f8f6f4 v[70:73], v[2:9], v[34:41], 0
	v_mfma_f32_16x16x128_f8f6f4 v[74:77], v[10:17], v[34:41], 0
.Lpk7_1122:
	s_barrier
	s_add_i32 s64, 0, 0x18000
	s_add_i32 s65, 0, 0x1c000
	v_add_u32_e32 v2, s64, v228
	v_add_u32_e32 v14, s65, v228
	ds_read_b128 v[18:21], v2
	ds_read_b128 v[22:25], v2 offset:1024
	ds_read_b128 v[26:29], v2 offset:2048
	ds_read_b128 v[30:33], v2 offset:3072
	ds_read_b128 v[2:5], v14
	ds_read_b128 v[6:9], v14 offset:1024
	ds_read_b128 v[10:13], v14 offset:2048
	ds_read_b128 v[14:17], v14 offset:3072
	s_mov_b32 m0, s48
	v_lshl_add_u64 v[244:245], s[38:39], 0, v[210:211]
	s_waitcnt lgkmcnt(0)
	ds_read_b128 v[34:37], v241 offset:32768
	ds_read_b128 v[38:41], v241 offset:33792
	ds_read_b128 v[42:45], v241 offset:34816
	ds_read_b128 v[46:49], v241 offset:35840
	ds_read_b128 v[50:53], v241 offset:36864
	ds_read_b128 v[54:57], v241 offset:37888
	ds_read_b128 v[58:61], v241 offset:38912
	ds_read_b128 v[62:65], v241 offset:39936
	global_load_lds_dwordx4 v[244:245], off
	v_lshl_add_u64 v[244:245], s[38:39], 0, v[212:213]
	s_mov_b32 m0, s49
	s_nop 0
	global_load_lds_dwordx4 v[244:245], off
	s_waitcnt vmcnt(8)
	s_waitcnt lgkmcnt(0)
	s_barrier
	s_waitcnt lgkmcnt(0)
	v_mfma_f32_16x16x128_f8f6f4 v[194:197], v[18:25], v[34:41], v[194:197]
	v_mfma_f32_16x16x128_f8f6f4 v[190:193], v[26:33], v[34:41], v[190:193]
	v_mfma_f32_16x16x128_f8f6f4 v[174:177], v[18:25], v[42:49], v[174:177]
	v_mfma_f32_16x16x128_f8f6f4 v[182:185], v[26:33], v[42:49], v[182:185]
	v_mfma_f32_16x16x128_f8f6f4 v[166:169], v[18:25], v[50:57], v[166:169]
	v_mfma_f32_16x16x128_f8f6f4 v[158:161], v[26:33], v[50:57], v[158:161]
	v_mfma_f32_16x16x128_f8f6f4 v[142:145], v[18:25], v[58:65], v[142:145]
	v_mfma_f32_16x16x128_f8f6f4 v[150:153], v[26:33], v[58:65], v[150:153]
	v_mfma_f32_16x16x128_f8f6f4 v[186:189], v[2:9], v[34:41], v[186:189]
	v_mfma_f32_16x16x128_f8f6f4 v[178:181], v[10:17], v[34:41], v[178:181]
	v_mfma_f32_16x16x128_f8f6f4 v[162:165], v[2:9], v[42:49], v[162:165]
	v_mfma_f32_16x16x128_f8f6f4 v[170:173], v[10:17], v[42:49], v[170:173]
	v_mfma_f32_16x16x128_f8f6f4 v[154:157], v[2:9], v[50:57], v[154:157]
	v_mfma_f32_16x16x128_f8f6f4 v[146:149], v[10:17], v[50:57], v[146:149]
	v_mfma_f32_16x16x128_f8f6f4 v[138:141], v[2:9], v[58:65], v[138:141]
	v_mfma_f32_16x16x128_f8f6f4 v[134:137], v[10:17], v[58:65], v[134:137]
	s_barrier
	s_add_i32 s38, s64, s41
	v_lshl_add_u64 v[68:69], v[68:69], 0, s[10:11]
	s_mov_b32 m0, s38
	ds_read_b128 v[58:61], v241 offset:49152
	ds_read_b128 v[62:65], v241 offset:50176
	ds_read_b128 v[50:53], v241 offset:51200
	ds_read_b128 v[54:57], v241 offset:52224
	ds_read_b128 v[42:45], v241 offset:53248
	ds_read_b128 v[46:49], v241 offset:54272
	ds_read_b128 v[34:37], v241 offset:55296
	ds_read_b128 v[38:41], v241 offset:56320
	global_load_lds_dwordx4 v[68:69], off
	s_add_i32 m0, s38, 0x2000
	s_add_u32 s36, s36, 0x40080
	v_lshl_add_u64 v[68:69], v[220:221], 0, s[10:11]
	s_addc_u32 s37, s37, 0
	s_add_i32 s38, s65, s41
	global_load_lds_dwordx4 v[68:69], off
	v_lshl_add_u64 v[68:69], s[36:37], 0, v[202:203]
	s_mov_b32 m0, s38
	s_and_b64 vcc, exec, s[8:9]
	global_load_lds_dwordx4 v[68:69], off
	v_lshl_add_u64 v[68:69], s[36:37], 0, v[204:205]
	s_add_i32 m0, s38, 0x2000
	s_nop 0
	global_load_lds_dwordx4 v[68:69], off
	v_lshl_add_u64 v[68:69], v[222:223], 0, s[10:11]
	s_mov_b32 m0, s51
	s_nop 0
	global_load_lds_dwordx4 v[68:69], off
	v_lshl_add_u64 v[68:69], v[224:225], 0, s[10:11]
	s_mov_b32 m0, s52
	s_nop 0
	global_load_lds_dwordx4 v[68:69], off
	s_waitcnt vmcnt(8)
	s_waitcnt lgkmcnt(0)
	s_barrier
	s_cbranch_vccnz .LBB0_1119
	s_waitcnt lgkmcnt(0)
	v_mfma_f32_16x16x128_f8f6f4 v[130:133], v[18:25], v[58:65], v[130:133]
	v_mfma_f32_16x16x128_f8f6f4 v[126:129], v[26:33], v[58:65], v[126:129]
	v_mfma_f32_16x16x128_f8f6f4 v[110:113], v[18:25], v[50:57], v[110:113]
	v_mfma_f32_16x16x128_f8f6f4 v[114:117], v[26:33], v[50:57], v[114:117]
	v_mfma_f32_16x16x128_f8f6f4 v[98:101], v[18:25], v[42:49], v[98:101]
	v_mfma_f32_16x16x128_f8f6f4 v[90:93], v[26:33], v[42:49], v[90:93]
	v_mfma_f32_16x16x128_f8f6f4 v[78:81], v[18:25], v[34:41], v[78:81]
	v_mfma_f32_16x16x128_f8f6f4 v[82:85], v[26:33], v[34:41], v[82:85]
	v_mfma_f32_16x16x128_f8f6f4 v[122:125], v[2:9], v[58:65], v[122:125]
	v_mfma_f32_16x16x128_f8f6f4 v[118:121], v[10:17], v[58:65], v[118:121]
	v_mfma_f32_16x16x128_f8f6f4 v[102:105], v[2:9], v[50:57], v[102:105]
	v_mfma_f32_16x16x128_f8f6f4 v[106:109], v[10:17], v[50:57], v[106:109]
	v_mfma_f32_16x16x128_f8f6f4 v[94:97], v[2:9], v[42:49], v[94:97]
	v_mfma_f32_16x16x128_f8f6f4 v[86:89], v[10:17], v[42:49], v[86:89]
	v_mfma_f32_16x16x128_f8f6f4 v[70:73], v[2:9], v[34:41], v[70:73]
	v_mfma_f32_16x16x128_f8f6f4 v[74:77], v[10:17], v[34:41], v[74:77]
	s_branch .LBB0_1119

.LBB0_1120:
	ds_read_b128 v[18:21], v239
	ds_read_b128 v[22:25], v239 offset:1024
	ds_read_b128 v[26:29], v239 offset:2048
	ds_read_b128 v[30:33], v239 offset:3072
	ds_read_b128 v[2:5], v240
	ds_read_b128 v[6:9], v240 offset:1024
	ds_read_b128 v[10:13], v240 offset:2048
	ds_read_b128 v[14:17], v240 offset:3072
	s_mov_b64 s[8:9], s[28:29]
	s_add_u32 s28, s8, 0x100
	s_addc_u32 s29, s9, 0
	s_cmp_eq_u32 s63, 12
	s_cselect_b32 s39, s23, s29
	s_cselect_b32 s38, s22, s28
	s_cselect_b32 s37, s25, s21
	s_cselect_b32 s36, s24, s19
	v_lshl_add_u64 v[68:69], s[8:9], 0, v[216:217]
	s_add_i32 m0, s27, 0xc000
	s_waitcnt lgkmcnt(0)
	ds_read_b128 v[34:37], v241
	ds_read_b128 v[38:41], v241 offset:1024
	ds_read_b128 v[42:45], v241 offset:2048
	ds_read_b128 v[46:49], v241 offset:3072
	ds_read_b128 v[50:53], v241 offset:4096
	ds_read_b128 v[54:57], v241 offset:5120
	ds_read_b128 v[58:61], v241 offset:6144
	ds_read_b128 v[62:65], v241 offset:7168
	global_load_lds_dwordx4 v[68:69], off
	v_lshl_add_u64 v[68:69], s[8:9], 0, v[218:219]
	s_add_i32 m0, s27, 0xe000
	s_nop 0
	global_load_lds_dwordx4 v[68:69], off
	s_waitcnt vmcnt(8)
	s_waitcnt lgkmcnt(0)
	s_barrier
	s_waitcnt lgkmcnt(0)
	v_mfma_f32_16x16x128_f8f6f4 v[194:197], v[18:25], v[34:41], v[194:197]
	v_mfma_f32_16x16x128_f8f6f4 v[190:193], v[26:33], v[34:41], v[190:193]
	v_mfma_f32_16x16x128_f8f6f4 v[174:177], v[18:25], v[42:49], v[174:177]
	v_mfma_f32_16x16x128_f8f6f4 v[182:185], v[26:33], v[42:49], v[182:185]
	v_mfma_f32_16x16x128_f8f6f4 v[166:169], v[18:25], v[50:57], v[166:169]
	v_mfma_f32_16x16x128_f8f6f4 v[158:161], v[26:33], v[50:57], v[158:161]
	v_mfma_f32_16x16x128_f8f6f4 v[142:145], v[18:25], v[58:65], v[142:145]
	v_mfma_f32_16x16x128_f8f6f4 v[150:153], v[26:33], v[58:65], v[150:153]
	v_mfma_f32_16x16x128_f8f6f4 v[186:189], v[2:9], v[34:41], v[186:189]
	v_mfma_f32_16x16x128_f8f6f4 v[178:181], v[10:17], v[34:41], v[178:181]
	v_mfma_f32_16x16x128_f8f6f4 v[162:165], v[2:9], v[42:49], v[162:165]
	v_mfma_f32_16x16x128_f8f6f4 v[170:173], v[10:17], v[42:49], v[170:173]
	v_mfma_f32_16x16x128_f8f6f4 v[154:157], v[2:9], v[50:57], v[154:157]
	v_mfma_f32_16x16x128_f8f6f4 v[146:149], v[10:17], v[50:57], v[146:149]
	v_mfma_f32_16x16x128_f8f6f4 v[138:141], v[2:9], v[58:65], v[138:141]
	v_mfma_f32_16x16x128_f8f6f4 v[134:137], v[10:17], v[58:65], v[134:137]
	s_barrier
	s_add_i32 s8, s54, s41
	v_lshl_add_u64 v[68:69], s[36:37], 0, v[202:203]
	s_mov_b32 m0, s8
	ds_read_b128 v[58:61], v241 offset:16384
	ds_read_b128 v[62:65], v241 offset:17408
	ds_read_b128 v[50:53], v241 offset:18432
	ds_read_b128 v[54:57], v241 offset:19456
	ds_read_b128 v[42:45], v241 offset:20480
	ds_read_b128 v[46:49], v241 offset:21504
	ds_read_b128 v[34:37], v241 offset:22528
	ds_read_b128 v[38:41], v241 offset:23552
	global_load_lds_dwordx4 v[68:69], off
	s_add_i32 m0, s8, 0x2000
	s_add_u32 s8, s36, 0x40000
	v_lshl_add_u64 v[220:221], s[36:37], 0, v[204:205]
	s_addc_u32 s9, s37, 0
	s_add_i32 s64, s55, s41
	global_load_lds_dwordx4 v[220:221], off
	v_lshl_add_u64 v[222:223], s[8:9], 0, v[202:203]
	s_mov_b32 m0, s64
	v_lshl_add_u64 v[224:225], s[38:39], 0, v[208:209]
	global_load_lds_dwordx4 v[222:223], off
	v_lshl_add_u64 v[222:223], s[8:9], 0, v[204:205]
	s_add_i32 m0, s64, 0x2000
	v_cmp_ne_u32_e64 s[8:9], 1, v242
	global_load_lds_dwordx4 v[222:223], off
	v_lshl_add_u64 v[222:223], s[38:39], 0, v[206:207]
	s_mov_b32 m0, s27
	s_andn2_b64 vcc, exec, s[34:35]
	global_load_lds_dwordx4 v[222:223], off
	s_mov_b32 m0, s47
	s_nop 0
	global_load_lds_dwordx4 v[224:225], off
	s_waitcnt vmcnt(8)
	s_waitcnt lgkmcnt(0)
	s_barrier
	s_cbranch_vccnz .LBB0_1122
	s_waitcnt lgkmcnt(0)
	v_mfma_f32_16x16x128_f8f6f4 v[130:133], v[18:25], v[58:65], v[130:133]
	v_mfma_f32_16x16x128_f8f6f4 v[126:129], v[26:33], v[58:65], v[126:129]
	v_mfma_f32_16x16x128_f8f6f4 v[110:113], v[18:25], v[50:57], v[110:113]
	v_mfma_f32_16x16x128_f8f6f4 v[114:117], v[26:33], v[50:57], v[114:117]
	v_mfma_f32_16x16x128_f8f6f4 v[98:101], v[18:25], v[42:49], v[98:101]
	v_mfma_f32_16x16x128_f8f6f4 v[90:93], v[26:33], v[42:49], v[90:93]
	v_mfma_f32_16x16x128_f8f6f4 v[78:81], v[18:25], v[34:41], v[78:81]
	v_mfma_f32_16x16x128_f8f6f4 v[82:85], v[26:33], v[34:41], v[82:85]
	v_mfma_f32_16x16x128_f8f6f4 v[122:125], v[2:9], v[58:65], v[122:125]
	v_mfma_f32_16x16x128_f8f6f4 v[118:121], v[10:17], v[58:65], v[118:121]
	v_mfma_f32_16x16x128_f8f6f4 v[102:105], v[2:9], v[50:57], v[102:105]
	v_mfma_f32_16x16x128_f8f6f4 v[106:109], v[10:17], v[50:57], v[106:109]
	v_mfma_f32_16x16x128_f8f6f4 v[94:97], v[2:9], v[42:49], v[94:97]
	v_mfma_f32_16x16x128_f8f6f4 v[86:89], v[10:17], v[42:49], v[86:89]
	v_mfma_f32_16x16x128_f8f6f4 v[70:73], v[2:9], v[34:41], v[70:73]
	v_mfma_f32_16x16x128_f8f6f4 v[74:77], v[10:17], v[34:41], v[74:77]
